# v99 + hot loop heads (13 GEMM K-loops, 8 attention tile loops) aligned to 64 bytes with .p2align 6
# baseline (speedup 1.0000x reference)
.LBB0_187:
	s_ashr_i32 s47, s46, 31
	s_lshl_b64 s[38:39], s[46:47], 19
	s_add_u32 s50, s10, s38
	s_addc_u32 s51, s11, s39
	s_ashr_i32 s49, s48, 31
	s_lshl_b64 s[38:39], s[48:49], 19
	s_add_u32 s54, s6, s38
	v_mov_b32_e32 v3, 0
	s_addc_u32 s55, s7, s39
	s_andn2_b64 vcc, exec, s[42:43]
	v_mov_b32_e32 v2, v3
	v_mov_b32_e32 v1, v3
	v_mov_b32_e32 v0, v3
	v_mov_b32_e32 v7, v3
	v_mov_b32_e32 v6, v3
	v_mov_b32_e32 v5, v3
	v_mov_b32_e32 v4, v3
	v_mov_b32_e32 v19, v3
	v_mov_b32_e32 v18, v3
	v_mov_b32_e32 v17, v3
	v_mov_b32_e32 v16, v3
	v_mov_b32_e32 v23, v3
	v_mov_b32_e32 v22, v3
	v_mov_b32_e32 v21, v3
	v_mov_b32_e32 v20, v3
	v_mov_b32_e32 v127, v3
	v_mov_b32_e32 v126, v3
	v_mov_b32_e32 v125, v3
	v_mov_b32_e32 v124, v3
	v_mov_b32_e32 v123, v3
	v_mov_b32_e32 v122, v3
	v_mov_b32_e32 v121, v3
	v_mov_b32_e32 v120, v3
	v_mov_b32_e32 v111, v3
	v_mov_b32_e32 v110, v3
	v_mov_b32_e32 v109, v3
	v_mov_b32_e32 v108, v3
	v_mov_b32_e32 v107, v3
	v_mov_b32_e32 v106, v3
	v_mov_b32_e32 v105, v3
	v_mov_b32_e32 v104, v3
	v_mov_b32_e32 v95, v3
	v_mov_b32_e32 v94, v3
	v_mov_b32_e32 v93, v3
	v_mov_b32_e32 v92, v3
	v_mov_b32_e32 v91, v3
	v_mov_b32_e32 v90, v3
	v_mov_b32_e32 v89, v3
	v_mov_b32_e32 v88, v3
	v_mov_b32_e32 v79, v3
	v_mov_b32_e32 v78, v3
	v_mov_b32_e32 v77, v3
	v_mov_b32_e32 v76, v3
	v_mov_b32_e32 v75, v3
	v_mov_b32_e32 v74, v3
	v_mov_b32_e32 v73, v3
	v_mov_b32_e32 v72, v3
	v_mov_b32_e32 v119, v3
	v_mov_b32_e32 v118, v3
	v_mov_b32_e32 v117, v3
	v_mov_b32_e32 v116, v3
	v_mov_b32_e32 v115, v3
	v_mov_b32_e32 v114, v3
	v_mov_b32_e32 v113, v3
	v_mov_b32_e32 v112, v3
	v_mov_b32_e32 v103, v3
	v_mov_b32_e32 v102, v3
	v_mov_b32_e32 v101, v3
	v_mov_b32_e32 v100, v3
	v_mov_b32_e32 v99, v3
	v_mov_b32_e32 v98, v3
	v_mov_b32_e32 v97, v3
	v_mov_b32_e32 v96, v3
	v_mov_b32_e32 v87, v3
	v_mov_b32_e32 v86, v3
	v_mov_b32_e32 v85, v3
	v_mov_b32_e32 v84, v3
	v_mov_b32_e32 v83, v3
	v_mov_b32_e32 v82, v3
	v_mov_b32_e32 v81, v3
	v_mov_b32_e32 v80, v3
	v_mov_b32_e32 v71, v3
	v_mov_b32_e32 v70, v3
	v_mov_b32_e32 v69, v3
	v_mov_b32_e32 v68, v3
	v_mov_b32_e32 v67, v3
	v_mov_b32_e32 v66, v3
	v_mov_b32_e32 v65, v3
	v_mov_b32_e32 v64, v3
	v_mov_b32_e32 v63, v3
	v_mov_b32_e32 v62, v3
	v_mov_b32_e32 v61, v3
	v_mov_b32_e32 v60, v3
	v_mov_b32_e32 v59, v3
	v_mov_b32_e32 v58, v3
	v_mov_b32_e32 v57, v3
	v_mov_b32_e32 v56, v3
	v_mov_b32_e32 v47, v3
	v_mov_b32_e32 v46, v3
	v_mov_b32_e32 v45, v3
	v_mov_b32_e32 v44, v3
	v_mov_b32_e32 v43, v3
	v_mov_b32_e32 v42, v3
	v_mov_b32_e32 v41, v3
	v_mov_b32_e32 v40, v3
	v_mov_b32_e32 v31, v3
	v_mov_b32_e32 v30, v3
	v_mov_b32_e32 v29, v3
	v_mov_b32_e32 v28, v3
	v_mov_b32_e32 v27, v3
	v_mov_b32_e32 v26, v3
	v_mov_b32_e32 v25, v3
	v_mov_b32_e32 v24, v3
	v_mov_b32_e32 v15, v3
	v_mov_b32_e32 v14, v3
	v_mov_b32_e32 v13, v3
	v_mov_b32_e32 v12, v3
	v_mov_b32_e32 v11, v3
	v_mov_b32_e32 v10, v3
	v_mov_b32_e32 v9, v3
	v_mov_b32_e32 v8, v3
	v_mov_b32_e32 v55, v3
	v_mov_b32_e32 v54, v3
	v_mov_b32_e32 v53, v3
	v_mov_b32_e32 v52, v3
	v_mov_b32_e32 v51, v3
	v_mov_b32_e32 v50, v3
	v_mov_b32_e32 v49, v3
	v_mov_b32_e32 v48, v3
	v_mov_b32_e32 v39, v3
	v_mov_b32_e32 v38, v3
	v_mov_b32_e32 v37, v3
	v_mov_b32_e32 v36, v3
	v_mov_b32_e32 v35, v3
	v_mov_b32_e32 v34, v3
	v_mov_b32_e32 v33, v3
	v_mov_b32_e32 v32, v3
	s_cbranch_vccnz .LBB0_190
	s_and_b64 s[38:39], s[40:41], exec
	s_cselect_b32 s47, s51, s23
	s_cselect_b32 s49, s50, s22
	s_cselect_b32 s86, s55, s3
	s_cselect_b32 s87, s54, s2
	s_add_u32 s74, s22, 0x40080
	s_addc_u32 s75, s23, 0
	s_add_u32 s22, s2, 0x100
	v_mov_b32_e32 v32, 0
	s_addc_u32 s23, s3, 0
	s_mov_b32 s2, 0
	v_mov_b32_e32 v33, v32
	v_mov_b32_e32 v34, v32
	v_mov_b32_e32 v35, v32
	v_mov_b32_e32 v36, v32
	v_mov_b32_e32 v37, v32
	v_mov_b32_e32 v38, v32
	v_mov_b32_e32 v39, v32
	v_mov_b32_e32 v48, v32
	v_mov_b32_e32 v49, v32
	v_mov_b32_e32 v50, v32
	v_mov_b32_e32 v51, v32
	v_mov_b32_e32 v52, v32
	v_mov_b32_e32 v53, v32
	v_mov_b32_e32 v54, v32
	v_mov_b32_e32 v55, v32
	v_mov_b32_e32 v8, v32
	v_mov_b32_e32 v9, v32
	v_mov_b32_e32 v10, v32
	v_mov_b32_e32 v11, v32
	v_mov_b32_e32 v12, v32
	v_mov_b32_e32 v13, v32
	v_mov_b32_e32 v14, v32
	v_mov_b32_e32 v15, v32
	v_mov_b32_e32 v24, v32
	v_mov_b32_e32 v25, v32
	v_mov_b32_e32 v26, v32
	v_mov_b32_e32 v27, v32
	v_mov_b32_e32 v28, v32
	v_mov_b32_e32 v29, v32
	v_mov_b32_e32 v30, v32
	v_mov_b32_e32 v31, v32
	v_mov_b32_e32 v40, v32
	v_mov_b32_e32 v41, v32
	v_mov_b32_e32 v42, v32
	v_mov_b32_e32 v43, v32
	v_mov_b32_e32 v44, v32
	v_mov_b32_e32 v45, v32
	v_mov_b32_e32 v46, v32
	v_mov_b32_e32 v47, v32
	v_mov_b32_e32 v56, v32
	v_mov_b32_e32 v57, v32
	v_mov_b32_e32 v58, v32
	v_mov_b32_e32 v59, v32
	v_mov_b32_e32 v60, v32
	v_mov_b32_e32 v61, v32
	v_mov_b32_e32 v62, v32
	v_mov_b32_e32 v63, v32
	v_mov_b32_e32 v64, v32
	v_mov_b32_e32 v65, v32
	v_mov_b32_e32 v66, v32
	v_mov_b32_e32 v67, v32
	v_mov_b32_e32 v68, v32
	v_mov_b32_e32 v69, v32
	v_mov_b32_e32 v70, v32
	v_mov_b32_e32 v71, v32
	v_mov_b32_e32 v80, v32
	v_mov_b32_e32 v81, v32
	v_mov_b32_e32 v82, v32
	v_mov_b32_e32 v83, v32
	v_mov_b32_e32 v84, v32
	v_mov_b32_e32 v85, v32
	v_mov_b32_e32 v86, v32
	v_mov_b32_e32 v87, v32
	v_mov_b32_e32 v96, v32
	v_mov_b32_e32 v97, v32
	v_mov_b32_e32 v98, v32
	v_mov_b32_e32 v99, v32
	v_mov_b32_e32 v100, v32
	v_mov_b32_e32 v101, v32
	v_mov_b32_e32 v102, v32
	v_mov_b32_e32 v103, v32
	v_mov_b32_e32 v112, v32
	v_mov_b32_e32 v113, v32
	v_mov_b32_e32 v114, v32
	v_mov_b32_e32 v115, v32
	v_mov_b32_e32 v116, v32
	v_mov_b32_e32 v117, v32
	v_mov_b32_e32 v118, v32
	v_mov_b32_e32 v119, v32
	v_mov_b32_e32 v72, v32
	v_mov_b32_e32 v73, v32
	v_mov_b32_e32 v74, v32
	v_mov_b32_e32 v75, v32
	v_mov_b32_e32 v76, v32
	v_mov_b32_e32 v77, v32
	v_mov_b32_e32 v78, v32
	v_mov_b32_e32 v79, v32
	v_mov_b32_e32 v88, v32
	v_mov_b32_e32 v89, v32
	v_mov_b32_e32 v90, v32
	v_mov_b32_e32 v91, v32
	v_mov_b32_e32 v92, v32
	v_mov_b32_e32 v93, v32
	v_mov_b32_e32 v94, v32
	v_mov_b32_e32 v95, v32
	v_mov_b32_e32 v104, v32
	v_mov_b32_e32 v105, v32
	v_mov_b32_e32 v106, v32
	v_mov_b32_e32 v107, v32
	v_mov_b32_e32 v108, v32
	v_mov_b32_e32 v109, v32
	v_mov_b32_e32 v110, v32
	v_mov_b32_e32 v111, v32
	v_mov_b32_e32 v120, v32
	v_mov_b32_e32 v121, v32
	v_mov_b32_e32 v122, v32
	v_mov_b32_e32 v123, v32
	v_mov_b32_e32 v124, v32
	v_mov_b32_e32 v125, v32
	v_mov_b32_e32 v126, v32
	v_mov_b32_e32 v127, v32
	v_mov_b32_e32 v20, v32
	v_mov_b32_e32 v21, v32
	v_mov_b32_e32 v22, v32
	v_mov_b32_e32 v23, v32
	v_mov_b32_e32 v16, v32
	v_mov_b32_e32 v17, v32
	v_mov_b32_e32 v18, v32
	v_mov_b32_e32 v19, v32
	v_mov_b32_e32 v4, v32
	v_mov_b32_e32 v5, v32
	v_mov_b32_e32 v6, v32
	v_mov_b32_e32 v7, v32
	v_mov_b32_e32 v0, v32
	v_mov_b32_e32 v1, v32
	v_mov_b32_e32 v2, v32
	v_mov_b32_e32 v3, v32
	.p2align 6

.LBB0_204:
	s_ashr_i32 s43, s42, 31
	s_lshl_b64 s[38:39], s[42:43], 19
	s_add_u32 s46, s11, s38
	s_addc_u32 s47, s31, s39
	s_ashr_i32 s45, s44, 31
	s_lshl_b64 s[38:39], s[44:45], 19
	s_add_u32 s50, s6, s38
	v_mov_b32_e32 v3, 0
	s_addc_u32 s51, s7, s39
	s_andn2_b64 vcc, exec, s[36:37]
	v_mov_b32_e32 v2, v3
	v_mov_b32_e32 v1, v3
	v_mov_b32_e32 v0, v3
	v_mov_b32_e32 v7, v3
	v_mov_b32_e32 v6, v3
	v_mov_b32_e32 v5, v3
	v_mov_b32_e32 v4, v3
	v_mov_b32_e32 v19, v3
	v_mov_b32_e32 v18, v3
	v_mov_b32_e32 v17, v3
	v_mov_b32_e32 v16, v3
	v_mov_b32_e32 v23, v3
	v_mov_b32_e32 v22, v3
	v_mov_b32_e32 v21, v3
	v_mov_b32_e32 v20, v3
	v_mov_b32_e32 v127, v3
	v_mov_b32_e32 v126, v3
	v_mov_b32_e32 v125, v3
	v_mov_b32_e32 v124, v3
	v_mov_b32_e32 v123, v3
	v_mov_b32_e32 v122, v3
	v_mov_b32_e32 v121, v3
	v_mov_b32_e32 v120, v3
	v_mov_b32_e32 v111, v3
	v_mov_b32_e32 v110, v3
	v_mov_b32_e32 v109, v3
	v_mov_b32_e32 v108, v3
	v_mov_b32_e32 v107, v3
	v_mov_b32_e32 v106, v3
	v_mov_b32_e32 v105, v3
	v_mov_b32_e32 v104, v3
	v_mov_b32_e32 v95, v3
	v_mov_b32_e32 v94, v3
	v_mov_b32_e32 v93, v3
	v_mov_b32_e32 v92, v3
	v_mov_b32_e32 v91, v3
	v_mov_b32_e32 v90, v3
	v_mov_b32_e32 v89, v3
	v_mov_b32_e32 v88, v3
	v_mov_b32_e32 v79, v3
	v_mov_b32_e32 v78, v3
	v_mov_b32_e32 v77, v3
	v_mov_b32_e32 v76, v3
	v_mov_b32_e32 v75, v3
	v_mov_b32_e32 v74, v3
	v_mov_b32_e32 v73, v3
	v_mov_b32_e32 v72, v3
	v_mov_b32_e32 v119, v3
	v_mov_b32_e32 v118, v3
	v_mov_b32_e32 v117, v3
	v_mov_b32_e32 v116, v3
	v_mov_b32_e32 v115, v3
	v_mov_b32_e32 v114, v3
	v_mov_b32_e32 v113, v3
	v_mov_b32_e32 v112, v3
	v_mov_b32_e32 v103, v3
	v_mov_b32_e32 v102, v3
	v_mov_b32_e32 v101, v3
	v_mov_b32_e32 v100, v3
	v_mov_b32_e32 v99, v3
	v_mov_b32_e32 v98, v3
	v_mov_b32_e32 v97, v3
	v_mov_b32_e32 v96, v3
	v_mov_b32_e32 v87, v3
	v_mov_b32_e32 v86, v3
	v_mov_b32_e32 v85, v3
	v_mov_b32_e32 v84, v3
	v_mov_b32_e32 v83, v3
	v_mov_b32_e32 v82, v3
	v_mov_b32_e32 v81, v3
	v_mov_b32_e32 v80, v3
	v_mov_b32_e32 v71, v3
	v_mov_b32_e32 v70, v3
	v_mov_b32_e32 v69, v3
	v_mov_b32_e32 v68, v3
	v_mov_b32_e32 v67, v3
	v_mov_b32_e32 v66, v3
	v_mov_b32_e32 v65, v3
	v_mov_b32_e32 v64, v3
	v_mov_b32_e32 v63, v3
	v_mov_b32_e32 v62, v3
	v_mov_b32_e32 v61, v3
	v_mov_b32_e32 v60, v3
	v_mov_b32_e32 v59, v3
	v_mov_b32_e32 v58, v3
	v_mov_b32_e32 v57, v3
	v_mov_b32_e32 v56, v3
	v_mov_b32_e32 v47, v3
	v_mov_b32_e32 v46, v3
	v_mov_b32_e32 v45, v3
	v_mov_b32_e32 v44, v3
	v_mov_b32_e32 v43, v3
	v_mov_b32_e32 v42, v3
	v_mov_b32_e32 v41, v3
	v_mov_b32_e32 v40, v3
	v_mov_b32_e32 v31, v3
	v_mov_b32_e32 v30, v3
	v_mov_b32_e32 v29, v3
	v_mov_b32_e32 v28, v3
	v_mov_b32_e32 v27, v3
	v_mov_b32_e32 v26, v3
	v_mov_b32_e32 v25, v3
	v_mov_b32_e32 v24, v3
	v_mov_b32_e32 v15, v3
	v_mov_b32_e32 v14, v3
	v_mov_b32_e32 v13, v3
	v_mov_b32_e32 v12, v3
	v_mov_b32_e32 v11, v3
	v_mov_b32_e32 v10, v3
	v_mov_b32_e32 v9, v3
	v_mov_b32_e32 v8, v3
	v_mov_b32_e32 v55, v3
	v_mov_b32_e32 v54, v3
	v_mov_b32_e32 v53, v3
	v_mov_b32_e32 v52, v3
	v_mov_b32_e32 v51, v3
	v_mov_b32_e32 v50, v3
	v_mov_b32_e32 v49, v3
	v_mov_b32_e32 v48, v3
	v_mov_b32_e32 v39, v3
	v_mov_b32_e32 v38, v3
	v_mov_b32_e32 v37, v3
	v_mov_b32_e32 v36, v3
	v_mov_b32_e32 v35, v3
	v_mov_b32_e32 v34, v3
	v_mov_b32_e32 v33, v3
	v_mov_b32_e32 v32, v3
	s_cbranch_vccnz .LBB0_207
	s_and_b64 s[38:39], s[48:49], exec
	s_cselect_b32 s43, s47, s23
	s_cselect_b32 s45, s46, s22
	s_cselect_b32 s81, s51, s3
	s_cselect_b32 s83, s50, s2
	s_add_u32 s54, s22, 0x40080
	s_addc_u32 s55, s23, 0
	s_add_u32 s22, s2, 0x100
	v_mov_b32_e32 v32, 0
	s_addc_u32 s23, s3, 0
	s_mov_b32 s2, 0
	v_mov_b32_e32 v33, v32
	v_mov_b32_e32 v34, v32
	v_mov_b32_e32 v35, v32
	v_mov_b32_e32 v36, v32
	v_mov_b32_e32 v37, v32
	v_mov_b32_e32 v38, v32
	v_mov_b32_e32 v39, v32
	v_mov_b32_e32 v48, v32
	v_mov_b32_e32 v49, v32
	v_mov_b32_e32 v50, v32
	v_mov_b32_e32 v51, v32
	v_mov_b32_e32 v52, v32
	v_mov_b32_e32 v53, v32
	v_mov_b32_e32 v54, v32
	v_mov_b32_e32 v55, v32
	v_mov_b32_e32 v8, v32
	v_mov_b32_e32 v9, v32
	v_mov_b32_e32 v10, v32
	v_mov_b32_e32 v11, v32
	v_mov_b32_e32 v12, v32
	v_mov_b32_e32 v13, v32
	v_mov_b32_e32 v14, v32
	v_mov_b32_e32 v15, v32
	v_mov_b32_e32 v24, v32
	v_mov_b32_e32 v25, v32
	v_mov_b32_e32 v26, v32
	v_mov_b32_e32 v27, v32
	v_mov_b32_e32 v28, v32
	v_mov_b32_e32 v29, v32
	v_mov_b32_e32 v30, v32
	v_mov_b32_e32 v31, v32
	v_mov_b32_e32 v40, v32
	v_mov_b32_e32 v41, v32
	v_mov_b32_e32 v42, v32
	v_mov_b32_e32 v43, v32
	v_mov_b32_e32 v44, v32
	v_mov_b32_e32 v45, v32
	v_mov_b32_e32 v46, v32
	v_mov_b32_e32 v47, v32
	v_mov_b32_e32 v56, v32
	v_mov_b32_e32 v57, v32
	v_mov_b32_e32 v58, v32
	v_mov_b32_e32 v59, v32
	v_mov_b32_e32 v60, v32
	v_mov_b32_e32 v61, v32
	v_mov_b32_e32 v62, v32
	v_mov_b32_e32 v63, v32
	v_mov_b32_e32 v64, v32
	v_mov_b32_e32 v65, v32
	v_mov_b32_e32 v66, v32
	v_mov_b32_e32 v67, v32
	v_mov_b32_e32 v68, v32
	v_mov_b32_e32 v69, v32
	v_mov_b32_e32 v70, v32
	v_mov_b32_e32 v71, v32
	v_mov_b32_e32 v80, v32
	v_mov_b32_e32 v81, v32
	v_mov_b32_e32 v82, v32
	v_mov_b32_e32 v83, v32
	v_mov_b32_e32 v84, v32
	v_mov_b32_e32 v85, v32
	v_mov_b32_e32 v86, v32
	v_mov_b32_e32 v87, v32
	v_mov_b32_e32 v96, v32
	v_mov_b32_e32 v97, v32
	v_mov_b32_e32 v98, v32
	v_mov_b32_e32 v99, v32
	v_mov_b32_e32 v100, v32
	v_mov_b32_e32 v101, v32
	v_mov_b32_e32 v102, v32
	v_mov_b32_e32 v103, v32
	v_mov_b32_e32 v112, v32
	v_mov_b32_e32 v113, v32
	v_mov_b32_e32 v114, v32
	v_mov_b32_e32 v115, v32
	v_mov_b32_e32 v116, v32
	v_mov_b32_e32 v117, v32
	v_mov_b32_e32 v118, v32
	v_mov_b32_e32 v119, v32
	v_mov_b32_e32 v72, v32
	v_mov_b32_e32 v73, v32
	v_mov_b32_e32 v74, v32
	v_mov_b32_e32 v75, v32
	v_mov_b32_e32 v76, v32
	v_mov_b32_e32 v77, v32
	v_mov_b32_e32 v78, v32
	v_mov_b32_e32 v79, v32
	v_mov_b32_e32 v88, v32
	v_mov_b32_e32 v89, v32
	v_mov_b32_e32 v90, v32
	v_mov_b32_e32 v91, v32
	v_mov_b32_e32 v92, v32
	v_mov_b32_e32 v93, v32
	v_mov_b32_e32 v94, v32
	v_mov_b32_e32 v95, v32
	v_mov_b32_e32 v104, v32
	v_mov_b32_e32 v105, v32
	v_mov_b32_e32 v106, v32
	v_mov_b32_e32 v107, v32
	v_mov_b32_e32 v108, v32
	v_mov_b32_e32 v109, v32
	v_mov_b32_e32 v110, v32
	v_mov_b32_e32 v111, v32
	v_mov_b32_e32 v120, v32
	v_mov_b32_e32 v121, v32
	v_mov_b32_e32 v122, v32
	v_mov_b32_e32 v123, v32
	v_mov_b32_e32 v124, v32
	v_mov_b32_e32 v125, v32
	v_mov_b32_e32 v126, v32
	v_mov_b32_e32 v127, v32
	v_mov_b32_e32 v20, v32
	v_mov_b32_e32 v21, v32
	v_mov_b32_e32 v22, v32
	v_mov_b32_e32 v23, v32
	v_mov_b32_e32 v16, v32
	v_mov_b32_e32 v17, v32
	v_mov_b32_e32 v18, v32
	v_mov_b32_e32 v19, v32
	v_mov_b32_e32 v4, v32
	v_mov_b32_e32 v5, v32
	v_mov_b32_e32 v6, v32
	v_mov_b32_e32 v7, v32
	v_mov_b32_e32 v0, v32
	v_mov_b32_e32 v1, v32
	v_mov_b32_e32 v2, v32
	v_mov_b32_e32 v3, v32
	.p2align 6

.LBB0_337:
	s_ashr_i32 s34, s86, 31
	s_cmp_gt_i32 s86, 2
	s_cselect_b32 s35, s31, s10
	s_cselect_b32 s75, s33, s11
	s_add_i32 s38, s86, -3
	s_cmp_gt_i32 s86, 2
	s_cselect_b32 s74, 0x200, 0
	s_cselect_b32 s39, 0, s34
	s_cselect_b32 s38, s38, s86
	s_ashr_i32 s47, s46, 31
	s_lshl_b64 s[48:49], s[46:47], 18
	s_add_u32 s34, s6, s48
	s_addc_u32 s47, s7, s49
	s_add_u32 s48, s34, s74
	s_addc_u32 s49, s47, 0
	s_lshl_b64 s[38:39], s[38:39], 17
	s_add_u32 s74, s35, s38
	v_mov_b32_e32 v3, 0
	s_addc_u32 s75, s75, s39
	s_andn2_b64 vcc, exec, s[42:43]
	v_mov_b32_e32 v2, v3
	v_mov_b32_e32 v1, v3
	v_mov_b32_e32 v0, v3
	v_mov_b32_e32 v7, v3
	v_mov_b32_e32 v6, v3
	v_mov_b32_e32 v5, v3
	v_mov_b32_e32 v4, v3
	v_mov_b32_e32 v19, v3
	v_mov_b32_e32 v18, v3
	v_mov_b32_e32 v17, v3
	v_mov_b32_e32 v16, v3
	v_mov_b32_e32 v23, v3
	v_mov_b32_e32 v22, v3
	v_mov_b32_e32 v21, v3
	v_mov_b32_e32 v20, v3
	v_mov_b32_e32 v127, v3
	v_mov_b32_e32 v126, v3
	v_mov_b32_e32 v125, v3
	v_mov_b32_e32 v124, v3
	v_mov_b32_e32 v123, v3
	v_mov_b32_e32 v122, v3
	v_mov_b32_e32 v121, v3
	v_mov_b32_e32 v120, v3
	v_mov_b32_e32 v111, v3
	v_mov_b32_e32 v110, v3
	v_mov_b32_e32 v109, v3
	v_mov_b32_e32 v108, v3
	v_mov_b32_e32 v107, v3
	v_mov_b32_e32 v106, v3
	v_mov_b32_e32 v105, v3
	v_mov_b32_e32 v104, v3
	v_mov_b32_e32 v95, v3
	v_mov_b32_e32 v94, v3
	v_mov_b32_e32 v93, v3
	v_mov_b32_e32 v92, v3
	v_mov_b32_e32 v91, v3
	v_mov_b32_e32 v90, v3
	v_mov_b32_e32 v89, v3
	v_mov_b32_e32 v88, v3
	v_mov_b32_e32 v79, v3
	v_mov_b32_e32 v78, v3
	v_mov_b32_e32 v77, v3
	v_mov_b32_e32 v76, v3
	v_mov_b32_e32 v75, v3
	v_mov_b32_e32 v74, v3
	v_mov_b32_e32 v73, v3
	v_mov_b32_e32 v72, v3
	v_mov_b32_e32 v119, v3
	v_mov_b32_e32 v118, v3
	v_mov_b32_e32 v117, v3
	v_mov_b32_e32 v116, v3
	v_mov_b32_e32 v115, v3
	v_mov_b32_e32 v114, v3
	v_mov_b32_e32 v113, v3
	v_mov_b32_e32 v112, v3
	v_mov_b32_e32 v103, v3
	v_mov_b32_e32 v102, v3
	v_mov_b32_e32 v101, v3
	v_mov_b32_e32 v100, v3
	v_mov_b32_e32 v99, v3
	v_mov_b32_e32 v98, v3
	v_mov_b32_e32 v97, v3
	v_mov_b32_e32 v96, v3
	v_mov_b32_e32 v87, v3
	v_mov_b32_e32 v86, v3
	v_mov_b32_e32 v85, v3
	v_mov_b32_e32 v84, v3
	v_mov_b32_e32 v83, v3
	v_mov_b32_e32 v82, v3
	v_mov_b32_e32 v81, v3
	v_mov_b32_e32 v80, v3
	v_mov_b32_e32 v71, v3
	v_mov_b32_e32 v70, v3
	v_mov_b32_e32 v69, v3
	v_mov_b32_e32 v68, v3
	v_mov_b32_e32 v67, v3
	v_mov_b32_e32 v66, v3
	v_mov_b32_e32 v65, v3
	v_mov_b32_e32 v64, v3
	v_mov_b32_e32 v63, v3
	v_mov_b32_e32 v62, v3
	v_mov_b32_e32 v61, v3
	v_mov_b32_e32 v60, v3
	v_mov_b32_e32 v59, v3
	v_mov_b32_e32 v58, v3
	v_mov_b32_e32 v57, v3
	v_mov_b32_e32 v56, v3
	v_mov_b32_e32 v47, v3
	v_mov_b32_e32 v46, v3
	v_mov_b32_e32 v45, v3
	v_mov_b32_e32 v44, v3
	v_mov_b32_e32 v43, v3
	v_mov_b32_e32 v42, v3
	v_mov_b32_e32 v41, v3
	v_mov_b32_e32 v40, v3
	v_mov_b32_e32 v31, v3
	v_mov_b32_e32 v30, v3
	v_mov_b32_e32 v29, v3
	v_mov_b32_e32 v28, v3
	v_mov_b32_e32 v27, v3
	v_mov_b32_e32 v26, v3
	v_mov_b32_e32 v25, v3
	v_mov_b32_e32 v24, v3
	v_mov_b32_e32 v15, v3
	v_mov_b32_e32 v14, v3
	v_mov_b32_e32 v13, v3
	v_mov_b32_e32 v12, v3
	v_mov_b32_e32 v11, v3
	v_mov_b32_e32 v10, v3
	v_mov_b32_e32 v9, v3
	v_mov_b32_e32 v8, v3
	v_mov_b32_e32 v55, v3
	v_mov_b32_e32 v54, v3
	v_mov_b32_e32 v53, v3
	v_mov_b32_e32 v52, v3
	v_mov_b32_e32 v51, v3
	v_mov_b32_e32 v50, v3
	v_mov_b32_e32 v49, v3
	v_mov_b32_e32 v48, v3
	v_mov_b32_e32 v39, v3
	v_mov_b32_e32 v38, v3
	v_mov_b32_e32 v37, v3
	v_mov_b32_e32 v36, v3
	v_mov_b32_e32 v35, v3
	v_mov_b32_e32 v34, v3
	v_mov_b32_e32 v33, v3
	v_mov_b32_e32 v32, v3
	s_cbranch_vccnz .LBB0_340
	s_and_b64 s[38:39], s[40:41], exec
	s_cselect_b32 s47, s49, s23
	s_cselect_b32 s93, s48, s22
	s_cselect_b32 s95, s75, s3
	s_cselect_b32 vcc_lo, s74, s2
	s_add_u32 vcc_hi, s2, 0x100
	s_addc_u32 s38, s3, 0
	s_add_u32 s90, s22, 0x20080
	v_mov_b32_e32 v32, 0
	s_addc_u32 s91, s23, 0
	s_mov_b32 s2, 0
	v_mov_b32_e32 v33, v32
	v_mov_b32_e32 v34, v32
	v_mov_b32_e32 v35, v32
	v_mov_b32_e32 v36, v32
	v_mov_b32_e32 v37, v32
	v_mov_b32_e32 v38, v32
	v_mov_b32_e32 v39, v32
	v_mov_b32_e32 v48, v32
	v_mov_b32_e32 v49, v32
	v_mov_b32_e32 v50, v32
	v_mov_b32_e32 v51, v32
	v_mov_b32_e32 v52, v32
	v_mov_b32_e32 v53, v32
	v_mov_b32_e32 v54, v32
	v_mov_b32_e32 v55, v32
	v_mov_b32_e32 v8, v32
	v_mov_b32_e32 v9, v32
	v_mov_b32_e32 v10, v32
	v_mov_b32_e32 v11, v32
	v_mov_b32_e32 v12, v32
	v_mov_b32_e32 v13, v32
	v_mov_b32_e32 v14, v32
	v_mov_b32_e32 v15, v32
	v_mov_b32_e32 v24, v32
	v_mov_b32_e32 v25, v32
	v_mov_b32_e32 v26, v32
	v_mov_b32_e32 v27, v32
	v_mov_b32_e32 v28, v32
	v_mov_b32_e32 v29, v32
	v_mov_b32_e32 v30, v32
	v_mov_b32_e32 v31, v32
	v_mov_b32_e32 v40, v32
	v_mov_b32_e32 v41, v32
	v_mov_b32_e32 v42, v32
	v_mov_b32_e32 v43, v32
	v_mov_b32_e32 v44, v32
	v_mov_b32_e32 v45, v32
	v_mov_b32_e32 v46, v32
	v_mov_b32_e32 v47, v32
	v_mov_b32_e32 v56, v32
	v_mov_b32_e32 v57, v32
	v_mov_b32_e32 v58, v32
	v_mov_b32_e32 v59, v32
	v_mov_b32_e32 v60, v32
	v_mov_b32_e32 v61, v32
	v_mov_b32_e32 v62, v32
	v_mov_b32_e32 v63, v32
	v_mov_b32_e32 v64, v32
	v_mov_b32_e32 v65, v32
	v_mov_b32_e32 v66, v32
	v_mov_b32_e32 v67, v32
	v_mov_b32_e32 v68, v32
	v_mov_b32_e32 v69, v32
	v_mov_b32_e32 v70, v32
	v_mov_b32_e32 v71, v32
	v_mov_b32_e32 v80, v32
	v_mov_b32_e32 v81, v32
	v_mov_b32_e32 v82, v32
	v_mov_b32_e32 v83, v32
	v_mov_b32_e32 v84, v32
	v_mov_b32_e32 v85, v32
	v_mov_b32_e32 v86, v32
	v_mov_b32_e32 v87, v32
	v_mov_b32_e32 v96, v32
	v_mov_b32_e32 v97, v32
	v_mov_b32_e32 v98, v32
	v_mov_b32_e32 v99, v32
	v_mov_b32_e32 v100, v32
	v_mov_b32_e32 v101, v32
	v_mov_b32_e32 v102, v32
	v_mov_b32_e32 v103, v32
	v_mov_b32_e32 v112, v32
	v_mov_b32_e32 v113, v32
	v_mov_b32_e32 v114, v32
	v_mov_b32_e32 v115, v32
	v_mov_b32_e32 v116, v32
	v_mov_b32_e32 v117, v32
	v_mov_b32_e32 v118, v32
	v_mov_b32_e32 v119, v32
	v_mov_b32_e32 v72, v32
	v_mov_b32_e32 v73, v32
	v_mov_b32_e32 v74, v32
	v_mov_b32_e32 v75, v32
	v_mov_b32_e32 v76, v32
	v_mov_b32_e32 v77, v32
	v_mov_b32_e32 v78, v32
	v_mov_b32_e32 v79, v32
	v_mov_b32_e32 v88, v32
	v_mov_b32_e32 v89, v32
	v_mov_b32_e32 v90, v32
	v_mov_b32_e32 v91, v32
	v_mov_b32_e32 v92, v32
	v_mov_b32_e32 v93, v32
	v_mov_b32_e32 v94, v32
	v_mov_b32_e32 v95, v32
	v_mov_b32_e32 v104, v32
	v_mov_b32_e32 v105, v32
	v_mov_b32_e32 v106, v32
	v_mov_b32_e32 v107, v32
	v_mov_b32_e32 v108, v32
	v_mov_b32_e32 v109, v32
	v_mov_b32_e32 v110, v32
	v_mov_b32_e32 v111, v32
	v_mov_b32_e32 v120, v32
	v_mov_b32_e32 v121, v32
	v_mov_b32_e32 v122, v32
	v_mov_b32_e32 v123, v32
	v_mov_b32_e32 v124, v32
	v_mov_b32_e32 v125, v32
	v_mov_b32_e32 v126, v32
	v_mov_b32_e32 v127, v32
	v_mov_b32_e32 v20, v32
	v_mov_b32_e32 v21, v32
	v_mov_b32_e32 v22, v32
	v_mov_b32_e32 v23, v32
	v_mov_b32_e32 v16, v32
	v_mov_b32_e32 v17, v32
	v_mov_b32_e32 v18, v32
	v_mov_b32_e32 v19, v32
	v_mov_b32_e32 v4, v32
	v_mov_b32_e32 v5, v32
	v_mov_b32_e32 v6, v32
	v_mov_b32_e32 v7, v32
	v_mov_b32_e32 v0, v32
	v_mov_b32_e32 v1, v32
	v_mov_b32_e32 v2, v32
	v_mov_b32_e32 v3, v32
	s_mov_b64 s[4:5], 0x18000
	s_mov_b64 s[64:65], 0x8000
	s_mov_b64 s[12:13], 0x8080
	s_mov_b64 s[88:89], 0x18080
	.p2align 6

.LBB0_494:
	s_lshl_b32 s2, s81, 1
	s_and_b32 s87, s2, 0x300
	v_readlane_b32 s2, v254, 51
	v_mov_b32_e32 v191, v161
	v_mov_b32_e32 v17, v161
	v_mov_b32_e32 v0, s2
	v_readlane_b32 s2, v254, 52
	ds_read_b32 v0, v0
	s_waitcnt lgkmcnt(0)
	v_readfirstlane_b32 s6, v0
	v_mov_b32_e32 v1, s2
	ds_read_b32 v1, v1
	s_ashr_i32 s2, s86, 5
	s_ashr_i32 s3, s2, 31
	s_lshl_b64 s[18:19], s[2:3], 11
	s_waitcnt lgkmcnt(0)
	v_readfirstlane_b32 s7, v1
	s_add_u32 s92, s6, s54
	s_addc_u32 s93, s7, s55
	s_lshl_b32 s3, s86, 8
	s_and_b32 s10, s3, 0x700
	s_or_b32 s18, s18, s10
	s_mul_i32 s3, s19, 0x1a00
	s_mul_hi_u32 s6, s18, 0x1a00
	s_add_i32 s6, s6, s3
	s_mul_i32 s3, s18, 0x1a00
	s_add_u32 s3, s83, s3
	s_addc_u32 s6, s95, s6
	s_lshl_b32 s7, s86, 4
	s_and_b32 s7, s7, 0x180
	s_lshl_b32 s11, s7, 1
	s_add_u32 s34, s3, s11
	v_readlane_b32 s3, v253, 20
	v_mbcnt_lo_u32_b32 v99, -1, 0
	v_mbcnt_hi_u32_b32 v99, -1, v99
	s_addc_u32 s35, s6, 0
	v_and_b32_e32 v202, 31, v99
	v_add_u32_e32 v205, s3, v99
	v_bfe_u32 v204, v205, 6, 3
	v_lshl_or_b32 v16, v204, 5, v202
	v_mul_u32_u24_e32 v0, 0xd00, v16
	v_bfe_u32 v203, v99, 5, 1
	v_lshlrev_b32_e32 v160, 1, v0
	v_lshl_add_u64 v[0:1], s[34:35], 0, v[160:161]
	v_lshlrev_b32_e32 v190, 4, v203
	v_lshl_add_u64 v[12:13], v[0:1], 0, v[190:191]
	global_load_dwordx4 v[0:3], v[12:13], off offset:32
	global_load_dwordx4 v[4:7], v[12:13], off offset:96
	global_load_dwordx4 v[8:11], v[12:13], off
	s_nop 0
	global_load_dwordx4 v[12:15], v[12:13], off offset:64
	v_or_b32_e32 v16, s10, v16
	v_lshlrev_b32_e32 v16, 7, v16
	v_lshl_add_u64 v[48:49], s[44:45], 0, v[16:17]
	v_lshl_add_u64 v[50:51], s[46:47], 0, v[16:17]
	v_and_b32_e32 v160, 32, v99
	global_load_dwordx4 v[16:19], v160, s[92:93]
	global_load_dwordx4 v[20:23], v160, s[92:93] offset:16
	global_load_dwordx4 v[24:27], v160, s[92:93] offset:64
	global_load_dwordx4 v[28:31], v160, s[92:93] offset:80
	global_load_dwordx4 v[32:35], v160, s[92:93] offset:128
	global_load_dwordx4 v[36:39], v160, s[92:93] offset:144
	global_load_dwordx4 v[40:43], v160, s[92:93] offset:192
	global_load_dwordx4 v[44:47], v160, s[92:93] offset:208
	v_lshl_add_u64 v[68:69], v[48:49], 0, v[160:161]
	v_lshl_add_u64 v[76:77], v[50:51], 0, v[160:161]
	global_load_dwordx4 v[48:51], v[68:69], off
	global_load_dwordx4 v[52:55], v[68:69], off offset:16
	global_load_dwordx4 v[56:59], v[76:77], off
	global_load_dwordx4 v[60:63], v[76:77], off offset:16
	global_load_dwordx4 v[64:67], v[68:69], off offset:64
	s_nop 0
	global_load_dwordx4 v[68:71], v[68:69], off offset:80
	s_nop 0
	global_load_dwordx4 v[72:75], v[76:77], off offset:64
	s_nop 0
	global_load_dwordx4 v[76:79], v[76:77], off offset:80
	s_mul_i32 s7, s2, 0xd00000
	s_mul_hi_i32 s6, s2, 0xd00000
	s_add_u32 s2, s83, s7
	s_addc_u32 s3, s95, s6
	s_add_u32 s90, s2, s11
	s_addc_u32 s91, s3, 0
	v_and_b32_e32 v191, 63, v99
	s_waitcnt vmcnt(19)
	v_lshlrev_b32_e32 v80, 16, v3
	v_and_b32_e32 v81, 0xffff0000, v3
	s_waitcnt vmcnt(17)
	v_and_b32_e32 v97, 0xffff0000, v8
	v_lshlrev_b32_e32 v82, 16, v7
	v_and_b32_e32 v83, 0xffff0000, v7
	v_lshlrev_b32_e32 v84, 16, v2
	v_and_b32_e32 v85, 0xffff0000, v2
	v_lshlrev_b32_e32 v2, 16, v6
	v_and_b32_e32 v3, 0xffff0000, v6
	v_lshlrev_b32_e32 v6, 16, v1
	v_and_b32_e32 v7, 0xffff0000, v1
	v_lshlrev_b32_e32 v86, 16, v5
	v_and_b32_e32 v87, 0xffff0000, v5
	v_lshlrev_b32_e32 v88, 16, v0
	v_and_b32_e32 v89, 0xffff0000, v0
	v_lshlrev_b32_e32 v0, 16, v4
	v_and_b32_e32 v1, 0xffff0000, v4
	v_lshlrev_b32_e32 v4, 16, v11
	v_and_b32_e32 v5, 0xffff0000, v11
	s_waitcnt vmcnt(16)
	v_lshlrev_b32_e32 v90, 16, v15
	v_and_b32_e32 v91, 0xffff0000, v15
	v_lshlrev_b32_e32 v92, 16, v10
	v_and_b32_e32 v93, 0xffff0000, v10
	v_lshlrev_b32_e32 v10, 16, v14
	v_and_b32_e32 v11, 0xffff0000, v14
	v_lshlrev_b32_e32 v14, 16, v9
	v_and_b32_e32 v15, 0xffff0000, v9
	v_lshlrev_b32_e32 v96, 16, v8
	v_lshlrev_b32_e32 v8, 16, v12
	v_and_b32_e32 v9, 0xffff0000, v12
	v_mul_f32_e32 v12, v97, v97
	v_lshlrev_b32_e32 v94, 16, v13
	v_and_b32_e32 v95, 0xffff0000, v13
	v_pk_fma_f32 v[12:13], v[96:97], v[96:97], v[12:13] op_sel_hi:[1,1,0]
	v_mul_f32_e32 v98, v15, v15
	v_pk_fma_f32 v[12:13], v[14:15], v[14:15], v[12:13]
	s_nop 0
	v_pk_add_f32 v[12:13], v[98:99], v[12:13] op_sel_hi:[0,1]
	v_pk_fma_f32 v[12:13], v[92:93], v[92:93], v[12:13]
	v_mul_f32_e32 v98, v93, v93
	v_pk_add_f32 v[12:13], v[98:99], v[12:13] op_sel_hi:[0,1]
	v_pk_fma_f32 v[12:13], v[4:5], v[4:5], v[12:13]
	v_mul_f32_e32 v98, v5, v5
	v_pk_add_f32 v[12:13], v[98:99], v[12:13] op_sel_hi:[0,1]
	v_pk_fma_f32 v[12:13], v[88:89], v[88:89], v[12:13]
	v_mul_f32_e32 v98, v89, v89
	v_pk_add_f32 v[12:13], v[98:99], v[12:13] op_sel_hi:[0,1]
	v_pk_fma_f32 v[12:13], v[6:7], v[6:7], v[12:13]
	v_mul_f32_e32 v98, v7, v7
	v_pk_add_f32 v[12:13], v[98:99], v[12:13] op_sel_hi:[0,1]
	v_pk_fma_f32 v[12:13], v[84:85], v[84:85], v[12:13]
	v_mul_f32_e32 v98, v85, v85
	v_pk_add_f32 v[12:13], v[98:99], v[12:13] op_sel_hi:[0,1]
	v_pk_fma_f32 v[12:13], v[80:81], v[80:81], v[12:13]
	v_mul_f32_e32 v98, v81, v81
	v_pk_add_f32 v[12:13], v[98:99], v[12:13] op_sel_hi:[0,1]
	v_pk_fma_f32 v[12:13], v[8:9], v[8:9], v[12:13]
	v_mul_f32_e32 v98, v9, v9
	v_pk_add_f32 v[12:13], v[98:99], v[12:13] op_sel_hi:[0,1]
	v_pk_fma_f32 v[12:13], v[94:95], v[94:95], v[12:13]
	v_mul_f32_e32 v98, v95, v95
	v_pk_add_f32 v[12:13], v[98:99], v[12:13] op_sel_hi:[0,1]
	v_pk_fma_f32 v[12:13], v[10:11], v[10:11], v[12:13]
	v_mul_f32_e32 v98, v11, v11
	v_pk_add_f32 v[12:13], v[98:99], v[12:13] op_sel_hi:[0,1]
	v_pk_fma_f32 v[12:13], v[90:91], v[90:91], v[12:13]
	v_mul_f32_e32 v98, v91, v91
	v_pk_add_f32 v[12:13], v[98:99], v[12:13] op_sel_hi:[0,1]
	v_pk_fma_f32 v[12:13], v[0:1], v[0:1], v[12:13]
	v_mul_f32_e32 v98, v1, v1
	v_pk_add_f32 v[12:13], v[98:99], v[12:13] op_sel_hi:[0,1]
	v_pk_fma_f32 v[12:13], v[86:87], v[86:87], v[12:13]
	v_mul_f32_e32 v98, v87, v87
	v_pk_add_f32 v[12:13], v[98:99], v[12:13] op_sel_hi:[0,1]
	v_pk_fma_f32 v[12:13], v[2:3], v[2:3], v[12:13]
	v_mul_f32_e32 v98, v3, v3
	v_pk_add_f32 v[12:13], v[98:99], v[12:13] op_sel_hi:[0,1]
	v_pk_fma_f32 v[12:13], v[82:83], v[82:83], v[12:13]
	v_mul_f32_e32 v98, v83, v83
	v_pk_add_f32 v[12:13], v[98:99], v[12:13] op_sel_hi:[0,1]
	v_mov_b32_e32 v13, v12
	s_nop 1
	v_permlane32_swap_b32_e32 v12, v13
	v_add_f32_e32 v12, v12, v13
	v_fmamk_f32 v12, v12, 0x3c800000, v240
	v_rsq_f32_e32 v12, v12
	s_waitcnt vmcnt(13)
	v_pk_mul_f32 v[24:25], v[24:25], v[12:13] op_sel_hi:[1,0]
	s_nop 0
	v_pk_mul_f32 v[24:25], v[24:25], v[88:89]
	s_waitcnt vmcnt(9)
	v_pk_mul_f32 v[40:41], v[12:13], v[40:41] op_sel_hi:[0,1]
	v_pk_mul_f32 v[0:1], v[40:41], v[0:1]
	s_waitcnt vmcnt(1)
	v_pk_mul_f32 v[40:41], v[24:25], v[72:73]
	v_pk_mul_f32 v[26:27], v[26:27], v[12:13] op_sel_hi:[1,0]
	v_pk_fma_f32 v[40:41], v[0:1], v[64:65], v[40:41]
	v_pk_mul_f32 v[0:1], v[0:1], v[72:73]
	v_pk_mul_f32 v[6:7], v[26:27], v[6:7]
	v_pk_mul_f32 v[26:27], v[12:13], v[42:43] op_sel_hi:[0,1]
	v_pk_fma_f32 v[0:1], v[24:25], v[64:65], v[0:1] neg_lo:[0,0,1] neg_hi:[0,0,1]
	v_pk_mul_f32 v[26:27], v[26:27], v[86:87]
	v_pk_mul_f32 v[0:1], v[0:1], s[62:63] op_sel_hi:[1,0]
	v_pk_mul_f32 v[44:45], v[12:13], v[44:45] op_sel_hi:[0,1]
	v_cvt_pk_bf16_f32 v166, v0, v1
	v_pk_mul_f32 v[0:1], v[26:27], v[74:75]
	v_pk_mul_f32 v[28:29], v[28:29], v[12:13] op_sel_hi:[1,0]
	v_pk_fma_f32 v[0:1], v[6:7], v[66:67], v[0:1] neg_lo:[0,0,1] neg_hi:[0,0,1]
	v_pk_mul_f32 v[2:3], v[44:45], v[2:3]
	v_pk_mul_f32 v[22:23], v[22:23], v[12:13] op_sel_hi:[1,0]
	v_pk_mul_f32 v[18:19], v[18:19], v[12:13] op_sel_hi:[1,0]
	v_pk_mul_f32 v[16:17], v[16:17], v[12:13] op_sel_hi:[1,0]
	v_pk_mul_f32 v[0:1], v[0:1], s[62:63] op_sel_hi:[1,0]
	v_pk_mul_f32 v[30:31], v[30:31], v[12:13] op_sel_hi:[1,0]
	v_pk_mul_f32 v[46:47], v[12:13], v[46:47] op_sel_hi:[0,1]
	v_pk_mul_f32 v[28:29], v[28:29], v[84:85]
	v_pk_mul_f32 v[4:5], v[22:23], v[4:5]
	v_pk_mul_f32 v[22:23], v[12:13], v[38:39] op_sel_hi:[0,1]
	v_pk_mul_f32 v[20:21], v[20:21], v[12:13] op_sel_hi:[1,0]
	v_pk_mul_f32 v[36:37], v[12:13], v[36:37] op_sel_hi:[0,1]
	v_pk_mul_f32 v[14:15], v[18:19], v[14:15]
	v_pk_mul_f32 v[18:19], v[12:13], v[34:35] op_sel_hi:[0,1]
	v_pk_mul_f32 v[16:17], v[16:17], v[96:97]
	v_pk_mul_f32 v[12:13], v[12:13], v[32:33] op_sel_hi:[0,1]
	v_cvt_pk_bf16_f32 v167, v0, v1
	s_waitcnt vmcnt(0)
	v_pk_mul_f32 v[0:1], v[2:3], v[76:77]
	v_pk_mul_f32 v[8:9], v[12:13], v[8:9]
	v_pk_mul_f32 v[12:13], v[16:17], v[56:57]
	v_pk_fma_f32 v[0:1], v[28:29], v[68:69], v[0:1] neg_lo:[0,0,1] neg_hi:[0,0,1]
	v_pk_mul_f32 v[46:47], v[46:47], v[82:83]
	v_pk_fma_f32 v[12:13], v[8:9], v[48:49], v[12:13]
	v_pk_mul_f32 v[8:9], v[8:9], v[56:57]
	v_pk_mul_f32 v[0:1], v[0:1], s[62:63] op_sel_hi:[1,0]
	v_pk_mul_f32 v[30:31], v[30:31], v[80:81]
	v_pk_fma_f32 v[8:9], v[16:17], v[48:49], v[8:9] neg_lo:[0,0,1] neg_hi:[0,0,1]
	v_cvt_pk_bf16_f32 v168, v0, v1
	v_pk_mul_f32 v[0:1], v[46:47], v[78:79]
	v_pk_mul_f32 v[18:19], v[18:19], v[94:95]
	v_pk_mul_f32 v[8:9], v[8:9], s[62:63] op_sel_hi:[1,0]
	v_pk_fma_f32 v[0:1], v[30:31], v[70:71], v[0:1] neg_lo:[0,0,1] neg_hi:[0,0,1]
	v_pk_mul_f32 v[20:21], v[20:21], v[92:93]
	v_pk_mul_f32 v[34:35], v[14:15], v[58:59]
	v_cvt_pk_bf16_f32 v162, v8, v9
	v_pk_mul_f32 v[8:9], v[18:19], v[58:59]
	v_pk_mul_f32 v[0:1], v[0:1], s[62:63] op_sel_hi:[1,0]
	v_pk_mul_f32 v[10:11], v[36:37], v[10:11]
	v_pk_mul_f32 v[36:37], v[20:21], v[60:61]
	v_pk_fma_f32 v[34:35], v[18:19], v[50:51], v[34:35]
	v_pk_fma_f32 v[8:9], v[14:15], v[50:51], v[8:9] neg_lo:[0,0,1] neg_hi:[0,0,1]
	v_cvt_pk_bf16_f32 v169, v0, v1
	v_pk_mul_f32 v[0:1], v[12:13], s[62:63] op_sel_hi:[1,0]
	v_pk_mul_f32 v[22:23], v[22:23], v[90:91]
	v_pk_mul_f32 v[38:39], v[4:5], v[62:63]
	v_pk_fma_f32 v[36:37], v[10:11], v[52:53], v[36:37]
	v_pk_mul_f32 v[8:9], v[8:9], s[62:63] op_sel_hi:[1,0]
	v_cvt_pk_bf16_f32 v170, v0, v1
	v_pk_mul_f32 v[0:1], v[34:35], s[62:63] op_sel_hi:[1,0]
	v_pk_fma_f32 v[38:39], v[22:23], v[54:55], v[38:39]
	v_cvt_pk_bf16_f32 v163, v8, v9
	v_pk_mul_f32 v[8:9], v[10:11], v[60:61]
	v_cvt_pk_bf16_f32 v171, v0, v1
	v_pk_mul_f32 v[0:1], v[36:37], s[62:63] op_sel_hi:[1,0]
	v_pk_mul_f32 v[42:43], v[6:7], v[74:75]
	v_pk_fma_f32 v[8:9], v[20:21], v[52:53], v[8:9] neg_lo:[0,0,1] neg_hi:[0,0,1]
	v_cvt_pk_bf16_f32 v172, v0, v1
	v_pk_mul_f32 v[0:1], v[38:39], s[62:63] op_sel_hi:[1,0]
	v_pk_mul_f32 v[44:45], v[28:29], v[76:77]
	v_pk_fma_f32 v[42:43], v[26:27], v[66:67], v[42:43]
	v_pk_mul_f32 v[8:9], v[8:9], s[62:63] op_sel_hi:[1,0]
	v_cvt_pk_bf16_f32 v173, v0, v1
	v_pk_mul_f32 v[0:1], v[40:41], s[62:63] op_sel_hi:[1,0]
	v_pk_fma_f32 v[44:45], v[2:3], v[68:69], v[44:45]
	v_pk_mul_f32 v[32:33], v[30:31], v[78:79]
	v_cvt_pk_bf16_f32 v164, v8, v9
	v_pk_mul_f32 v[8:9], v[22:23], v[62:63]
	v_cvt_pk_bf16_f32 v174, v0, v1
	v_pk_mul_f32 v[0:1], v[42:43], s[62:63] op_sel_hi:[1,0]
	v_pk_fma_f32 v[32:33], v[46:47], v[70:71], v[32:33]
	v_pk_fma_f32 v[4:5], v[4:5], v[54:55], v[8:9] neg_lo:[0,0,1] neg_hi:[0,0,1]
	v_cvt_pk_bf16_f32 v175, v0, v1
	v_pk_mul_f32 v[0:1], v[44:45], s[62:63] op_sel_hi:[1,0]
	v_pk_mul_f32 v[4:5], v[4:5], s[62:63] op_sel_hi:[1,0]
	v_cvt_pk_bf16_f32 v176, v0, v1
	v_pk_mul_f32 v[0:1], v[32:33], s[62:63] op_sel_hi:[1,0]
	v_cvt_pk_bf16_f32 v165, v4, v5
	v_cvt_pk_bf16_f32 v177, v0, v1
	v_bfe_u32 v12, v205, 3, 6
	v_lshlrev_b32_e32 v13, 3, v99
	v_and_b32_e32 v14, 56, v13
	v_mul_u32_u24_e32 v0, 0xd00, v12
	v_bfe_u32 v15, v205, 4, 5
	v_or_b32_e32 v0, v0, v14
	v_and_b32_e32 v1, 0x78, v13
	v_mul_u32_u24_e32 v2, 0xd00, v15
	v_or_b32_e32 v4, v2, v1
	v_lshlrev_b32_e32 v192, 1, v0
	v_add_u32_e32 v8, 0x1a000, v4
	global_load_dwordx4 v[0:3], v192, s[90:91] offset:1024
	v_lshlrev_b32_e32 v194, 1, v4
	global_load_dwordx4 v[4:7], v194, s[90:91] offset:2048
	v_lshlrev_b32_e32 v160, 1, v8
	global_load_dwordx4 v[8:11], v160, s[90:91] offset:2048
	v_lshlrev_b32_e32 v16, 1, v205
	v_and_b32_e32 v17, 0x80, v205
	v_lshrrev_b32_e32 v18, 5, v205
	s_movk_i32 s22, 0x70
	v_lshlrev_b32_e32 v19, 4, v99
	v_and_b32_e32 v22, 7, v99
	v_lshrrev_b32_e32 v23, 1, v99
	v_readlane_b32 s2, v253, 31
	v_and_or_b32 v16, v16, s22, v17
	v_and_b32_e32 v17, 4, v18
	v_and_b32_e32 v25, 8, v12
	v_or_b32_e32 v26, 32, v15
	v_lshlrev_b32_e32 v20, 3, v191
	v_readlane_b32 s3, v253, 32
	v_and_b32_e32 v18, 48, v19
	v_and_b32_e32 v19, 0xc0, v19
	v_and_or_b32 v22, v23, 8, v22
	v_and_or_b32 v23, v15, 16, v25
	v_and_or_b32 v15, v15, 3, v17
	v_and_or_b32 v17, v26, 48, v25
	v_lshlrev_b32_e32 v21, 1, v99
	v_cndmask_b32_e64 v24, 0, 1, s[2:3]
	v_bfe_u32 v13, v13, 5, 2
	v_lshlrev_b32_e32 v12, 8, v12
	v_and_b32_e32 v27, 0x100, v20
	v_lshlrev_b32_e32 v14, 1, v14
	v_and_or_b32 v19, v20, 24, v19
	v_lshlrev_b32_e32 v20, 4, v22
	v_lshrrev_b32_e32 v22, 1, v23
	v_lshrrev_b32_e32 v17, 1, v17
	v_and_b32_e32 v21, 32, v21
	v_cmp_ne_u32_e64 s[4:5], 1, v24
	v_lshl_or_b32 v15, v15, 6, v18
	v_bitop3_b32 v12, v16, v12, v14 bitop3:0xde
	v_or_b32_e32 v14, v22, v13
	v_or_b32_e32 v13, v17, v13
	s_waitcnt vmcnt(0)
	v_writelane_b32 v255, s4, 44
	s_andn2_b64 vcc, exec, s[2:3]
	v_or3_b32 v216, v19, v21, v27
	s_movk_i32 s2, 0x60
	v_add_u32_e32 v211, 0, v12
	v_lshl_or_b32 v12, v14, 9, v15
	v_lshl_or_b32 v13, v13, 9, v15
	v_lshl_add_u32 v206, v202, 8, 0
	v_writelane_b32 v255, s5, 45
	v_xor_b32_e32 v207, v20, v190
	v_bitop3_b32 v208, v190, v20, 32 bitop3:0x36
	v_bitop3_b32 v209, v190, v20, 64 bitop3:0x36
	v_bitop3_b32 v210, v190, v20, s2 bitop3:0x36
	v_add_u32_e32 v212, 0, v216
	v_add_u32_e32 v213, 0, v12
	v_add_u32_e32 v214, 0, v13
	s_mov_b64 s[2:3], -1
	s_waitcnt vmcnt(2)
	ds_write_b128 v211, v[0:3] offset:32768
	s_waitcnt vmcnt(1)
	ds_write_b128 v213, v[4:7]
	s_waitcnt vmcnt(0)
	ds_write_b128 v214, v[8:11]
	s_waitcnt lgkmcnt(0)
	s_barrier
	s_cbranch_vccnz .LBB0_520
	s_add_i32 s2, 0, 0x4000
	v_add_u32_e32 v217, s2, v216
	s_add_u32 s2, s7, s87
	s_addc_u32 s3, s6, 0
	s_add_u32 s2, s36, s2
	v_mov_b32_e32 v14, v161
	v_mov_b32_e32 v15, v161
	s_addc_u32 s3, s37, s3
	v_mov_b32_e32 v195, v161
	v_mov_b32_e32 v193, v161
	v_mov_b32_e32 v0, v161
	v_mov_b32_e32 v1, v161
	v_mov_b32_e32 v2, v161
	v_mov_b32_e32 v3, v161
	v_mov_b32_e32 v4, v161
	v_mov_b32_e32 v5, v161
	v_mov_b32_e32 v6, v161
	v_mov_b32_e32 v7, v161
	v_mov_b32_e32 v8, v161
	v_mov_b32_e32 v9, v161
	v_mov_b32_e32 v10, v161
	v_mov_b32_e32 v11, v161
	v_mov_b32_e32 v12, v161
	v_mov_b32_e32 v13, v161
	v_mov_b64_e32 v[30:31], v[14:15]
	v_mov_b64_e32 v[46:47], v[14:15]
	v_mov_b64_e32 v[62:63], v[14:15]
	v_lshl_add_u64 v[196:197], s[2:3], 0, v[160:161]
	v_lshl_add_u64 v[198:199], s[2:3], 0, v[194:195]
	v_lshl_add_u64 v[200:201], s[2:3], 0, v[192:193]
	s_mov_b32 s63, 0
	v_mov_b32_e32 v215, 0
	s_mov_b64 s[74:75], 0
	v_mov_b64_e32 v[28:29], v[12:13]
	v_mov_b64_e32 v[26:27], v[10:11]
	v_mov_b64_e32 v[24:25], v[8:9]
	v_mov_b64_e32 v[22:23], v[6:7]
	v_mov_b64_e32 v[20:21], v[4:5]
	v_mov_b64_e32 v[18:19], v[2:3]
	v_mov_b64_e32 v[16:17], v[0:1]
	v_mov_b64_e32 v[44:45], v[12:13]
	v_mov_b64_e32 v[42:43], v[10:11]
	v_mov_b64_e32 v[40:41], v[8:9]
	v_mov_b64_e32 v[38:39], v[6:7]
	v_mov_b64_e32 v[36:37], v[4:5]
	v_mov_b64_e32 v[34:35], v[2:3]
	v_mov_b64_e32 v[32:33], v[0:1]
	v_mov_b64_e32 v[60:61], v[12:13]
	v_mov_b64_e32 v[58:59], v[10:11]
	v_mov_b64_e32 v[56:57], v[8:9]
	v_mov_b64_e32 v[54:55], v[6:7]
	v_mov_b64_e32 v[52:53], v[4:5]
	v_mov_b64_e32 v[50:51], v[2:3]
	v_mov_b64_e32 v[48:49], v[0:1]
	s_branch .LBB0_497
	.p2align 6

.LBB0_520:
	s_and_b64 vcc, exec, s[2:3]
	s_cbranch_vccz .LBB0_543
	s_add_i32 s2, 0, 0x4000
	v_add_u32_e32 v158, s2, v216
	s_add_u32 s2, s7, s87
	s_addc_u32 s3, s6, 0
	s_add_u32 s74, s36, s2
	v_mov_b32_e32 v215, 0
	s_addc_u32 s75, s37, s3
	v_mov_b32_e32 v195, v161
	v_mov_b32_e32 v193, v161
	s_mov_b32 s63, 0
	v_mov_b32_e32 v0, 0
	v_mov_b32_e32 v1, v215
	v_mov_b32_e32 v2, v215
	v_mov_b32_e32 v3, v215
	v_mov_b32_e32 v4, v215
	v_mov_b32_e32 v5, v215
	v_mov_b32_e32 v6, v215
	v_mov_b32_e32 v7, v215
	v_mov_b32_e32 v8, v215
	v_mov_b32_e32 v9, v215
	v_mov_b32_e32 v10, v215
	v_mov_b32_e32 v11, v215
	v_mov_b32_e32 v12, v215
	v_mov_b32_e32 v13, v215
	v_mov_b32_e32 v14, v215
	v_mov_b32_e32 v15, v215
	v_mov_b32_e32 v16, 0
	v_mov_b32_e32 v17, v215
	v_mov_b32_e32 v18, v215
	v_mov_b32_e32 v19, v215
	v_mov_b32_e32 v20, v215
	v_mov_b32_e32 v21, v215
	v_mov_b32_e32 v22, v215
	v_mov_b32_e32 v23, v215
	v_mov_b32_e32 v24, v215
	v_mov_b32_e32 v25, v215
	v_mov_b32_e32 v26, v215
	v_mov_b32_e32 v27, v215
	v_mov_b32_e32 v28, v215
	v_mov_b32_e32 v29, v215
	v_mov_b32_e32 v30, v215
	v_mov_b32_e32 v31, v215
	v_mov_b32_e32 v32, 0
	v_mov_b32_e32 v33, v215
	v_mov_b32_e32 v34, v215
	v_mov_b32_e32 v35, v215
	v_mov_b32_e32 v36, v215
	v_mov_b32_e32 v37, v215
	v_mov_b32_e32 v38, v215
	v_mov_b32_e32 v39, v215
	v_mov_b32_e32 v40, v215
	v_mov_b32_e32 v41, v215
	v_mov_b32_e32 v42, v215
	v_mov_b32_e32 v43, v215
	v_mov_b32_e32 v44, v215
	v_mov_b32_e32 v45, v215
	v_mov_b32_e32 v46, v215
	v_mov_b32_e32 v47, v215
	v_mov_b32_e32 v48, 0
	v_mov_b32_e32 v49, v215
	v_mov_b32_e32 v50, v215
	v_mov_b32_e32 v51, v215
	v_mov_b32_e32 v52, v215
	v_mov_b32_e32 v53, v215
	v_mov_b32_e32 v54, v215
	v_mov_b32_e32 v55, v215
	v_mov_b32_e32 v56, v215
	v_mov_b32_e32 v57, v215
	v_mov_b32_e32 v58, v215
	v_mov_b32_e32 v59, v215
	v_mov_b32_e32 v60, v215
	v_mov_b32_e32 v61, v215
	v_mov_b32_e32 v62, v215
	v_mov_b32_e32 v63, v215
	s_branch .LBB0_523
	.p2align 6

.LBB0_543:
	v_and_b32_e32 v64, 0x1c0, v205
	s_add_i32 s63, 0, 0x10000
	v_mov_b32_e32 v65, v215
	v_lshl_add_u32 v64, v64, 2, s63
	s_nop 0
	v_permlane32_swap_b32_e32 v215, v65
	v_cmp_gt_u32_e32 vcc, 32, v191
	s_and_saveexec_b64 s[2:3], vcc
	v_add_f32_e32 v65, v215, v65
	v_lshl_add_u32 v66, v202, 2, v64
	ds_write_b32 v66, v65
	s_or_b64 exec, exec, s[2:3]
	s_waitcnt lgkmcnt(0)
	v_add_u32_e32 v72, v64, v190
	ds_read_b128 v[64:67], v72
	ds_read_b128 v[68:71], v72 offset:32
	s_lshl_b64 s[2:3], s[18:19], 11
	s_add_u32 s2, s79, s2
	s_addc_u32 s3, s80, s3
	s_waitcnt lgkmcnt(1)
	v_rcp_f32_e32 v73, v64
	v_rcp_f32_e32 v74, v65
	v_rcp_f32_e32 v75, v66
	v_rcp_f32_e32 v76, v67
	ds_read_b128 v[64:67], v72 offset:64
	s_add_u32 s74, s2, s11
	s_addc_u32 s75, s3, 0
	v_lshlrev_b32_e32 v160, 16, v204
	s_waitcnt lgkmcnt(1)
	v_rcp_f32_e32 v77, v68
	v_rcp_f32_e32 v78, v69
	v_rcp_f32_e32 v79, v70
	v_rcp_f32_e32 v80, v71
	ds_read_b128 v[68:71], v72 offset:96
	s_waitcnt lgkmcnt(1)
	v_rcp_f32_e32 v72, v64
	v_rcp_f32_e32 v81, v65
	v_lshl_add_u64 v[64:65], s[74:75], 0, v[160:161]
	v_lshlrev_b32_e32 v160, 1, v202
	v_rcp_f32_e32 v82, v66
	v_rcp_f32_e32 v83, v67
	v_lshlrev_b32_e32 v66, 13, v203
	v_lshl_add_u64 v[64:65], v[64:65], 0, v[160:161]
	v_mov_b32_e32 v67, v161
	v_mul_f32_e32 v0, v0, v73
	v_lshl_add_u64 v[64:65], v[64:65], 0, v[66:67]
	v_cvt_pk_bf16_f32 v0, v0, s0
	global_store_short v[64:65], v0, off
	v_mul_f32_e32 v0, v16, v73
	v_cvt_pk_bf16_f32 v0, v0, s0
	global_store_short v[64:65], v0, off offset:64
	v_mul_f32_e32 v0, v32, v73
	v_cvt_pk_bf16_f32 v0, v0, s0
	global_store_short v[64:65], v0, off offset:128
	v_mul_f32_e32 v0, v48, v73
	v_cvt_pk_bf16_f32 v0, v0, s0
	global_store_short v[64:65], v0, off offset:192
	v_mul_f32_e32 v0, v1, v74
	v_cvt_pk_bf16_f32 v0, v0, s0
	global_store_short v[64:65], v0, off offset:2048
	v_mul_f32_e32 v0, v17, v74
	v_cvt_pk_bf16_f32 v0, v0, s0
	global_store_short v[64:65], v0, off offset:2112
	v_mul_f32_e32 v0, v33, v74
	v_cvt_pk_bf16_f32 v0, v0, s0
	global_store_short v[64:65], v0, off offset:2176
	v_mul_f32_e32 v0, v49, v74
	v_cvt_pk_bf16_f32 v0, v0, s0
	global_store_short v[64:65], v0, off offset:2240
	v_mul_f32_e32 v0, v2, v75
	s_movk_i32 s2, 0x1000
	v_cvt_pk_bf16_f32 v2, v0, s0
	v_add_co_u32_e32 v0, vcc, s2, v64
	s_movk_i32 s2, 0x4000
	s_nop 0
	v_addc_co_u32_e32 v1, vcc, 0, v65, vcc
	global_store_short v[0:1], v2, off
	v_mul_f32_e32 v2, v18, v75
	v_cvt_pk_bf16_f32 v2, v2, s0
	global_store_short v[0:1], v2, off offset:64
	v_mul_f32_e32 v2, v34, v75
	v_cvt_pk_bf16_f32 v2, v2, s0
	global_store_short v[0:1], v2, off offset:128
	v_mul_f32_e32 v2, v50, v75
	v_cvt_pk_bf16_f32 v2, v2, s0
	global_store_short v[0:1], v2, off offset:192
	v_mul_f32_e32 v2, v3, v76
	v_cvt_pk_bf16_f32 v2, v2, s0
	global_store_short v[0:1], v2, off offset:2048
	v_mul_f32_e32 v2, v19, v76
	v_cvt_pk_bf16_f32 v2, v2, s0
	global_store_short v[0:1], v2, off offset:2112
	v_mul_f32_e32 v2, v35, v76
	v_cvt_pk_bf16_f32 v2, v2, s0
	global_store_short v[0:1], v2, off offset:2176
	v_mul_f32_e32 v2, v51, v76
	v_cvt_pk_bf16_f32 v2, v2, s0
	global_store_short v[0:1], v2, off offset:2240
	v_mul_f32_e32 v0, v4, v77
	v_cvt_pk_bf16_f32 v4, v0, s0
	v_add_co_u32_e32 v0, vcc, s2, v64
	s_movk_i32 s2, 0x5000
	s_nop 0
	v_addc_co_u32_e32 v1, vcc, 0, v65, vcc
	v_add_co_u32_e32 v2, vcc, s2, v64
	s_mov_b32 s2, 0x8000
	s_nop 0
	v_addc_co_u32_e32 v3, vcc, 0, v65, vcc
	global_store_short v[2:3], v4, off offset:-4096
	v_mul_f32_e32 v4, v20, v77
	v_cvt_pk_bf16_f32 v4, v4, s0
	global_store_short v[0:1], v4, off offset:64
	v_mul_f32_e32 v4, v36, v77
	v_cvt_pk_bf16_f32 v4, v4, s0
	global_store_short v[0:1], v4, off offset:128
	v_mul_f32_e32 v4, v52, v77
	v_cvt_pk_bf16_f32 v4, v4, s0
	global_store_short v[0:1], v4, off offset:192
	v_mul_f32_e32 v4, v5, v78
	v_cvt_pk_bf16_f32 v4, v4, s0
	global_store_short v[0:1], v4, off offset:2048
	v_mul_f32_e32 v4, v21, v78
	v_cvt_pk_bf16_f32 v4, v4, s0
	global_store_short v[0:1], v4, off offset:2112
	v_mul_f32_e32 v4, v37, v78
	v_cvt_pk_bf16_f32 v4, v4, s0
	global_store_short v[0:1], v4, off offset:2176
	v_mul_f32_e32 v4, v53, v78
	v_cvt_pk_bf16_f32 v4, v4, s0
	global_store_short v[0:1], v4, off offset:2240
	v_mul_f32_e32 v0, v6, v79
	v_cvt_pk_bf16_f32 v0, v0, s0
	global_store_short v[2:3], v0, off
	v_mul_f32_e32 v0, v22, v79
	v_cvt_pk_bf16_f32 v0, v0, s0
	global_store_short v[2:3], v0, off offset:64
	v_mul_f32_e32 v0, v38, v79
	v_cvt_pk_bf16_f32 v0, v0, s0
	global_store_short v[2:3], v0, off offset:128
	v_mul_f32_e32 v0, v54, v79
	v_cvt_pk_bf16_f32 v0, v0, s0
	global_store_short v[2:3], v0, off offset:192
	v_mul_f32_e32 v0, v7, v80
	v_cvt_pk_bf16_f32 v0, v0, s0
	global_store_short v[2:3], v0, off offset:2048
	v_mul_f32_e32 v0, v23, v80
	v_cvt_pk_bf16_f32 v0, v0, s0
	global_store_short v[2:3], v0, off offset:2112
	v_mul_f32_e32 v0, v39, v80
	v_cvt_pk_bf16_f32 v0, v0, s0
	global_store_short v[2:3], v0, off offset:2176
	v_mul_f32_e32 v0, v55, v80
	v_cvt_pk_bf16_f32 v0, v0, s0
	global_store_short v[2:3], v0, off offset:2240
	v_mul_f32_e32 v0, v8, v72
	v_cvt_pk_bf16_f32 v4, v0, s0
	v_add_co_u32_e32 v0, vcc, s2, v64
	s_mov_b32 s2, 0x9000
	s_nop 0
	v_addc_co_u32_e32 v1, vcc, 0, v65, vcc
	v_add_co_u32_e32 v2, vcc, s2, v64
	s_waitcnt lgkmcnt(0)
	v_rcp_f32_e32 v68, v68
	v_addc_co_u32_e32 v3, vcc, 0, v65, vcc
	global_store_short v[2:3], v4, off offset:-4096
	v_mul_f32_e32 v4, v24, v72
	v_cvt_pk_bf16_f32 v4, v4, s0
	global_store_short v[0:1], v4, off offset:64
	v_mul_f32_e32 v4, v40, v72
	v_cvt_pk_bf16_f32 v4, v4, s0
	global_store_short v[0:1], v4, off offset:128
	v_mul_f32_e32 v4, v56, v72
	v_cvt_pk_bf16_f32 v4, v4, s0
	global_store_short v[0:1], v4, off offset:192
	v_mul_f32_e32 v4, v9, v81
	v_cvt_pk_bf16_f32 v4, v4, s0
	global_store_short v[0:1], v4, off offset:2048
	v_mul_f32_e32 v4, v25, v81
	v_cvt_pk_bf16_f32 v4, v4, s0
	global_store_short v[0:1], v4, off offset:2112
	v_mul_f32_e32 v4, v41, v81
	v_cvt_pk_bf16_f32 v4, v4, s0
	global_store_short v[0:1], v4, off offset:2176
	v_mul_f32_e32 v4, v57, v81
	v_cvt_pk_bf16_f32 v4, v4, s0
	global_store_short v[0:1], v4, off offset:2240
	v_mul_f32_e32 v0, v10, v82
	v_cvt_pk_bf16_f32 v0, v0, s0
	global_store_short v[2:3], v0, off
	v_mul_f32_e32 v0, v26, v82
	v_cvt_pk_bf16_f32 v0, v0, s0
	global_store_short v[2:3], v0, off offset:64
	v_mul_f32_e32 v0, v42, v82
	v_cvt_pk_bf16_f32 v0, v0, s0
	global_store_short v[2:3], v0, off offset:128
	v_mul_f32_e32 v0, v58, v82
	v_cvt_pk_bf16_f32 v0, v0, s0
	global_store_short v[2:3], v0, off offset:192
	v_mul_f32_e32 v0, v11, v83
	v_cvt_pk_bf16_f32 v0, v0, s0
	global_store_short v[2:3], v0, off offset:2048
	v_mul_f32_e32 v0, v27, v83
	v_cvt_pk_bf16_f32 v0, v0, s0
	global_store_short v[2:3], v0, off offset:2112
	v_mul_f32_e32 v0, v43, v83
	v_cvt_pk_bf16_f32 v0, v0, s0
	global_store_short v[2:3], v0, off offset:2176
	v_mul_f32_e32 v0, v59, v83
	v_cvt_pk_bf16_f32 v0, v0, s0
	global_store_short v[2:3], v0, off offset:2240
	v_mul_f32_e32 v0, v12, v68
	s_mov_b32 s2, 0xc000
	v_cvt_pk_bf16_f32 v4, v0, s0
	v_add_co_u32_e32 v0, vcc, s2, v64
	s_mov_b32 s2, 0xd000
	s_nop 0
	v_addc_co_u32_e32 v1, vcc, 0, v65, vcc
	v_add_co_u32_e32 v2, vcc, s2, v64
	v_rcp_f32_e32 v69, v69
	s_nop 0
	v_addc_co_u32_e32 v3, vcc, 0, v65, vcc
	global_store_short v[2:3], v4, off offset:-4096
	v_mul_f32_e32 v4, v28, v68
	v_cvt_pk_bf16_f32 v4, v4, s0
	global_store_short v[0:1], v4, off offset:64
	v_mul_f32_e32 v4, v44, v68
	v_cvt_pk_bf16_f32 v4, v4, s0
	global_store_short v[0:1], v4, off offset:128
	v_mul_f32_e32 v4, v60, v68
	v_cvt_pk_bf16_f32 v4, v4, s0
	global_store_short v[0:1], v4, off offset:192
	v_mul_f32_e32 v4, v13, v69
	v_cvt_pk_bf16_f32 v4, v4, s0
	global_store_short v[0:1], v4, off offset:2048
	v_mul_f32_e32 v4, v29, v69
	v_cvt_pk_bf16_f32 v4, v4, s0
	v_rcp_f32_e32 v70, v70
	global_store_short v[0:1], v4, off offset:2112
	v_mul_f32_e32 v4, v45, v69
	v_cvt_pk_bf16_f32 v4, v4, s0
	global_store_short v[0:1], v4, off offset:2176
	v_mul_f32_e32 v4, v61, v69
	v_cvt_pk_bf16_f32 v4, v4, s0
	global_store_short v[0:1], v4, off offset:2240
	v_mul_f32_e32 v0, v14, v70
	v_cvt_pk_bf16_f32 v0, v0, s0
	global_store_short v[2:3], v0, off
	v_mul_f32_e32 v0, v30, v70
	v_cvt_pk_bf16_f32 v0, v0, s0
	v_rcp_f32_e32 v71, v71
	global_store_short v[2:3], v0, off offset:64
	v_mul_f32_e32 v0, v46, v70
	v_cvt_pk_bf16_f32 v0, v0, s0
	global_store_short v[2:3], v0, off offset:128
	v_mul_f32_e32 v0, v62, v70
	v_cvt_pk_bf16_f32 v0, v0, s0
	global_store_short v[2:3], v0, off offset:192
	v_mul_f32_e32 v0, v15, v71
	v_cvt_pk_bf16_f32 v0, v0, s0
	global_store_short v[2:3], v0, off offset:2048
	v_mul_f32_e32 v0, v31, v71
	v_cvt_pk_bf16_f32 v0, v0, s0
	global_store_short v[2:3], v0, off offset:2112
	v_mul_f32_e32 v0, v47, v71
	v_cvt_pk_bf16_f32 v0, v0, s0
	global_store_short v[2:3], v0, off offset:2176
	v_mul_f32_e32 v0, v63, v71
	v_cvt_pk_bf16_f32 v0, v0, s0
	v_readlane_b32 s2, v254, 61
	global_store_short v[2:3], v0, off offset:2240
	s_waitcnt vmcnt(63) expcnt(7) lgkmcnt(15)
	v_mov_b32_e32 v0, s2
	v_readlane_b32 s2, v254, 62
	s_barrier
	s_nop 0
	v_mov_b32_e32 v1, s2
	ds_read_b32 v0, v0
	ds_read_b32 v1, v1
	v_readlane_b32 s2, v253, 20
	v_mov_b32_e32 v191, v161
	v_mov_b32_e32 v49, v161
	s_waitcnt lgkmcnt(1)
	v_readfirstlane_b32 s18, v0
	s_waitcnt lgkmcnt(0)
	v_readfirstlane_b32 s19, v1
	v_mbcnt_lo_u32_b32 v99, -1, 0
	v_mbcnt_hi_u32_b32 v99, -1, v99
	s_nop 0
	v_add_u32_e32 v205, s2, v99
	v_lshrrev_b32_e32 v0, 1, v205
	v_and_b32_e32 v203, 31, v99
	v_and_b32_e32 v204, 0xe0, v0
	v_or_b32_e32 v48, v204, v203
	v_mul_u32_u24_e32 v0, 0xd00, v48
	v_bfe_u32 v202, v99, 5, 1
	v_lshlrev_b32_e32 v160, 1, v0
	v_lshl_add_u64 v[0:1], s[34:35], 0, v[160:161]
	v_lshlrev_b32_e32 v190, 4, v202
	v_lshl_add_u64 v[12:13], v[0:1], 0, v[190:191]
	global_load_dwordx4 v[0:3], v[12:13], off offset:160
	global_load_dwordx4 v[4:7], v[12:13], off offset:224
	global_load_dwordx4 v[8:11], v[12:13], off offset:128
	s_nop 0
	global_load_dwordx4 v[12:15], v[12:13], off offset:192
	v_or_b32_e32 v48, s10, v48
	v_lshlrev_b32_e32 v48, 7, v48
	v_and_b32_e32 v160, 32, v99
	v_lshl_add_u64 v[50:51], s[44:45], 0, v[48:49]
	v_lshl_add_u64 v[48:49], s[46:47], 0, v[48:49]
	global_load_dwordx4 v[16:19], v160, s[92:93]
	global_load_dwordx4 v[20:23], v160, s[92:93] offset:16
	global_load_dwordx4 v[24:27], v160, s[92:93] offset:64
	global_load_dwordx4 v[28:31], v160, s[92:93] offset:80
	global_load_dwordx4 v[32:35], v160, s[92:93] offset:128
	global_load_dwordx4 v[36:39], v160, s[92:93] offset:144
	global_load_dwordx4 v[40:43], v160, s[92:93] offset:192
	global_load_dwordx4 v[44:47], v160, s[92:93] offset:208
	v_lshl_add_u64 v[68:69], v[50:51], 0, v[160:161]
	v_lshl_add_u64 v[76:77], v[48:49], 0, v[160:161]
	global_load_dwordx4 v[48:51], v[68:69], off
	global_load_dwordx4 v[52:55], v[68:69], off offset:16
	global_load_dwordx4 v[56:59], v[76:77], off
	global_load_dwordx4 v[60:63], v[76:77], off offset:16
	global_load_dwordx4 v[64:67], v[68:69], off offset:64
	s_nop 0
	global_load_dwordx4 v[68:71], v[68:69], off offset:80
	s_nop 0
	global_load_dwordx4 v[72:75], v[76:77], off offset:64
	s_nop 0
	global_load_dwordx4 v[76:79], v[76:77], off offset:80
	v_and_b32_e32 v191, 63, v99
	s_waitcnt vmcnt(19)
	v_lshlrev_b32_e32 v80, 16, v3
	v_and_b32_e32 v81, 0xffff0000, v3
	s_waitcnt vmcnt(17)
	v_and_b32_e32 v97, 0xffff0000, v8
	v_lshlrev_b32_e32 v82, 16, v7
	v_and_b32_e32 v83, 0xffff0000, v7
	v_lshlrev_b32_e32 v84, 16, v2
	v_and_b32_e32 v85, 0xffff0000, v2
	v_lshlrev_b32_e32 v2, 16, v6
	v_and_b32_e32 v3, 0xffff0000, v6
	v_lshlrev_b32_e32 v6, 16, v1
	v_and_b32_e32 v7, 0xffff0000, v1
	v_lshlrev_b32_e32 v86, 16, v5
	v_and_b32_e32 v87, 0xffff0000, v5
	v_lshlrev_b32_e32 v88, 16, v0
	v_and_b32_e32 v89, 0xffff0000, v0
	v_lshlrev_b32_e32 v0, 16, v4
	v_and_b32_e32 v1, 0xffff0000, v4
	v_lshlrev_b32_e32 v4, 16, v11
	v_and_b32_e32 v5, 0xffff0000, v11
	s_waitcnt vmcnt(16)
	v_lshlrev_b32_e32 v90, 16, v15
	v_and_b32_e32 v91, 0xffff0000, v15
	v_lshlrev_b32_e32 v92, 16, v10
	v_and_b32_e32 v93, 0xffff0000, v10
	v_lshlrev_b32_e32 v10, 16, v14
	v_and_b32_e32 v11, 0xffff0000, v14
	v_lshlrev_b32_e32 v14, 16, v9
	v_and_b32_e32 v15, 0xffff0000, v9
	v_lshlrev_b32_e32 v96, 16, v8
	v_lshlrev_b32_e32 v8, 16, v12
	v_and_b32_e32 v9, 0xffff0000, v12
	v_mul_f32_e32 v12, v97, v97
	v_lshlrev_b32_e32 v94, 16, v13
	v_and_b32_e32 v95, 0xffff0000, v13
	v_pk_fma_f32 v[12:13], v[96:97], v[96:97], v[12:13] op_sel_hi:[1,1,0]
	v_mul_f32_e32 v98, v15, v15
	v_pk_fma_f32 v[12:13], v[14:15], v[14:15], v[12:13]
	s_nop 0
	v_pk_add_f32 v[12:13], v[98:99], v[12:13] op_sel_hi:[0,1]
	v_pk_fma_f32 v[12:13], v[92:93], v[92:93], v[12:13]
	v_mul_f32_e32 v98, v93, v93
	v_pk_add_f32 v[12:13], v[98:99], v[12:13] op_sel_hi:[0,1]
	v_pk_fma_f32 v[12:13], v[4:5], v[4:5], v[12:13]
	v_mul_f32_e32 v98, v5, v5
	v_pk_add_f32 v[12:13], v[98:99], v[12:13] op_sel_hi:[0,1]
	v_pk_fma_f32 v[12:13], v[88:89], v[88:89], v[12:13]
	v_mul_f32_e32 v98, v89, v89
	v_pk_add_f32 v[12:13], v[98:99], v[12:13] op_sel_hi:[0,1]
	v_pk_fma_f32 v[12:13], v[6:7], v[6:7], v[12:13]
	v_mul_f32_e32 v98, v7, v7
	v_pk_add_f32 v[12:13], v[98:99], v[12:13] op_sel_hi:[0,1]
	v_pk_fma_f32 v[12:13], v[84:85], v[84:85], v[12:13]
	v_mul_f32_e32 v98, v85, v85
	v_pk_add_f32 v[12:13], v[98:99], v[12:13] op_sel_hi:[0,1]
	v_pk_fma_f32 v[12:13], v[80:81], v[80:81], v[12:13]
	v_mul_f32_e32 v98, v81, v81
	v_pk_add_f32 v[12:13], v[98:99], v[12:13] op_sel_hi:[0,1]
	v_pk_fma_f32 v[12:13], v[8:9], v[8:9], v[12:13]
	v_mul_f32_e32 v98, v9, v9
	v_pk_add_f32 v[12:13], v[98:99], v[12:13] op_sel_hi:[0,1]
	v_pk_fma_f32 v[12:13], v[94:95], v[94:95], v[12:13]
	v_mul_f32_e32 v98, v95, v95
	v_pk_add_f32 v[12:13], v[98:99], v[12:13] op_sel_hi:[0,1]
	v_pk_fma_f32 v[12:13], v[10:11], v[10:11], v[12:13]
	v_mul_f32_e32 v98, v11, v11
	v_pk_add_f32 v[12:13], v[98:99], v[12:13] op_sel_hi:[0,1]
	v_pk_fma_f32 v[12:13], v[90:91], v[90:91], v[12:13]
	v_mul_f32_e32 v98, v91, v91
	v_pk_add_f32 v[12:13], v[98:99], v[12:13] op_sel_hi:[0,1]
	v_pk_fma_f32 v[12:13], v[0:1], v[0:1], v[12:13]
	v_mul_f32_e32 v98, v1, v1
	v_pk_add_f32 v[12:13], v[98:99], v[12:13] op_sel_hi:[0,1]
	v_pk_fma_f32 v[12:13], v[86:87], v[86:87], v[12:13]
	v_mul_f32_e32 v98, v87, v87
	v_pk_add_f32 v[12:13], v[98:99], v[12:13] op_sel_hi:[0,1]
	v_pk_fma_f32 v[12:13], v[2:3], v[2:3], v[12:13]
	v_mul_f32_e32 v98, v3, v3
	v_pk_add_f32 v[12:13], v[98:99], v[12:13] op_sel_hi:[0,1]
	v_pk_fma_f32 v[12:13], v[82:83], v[82:83], v[12:13]
	v_mul_f32_e32 v98, v83, v83
	v_pk_add_f32 v[12:13], v[98:99], v[12:13] op_sel_hi:[0,1]
	v_mov_b32_e32 v13, v12
	s_nop 1
	v_permlane32_swap_b32_e32 v12, v13
	v_add_f32_e32 v12, v12, v13
	v_fmamk_f32 v12, v12, 0x3c800000, v240
	v_rsq_f32_e32 v12, v12
	s_waitcnt vmcnt(13)
	v_pk_mul_f32 v[24:25], v[24:25], v[12:13] op_sel_hi:[1,0]
	s_nop 0
	v_pk_mul_f32 v[24:25], v[24:25], v[88:89]
	s_waitcnt vmcnt(9)
	v_pk_mul_f32 v[40:41], v[12:13], v[40:41] op_sel_hi:[0,1]
	v_pk_mul_f32 v[0:1], v[40:41], v[0:1]
	s_waitcnt vmcnt(1)
	v_pk_mul_f32 v[40:41], v[24:25], v[72:73]
	v_pk_mul_f32 v[26:27], v[26:27], v[12:13] op_sel_hi:[1,0]
	v_pk_fma_f32 v[40:41], v[0:1], v[64:65], v[40:41]
	v_pk_mul_f32 v[0:1], v[0:1], v[72:73]
	v_pk_mul_f32 v[6:7], v[26:27], v[6:7]
	v_pk_mul_f32 v[26:27], v[12:13], v[42:43] op_sel_hi:[0,1]
	v_pk_fma_f32 v[0:1], v[24:25], v[64:65], v[0:1] neg_lo:[0,0,1] neg_hi:[0,0,1]
	v_pk_mul_f32 v[26:27], v[26:27], v[86:87]
	v_pk_mul_f32 v[0:1], v[0:1], s[62:63] op_sel_hi:[1,0]
	v_pk_mul_f32 v[44:45], v[12:13], v[44:45] op_sel_hi:[0,1]
	v_cvt_pk_bf16_f32 v166, v0, v1
	v_pk_mul_f32 v[0:1], v[26:27], v[74:75]
	v_pk_mul_f32 v[28:29], v[28:29], v[12:13] op_sel_hi:[1,0]
	v_pk_fma_f32 v[0:1], v[6:7], v[66:67], v[0:1] neg_lo:[0,0,1] neg_hi:[0,0,1]
	v_pk_mul_f32 v[2:3], v[44:45], v[2:3]
	v_pk_mul_f32 v[22:23], v[22:23], v[12:13] op_sel_hi:[1,0]
	v_pk_mul_f32 v[18:19], v[18:19], v[12:13] op_sel_hi:[1,0]
	v_pk_mul_f32 v[16:17], v[16:17], v[12:13] op_sel_hi:[1,0]
	v_pk_mul_f32 v[0:1], v[0:1], s[62:63] op_sel_hi:[1,0]
	v_pk_mul_f32 v[30:31], v[30:31], v[12:13] op_sel_hi:[1,0]
	v_pk_mul_f32 v[46:47], v[12:13], v[46:47] op_sel_hi:[0,1]
	v_pk_mul_f32 v[28:29], v[28:29], v[84:85]
	v_pk_mul_f32 v[4:5], v[22:23], v[4:5]
	v_pk_mul_f32 v[22:23], v[12:13], v[38:39] op_sel_hi:[0,1]
	v_pk_mul_f32 v[20:21], v[20:21], v[12:13] op_sel_hi:[1,0]
	v_pk_mul_f32 v[36:37], v[12:13], v[36:37] op_sel_hi:[0,1]
	v_pk_mul_f32 v[14:15], v[18:19], v[14:15]
	v_pk_mul_f32 v[18:19], v[12:13], v[34:35] op_sel_hi:[0,1]
	v_pk_mul_f32 v[16:17], v[16:17], v[96:97]
	v_pk_mul_f32 v[12:13], v[12:13], v[32:33] op_sel_hi:[0,1]
	v_cvt_pk_bf16_f32 v167, v0, v1
	s_waitcnt vmcnt(0)
	v_pk_mul_f32 v[0:1], v[2:3], v[76:77]
	v_pk_mul_f32 v[8:9], v[12:13], v[8:9]
	v_pk_mul_f32 v[12:13], v[16:17], v[56:57]
	v_pk_fma_f32 v[0:1], v[28:29], v[68:69], v[0:1] neg_lo:[0,0,1] neg_hi:[0,0,1]
	v_pk_mul_f32 v[46:47], v[46:47], v[82:83]
	v_pk_fma_f32 v[12:13], v[8:9], v[48:49], v[12:13]
	v_pk_mul_f32 v[8:9], v[8:9], v[56:57]
	v_pk_mul_f32 v[0:1], v[0:1], s[62:63] op_sel_hi:[1,0]
	v_pk_mul_f32 v[30:31], v[30:31], v[80:81]
	v_pk_fma_f32 v[8:9], v[16:17], v[48:49], v[8:9] neg_lo:[0,0,1] neg_hi:[0,0,1]
	v_cvt_pk_bf16_f32 v168, v0, v1
	v_pk_mul_f32 v[0:1], v[46:47], v[78:79]
	v_pk_mul_f32 v[18:19], v[18:19], v[94:95]
	v_pk_mul_f32 v[8:9], v[8:9], s[62:63] op_sel_hi:[1,0]
	v_pk_fma_f32 v[0:1], v[30:31], v[70:71], v[0:1] neg_lo:[0,0,1] neg_hi:[0,0,1]
	v_pk_mul_f32 v[20:21], v[20:21], v[92:93]
	v_pk_mul_f32 v[34:35], v[14:15], v[58:59]
	v_cvt_pk_bf16_f32 v162, v8, v9
	v_pk_mul_f32 v[8:9], v[18:19], v[58:59]
	v_pk_mul_f32 v[0:1], v[0:1], s[62:63] op_sel_hi:[1,0]
	v_pk_mul_f32 v[10:11], v[36:37], v[10:11]
	v_pk_mul_f32 v[36:37], v[20:21], v[60:61]
	v_pk_fma_f32 v[34:35], v[18:19], v[50:51], v[34:35]
	v_pk_fma_f32 v[8:9], v[14:15], v[50:51], v[8:9] neg_lo:[0,0,1] neg_hi:[0,0,1]
	v_cvt_pk_bf16_f32 v169, v0, v1
	v_pk_mul_f32 v[0:1], v[12:13], s[62:63] op_sel_hi:[1,0]
	v_pk_mul_f32 v[22:23], v[22:23], v[90:91]
	v_pk_mul_f32 v[38:39], v[4:5], v[62:63]
	v_pk_fma_f32 v[36:37], v[10:11], v[52:53], v[36:37]
	v_pk_mul_f32 v[8:9], v[8:9], s[62:63] op_sel_hi:[1,0]
	v_cvt_pk_bf16_f32 v170, v0, v1
	v_pk_mul_f32 v[0:1], v[34:35], s[62:63] op_sel_hi:[1,0]
	v_pk_fma_f32 v[38:39], v[22:23], v[54:55], v[38:39]
	v_cvt_pk_bf16_f32 v163, v8, v9
	v_pk_mul_f32 v[8:9], v[10:11], v[60:61]
	v_cvt_pk_bf16_f32 v171, v0, v1
	v_pk_mul_f32 v[0:1], v[36:37], s[62:63] op_sel_hi:[1,0]
	v_pk_mul_f32 v[42:43], v[6:7], v[74:75]
	v_pk_fma_f32 v[8:9], v[20:21], v[52:53], v[8:9] neg_lo:[0,0,1] neg_hi:[0,0,1]
	v_cvt_pk_bf16_f32 v172, v0, v1
	v_pk_mul_f32 v[0:1], v[38:39], s[62:63] op_sel_hi:[1,0]
	v_pk_mul_f32 v[44:45], v[28:29], v[76:77]
	v_pk_fma_f32 v[42:43], v[26:27], v[66:67], v[42:43]
	v_pk_mul_f32 v[8:9], v[8:9], s[62:63] op_sel_hi:[1,0]
	v_cvt_pk_bf16_f32 v173, v0, v1
	v_pk_mul_f32 v[0:1], v[40:41], s[62:63] op_sel_hi:[1,0]
	v_pk_fma_f32 v[44:45], v[2:3], v[68:69], v[44:45]
	v_pk_mul_f32 v[32:33], v[30:31], v[78:79]
	v_cvt_pk_bf16_f32 v164, v8, v9
	v_pk_mul_f32 v[8:9], v[22:23], v[62:63]
	v_cvt_pk_bf16_f32 v174, v0, v1
	v_pk_mul_f32 v[0:1], v[42:43], s[62:63] op_sel_hi:[1,0]
	v_pk_fma_f32 v[32:33], v[46:47], v[70:71], v[32:33]
	v_pk_fma_f32 v[4:5], v[4:5], v[54:55], v[8:9] neg_lo:[0,0,1] neg_hi:[0,0,1]
	v_cvt_pk_bf16_f32 v175, v0, v1
	v_pk_mul_f32 v[0:1], v[44:45], s[62:63] op_sel_hi:[1,0]
	v_pk_mul_f32 v[4:5], v[4:5], s[62:63] op_sel_hi:[1,0]
	v_cvt_pk_bf16_f32 v176, v0, v1
	v_pk_mul_f32 v[0:1], v[32:33], s[62:63] op_sel_hi:[1,0]
	v_cvt_pk_bf16_f32 v165, v4, v5
	v_cvt_pk_bf16_f32 v177, v0, v1
	v_bfe_u32 v12, v205, 3, 6
	v_lshlrev_b32_e32 v13, 3, v99
	v_and_b32_e32 v14, 56, v13
	v_mul_u32_u24_e32 v0, 0xd00, v12
	v_bfe_u32 v15, v205, 4, 5
	v_or_b32_e32 v0, v0, v14
	v_and_b32_e32 v1, 0x78, v13
	v_mul_u32_u24_e32 v2, 0xd00, v15
	v_or_b32_e32 v4, v2, v1
	v_lshlrev_b32_e32 v192, 1, v0
	v_add_u32_e32 v8, 0x1a000, v4
	global_load_dwordx4 v[0:3], v192, s[90:91] offset:1152
	v_lshlrev_b32_e32 v194, 1, v4
	global_load_dwordx4 v[4:7], v194, s[90:91] offset:2048
	v_lshlrev_b32_e32 v160, 1, v8
	global_load_dwordx4 v[8:11], v160, s[90:91] offset:2048
	v_readlane_b32 s2, v255, 44
	v_readlane_b32 s3, v255, 45
	v_lshlrev_b32_e32 v16, 1, v205
	v_and_b32_e32 v17, 0x80, v205
	v_lshrrev_b32_e32 v18, 5, v205
	s_and_b64 vcc, exec, s[2:3]
	s_movk_i32 s2, 0x70
	v_lshlrev_b32_e32 v19, 4, v99
	v_and_b32_e32 v22, 7, v99
	v_lshrrev_b32_e32 v23, 1, v99
	v_and_or_b32 v16, v16, s2, v17
	v_and_b32_e32 v17, 4, v18
	v_and_b32_e32 v24, 8, v12
	v_or_b32_e32 v25, 32, v15
	v_lshlrev_b32_e32 v20, 3, v191
	v_and_b32_e32 v18, 48, v19
	v_and_b32_e32 v19, 0xc0, v19
	v_and_or_b32 v22, v23, 8, v22
	v_and_or_b32 v23, v15, 16, v24
	v_and_or_b32 v15, v15, 3, v17
	v_and_or_b32 v17, v25, 48, v24
	v_lshlrev_b32_e32 v21, 1, v99
	v_bfe_u32 v13, v13, 5, 2
	v_lshlrev_b32_e32 v12, 8, v12
	v_and_b32_e32 v26, 0x100, v20
	v_lshlrev_b32_e32 v14, 1, v14
	v_and_or_b32 v19, v20, 24, v19
	v_lshlrev_b32_e32 v20, 4, v22
	v_lshrrev_b32_e32 v22, 1, v23
	v_lshrrev_b32_e32 v17, 1, v17
	v_and_b32_e32 v21, 32, v21
	v_lshl_or_b32 v15, v15, 6, v18
	v_bitop3_b32 v12, v16, v12, v14 bitop3:0xde
	v_or_b32_e32 v14, v22, v13
	v_or_b32_e32 v13, v17, v13
	s_waitcnt vmcnt(0)
	v_or3_b32 v216, v19, v21, v26
	s_movk_i32 s2, 0x60
	v_add_u32_e32 v211, 0, v12
	v_lshl_or_b32 v12, v14, 9, v15
	v_lshl_or_b32 v13, v13, 9, v15
	v_lshl_add_u32 v206, v203, 8, 0
	v_xor_b32_e32 v207, v20, v190
	v_bitop3_b32 v208, v190, v20, 32 bitop3:0x36
	v_bitop3_b32 v209, v190, v20, 64 bitop3:0x36
	v_bitop3_b32 v210, v190, v20, s2 bitop3:0x36
	v_add_u32_e32 v212, 0, v216
	v_add_u32_e32 v213, 0, v12
	v_add_u32_e32 v214, 0, v13
	s_mov_b64 s[2:3], -1
	s_waitcnt vmcnt(2)
	ds_write_b128 v211, v[0:3] offset:32768
	s_waitcnt vmcnt(1)
	ds_write_b128 v213, v[4:7]
	s_waitcnt vmcnt(0)
	ds_write_b128 v214, v[8:11]
	s_waitcnt lgkmcnt(0)
	s_barrier
	s_cbranch_vccnz .LBB0_571
	s_add_i32 s2, 0, 0x4000
	v_add_u32_e32 v217, s2, v216
	s_add_u32 s2, s7, s87
	s_addc_u32 s3, s6, 0
	s_add_u32 s2, s36, s2
	v_mov_b32_e32 v14, v161
	v_mov_b32_e32 v15, v161
	s_addc_u32 s3, s37, s3
	v_mov_b32_e32 v195, v161
	v_mov_b32_e32 v193, v161
	v_mov_b32_e32 v0, v161
	v_mov_b32_e32 v1, v161
	v_mov_b32_e32 v2, v161
	v_mov_b32_e32 v3, v161
	v_mov_b32_e32 v4, v161
	v_mov_b32_e32 v5, v161
	v_mov_b32_e32 v6, v161
	v_mov_b32_e32 v7, v161
	v_mov_b32_e32 v8, v161
	v_mov_b32_e32 v9, v161
	v_mov_b32_e32 v10, v161
	v_mov_b32_e32 v11, v161
	v_mov_b32_e32 v12, v161
	v_mov_b32_e32 v13, v161
	v_mov_b64_e32 v[30:31], v[14:15]
	v_mov_b64_e32 v[46:47], v[14:15]
	v_mov_b64_e32 v[62:63], v[14:15]
	v_lshl_add_u64 v[196:197], s[2:3], 0, v[160:161]
	v_lshl_add_u64 v[198:199], s[2:3], 0, v[194:195]
	v_lshl_add_u64 v[200:201], s[2:3], 0, v[192:193]
	s_mov_b32 s10, 0
	v_mov_b32_e32 v215, 0
	s_mov_b64 s[90:91], 0
	v_mov_b64_e32 v[28:29], v[12:13]
	v_mov_b64_e32 v[26:27], v[10:11]
	v_mov_b64_e32 v[24:25], v[8:9]
	v_mov_b64_e32 v[22:23], v[6:7]
	v_mov_b64_e32 v[20:21], v[4:5]
	v_mov_b64_e32 v[18:19], v[2:3]
	v_mov_b64_e32 v[16:17], v[0:1]
	v_mov_b64_e32 v[44:45], v[12:13]
	v_mov_b64_e32 v[42:43], v[10:11]
	v_mov_b64_e32 v[40:41], v[8:9]
	v_mov_b64_e32 v[38:39], v[6:7]
	v_mov_b64_e32 v[36:37], v[4:5]
	v_mov_b64_e32 v[34:35], v[2:3]
	v_mov_b64_e32 v[32:33], v[0:1]
	v_mov_b64_e32 v[60:61], v[12:13]
	v_mov_b64_e32 v[58:59], v[10:11]
	v_mov_b64_e32 v[56:57], v[8:9]
	v_mov_b64_e32 v[54:55], v[6:7]
	v_mov_b64_e32 v[52:53], v[4:5]
	v_mov_b64_e32 v[50:51], v[2:3]
	v_mov_b64_e32 v[48:49], v[0:1]
	s_branch .LBB0_548
	.p2align 6

.LBB0_571:
	s_and_b64 vcc, exec, s[2:3]
	s_cbranch_vccz .LBB0_594
	s_add_i32 s2, 0, 0x4000
	v_add_u32_e32 v158, s2, v216
	s_add_u32 s2, s7, s87
	s_addc_u32 s3, s6, 0
	s_add_u32 s90, s36, s2
	v_mov_b32_e32 v215, 0
	s_addc_u32 s91, s37, s3
	v_mov_b32_e32 v195, v161
	v_mov_b32_e32 v193, v161
	s_mov_b32 s6, 0
	v_mov_b32_e32 v0, 0
	v_mov_b32_e32 v1, v215
	v_mov_b32_e32 v2, v215
	v_mov_b32_e32 v3, v215
	v_mov_b32_e32 v4, v215
	v_mov_b32_e32 v5, v215
	v_mov_b32_e32 v6, v215
	v_mov_b32_e32 v7, v215
	v_mov_b32_e32 v8, v215
	v_mov_b32_e32 v9, v215
	v_mov_b32_e32 v10, v215
	v_mov_b32_e32 v11, v215
	v_mov_b32_e32 v12, v215
	v_mov_b32_e32 v13, v215
	v_mov_b32_e32 v14, v215
	v_mov_b32_e32 v15, v215
	v_mov_b32_e32 v16, 0
	v_mov_b32_e32 v17, v215
	v_mov_b32_e32 v18, v215
	v_mov_b32_e32 v19, v215
	v_mov_b32_e32 v20, v215
	v_mov_b32_e32 v21, v215
	v_mov_b32_e32 v22, v215
	v_mov_b32_e32 v23, v215
	v_mov_b32_e32 v24, v215
	v_mov_b32_e32 v25, v215
	v_mov_b32_e32 v26, v215
	v_mov_b32_e32 v27, v215
	v_mov_b32_e32 v28, v215
	v_mov_b32_e32 v29, v215
	v_mov_b32_e32 v30, v215
	v_mov_b32_e32 v31, v215
	v_mov_b32_e32 v32, 0
	v_mov_b32_e32 v33, v215
	v_mov_b32_e32 v34, v215
	v_mov_b32_e32 v35, v215
	v_mov_b32_e32 v36, v215
	v_mov_b32_e32 v37, v215
	v_mov_b32_e32 v38, v215
	v_mov_b32_e32 v39, v215
	v_mov_b32_e32 v40, v215
	v_mov_b32_e32 v41, v215
	v_mov_b32_e32 v42, v215
	v_mov_b32_e32 v43, v215
	v_mov_b32_e32 v44, v215
	v_mov_b32_e32 v45, v215
	v_mov_b32_e32 v46, v215
	v_mov_b32_e32 v47, v215
	v_mov_b32_e32 v48, 0
	v_mov_b32_e32 v49, v215
	v_mov_b32_e32 v50, v215
	v_mov_b32_e32 v51, v215
	v_mov_b32_e32 v52, v215
	v_mov_b32_e32 v53, v215
	v_mov_b32_e32 v54, v215
	v_mov_b32_e32 v55, v215
	v_mov_b32_e32 v56, v215
	v_mov_b32_e32 v57, v215
	v_mov_b32_e32 v58, v215
	v_mov_b32_e32 v59, v215
	v_mov_b32_e32 v60, v215
	v_mov_b32_e32 v61, v215
	v_mov_b32_e32 v62, v215
	v_mov_b32_e32 v63, v215
	s_branch .LBB0_574
	.p2align 6

.LBB0_600:
	s_or_b64 exec, exec, s[22:23]
	v_add_f32_e32 v180, v180, v181
	v_fmamk_f32 v180, v180, 0x3c2aaaab, v240
	v_rsq_f32_e32 v180, v180
	s_lshr_b32 s3, s79, 2
	s_and_b32 s3, s3, 7
	s_lshl_b32 s23, s3, 8
	v_pk_mul_f32 v[16:17], v[16:17], v[180:181] op_sel_hi:[1,0]
	v_pk_mul_f32 v[18:19], v[18:19], v[180:181] op_sel_hi:[1,0]
	v_pk_mul_f32 v[16:17], v[16:17], v[176:177]
	v_pk_mul_f32 v[34:35], v[180:181], v[34:35] op_sel_hi:[0,1]
	v_pk_mul_f32 v[18:19], v[18:19], v[178:179]
	v_pk_mul_f32 v[20:21], v[20:21], v[180:181] op_sel_hi:[1,0]
	v_pk_mul_f32 v[16:17], v[16:17], s[66:67] op_sel_hi:[1,0]
	v_pk_mul_f32 v[34:35], v[34:35], v[162:163]
	v_pk_mul_f32 v[22:23], v[22:23], v[180:181] op_sel_hi:[1,0]
	v_pk_mul_f32 v[20:21], v[20:21], v[172:173]
	v_cvt_pk_bf16_f32 v162, v16, v17
	v_pk_mul_f32 v[16:17], v[18:19], s[66:67] op_sel_hi:[1,0]
	v_pk_mul_f32 v[28:29], v[28:29], v[180:181] op_sel_hi:[1,0]
	v_pk_mul_f32 v[24:25], v[24:25], v[180:181] op_sel_hi:[1,0]
	v_pk_mul_f32 v[22:23], v[22:23], v[174:175]
	v_cvt_pk_bf16_f32 v163, v16, v17
	v_pk_mul_f32 v[16:17], v[20:21], s[66:67] op_sel_hi:[1,0]
	v_pk_mul_f32 v[56:57], v[180:181], v[56:57] op_sel_hi:[0,1]
	v_pk_mul_f32 v[60:61], v[180:181], v[60:61] op_sel_hi:[0,1]
	v_pk_mul_f32 v[26:27], v[26:27], v[180:181] op_sel_hi:[1,0]
	v_pk_mul_f32 v[28:29], v[28:29], v[164:165]
	v_pk_mul_f32 v[24:25], v[24:25], v[168:169]
	v_cvt_pk_bf16_f32 v164, v16, v17
	v_pk_mul_f32 v[16:17], v[22:23], s[66:67] op_sel_hi:[1,0]
	v_pk_mul_f32 v[56:57], v[56:57], v[130:131]
	v_pk_mul_f32 v[60:61], v[60:61], v[134:135]
	v_pk_mul_f32 v[30:31], v[30:31], v[180:181] op_sel_hi:[1,0]
	v_pk_mul_f32 v[26:27], v[26:27], v[170:171]
	v_cvt_pk_bf16_f32 v165, v16, v17
	v_pk_mul_f32 v[16:17], v[24:25], s[66:67] op_sel_hi:[1,0]
	v_pk_mul_f32 v[130:131], v[56:57], v[4:5]
	v_pk_mul_f32 v[30:31], v[30:31], v[166:167]
	v_cvt_pk_bf16_f32 v166, v16, v17
	v_pk_mul_f32 v[16:17], v[26:27], s[66:67] op_sel_hi:[1,0]
	v_pk_mul_f32 v[4:5], v[60:61], v[4:5]
	v_pk_mul_f32 v[58:59], v[180:181], v[58:59] op_sel_hi:[0,1]
	v_pk_mul_f32 v[62:63], v[180:181], v[62:63] op_sel_hi:[0,1]
	v_pk_fma_f32 v[130:131], v[0:1], v[60:61], v[130:131]
	v_pk_mul_f32 v[32:33], v[180:181], v[32:33] op_sel_hi:[0,1]
	v_cvt_pk_bf16_f32 v167, v16, v17
	v_pk_mul_f32 v[16:17], v[28:29], s[66:67] op_sel_hi:[1,0]
	v_pk_fma_f32 v[0:1], v[56:57], v[0:1], v[4:5] neg_lo:[0,0,1] neg_hi:[0,0,1]
	v_pk_mul_f32 v[58:59], v[58:59], v[146:147]
	v_pk_mul_f32 v[62:63], v[62:63], v[148:149]
	v_pk_mul_f32 v[52:53], v[180:181], v[52:53] op_sel_hi:[0,1]
	v_pk_mul_f32 v[48:49], v[180:181], v[48:49] op_sel_hi:[0,1]
	v_pk_mul_f32 v[32:33], v[32:33], v[158:159]
	v_cvt_pk_bf16_f32 v168, v16, v17
	v_pk_mul_f32 v[16:17], v[30:31], s[66:67] op_sel_hi:[1,0]
	v_pk_mul_f32 v[0:1], v[0:1], s[66:67] op_sel_hi:[1,0]
	v_pk_mul_f32 v[54:55], v[180:181], v[54:55] op_sel_hi:[0,1]
	v_pk_mul_f32 v[50:51], v[180:181], v[50:51] op_sel_hi:[0,1]
	v_pk_mul_f32 v[52:53], v[52:53], v[136:137]
	v_pk_mul_f32 v[48:49], v[48:49], v[144:145]
	v_pk_mul_f32 v[46:47], v[180:181], v[46:47] op_sel_hi:[0,1]
	v_pk_mul_f32 v[42:43], v[180:181], v[42:43] op_sel_hi:[0,1]
	v_pk_mul_f32 v[44:45], v[180:181], v[44:45] op_sel_hi:[0,1]
	v_pk_mul_f32 v[40:41], v[180:181], v[40:41] op_sel_hi:[0,1]
	v_pk_mul_f32 v[38:39], v[180:181], v[38:39] op_sel_hi:[0,1]
	v_pk_mul_f32 v[36:37], v[180:181], v[36:37] op_sel_hi:[0,1]
	v_pk_mul_f32 v[136:137], v[58:59], v[6:7]
	v_cvt_pk_bf16_f32 v169, v16, v17
	v_pk_mul_f32 v[16:17], v[32:33], s[66:67] op_sel_hi:[1,0]
	v_cvt_pk_bf16_f32 v180, v0, v1
	v_pk_mul_f32 v[0:1], v[62:63], v[6:7]
	v_pk_mul_f32 v[54:55], v[54:55], v[132:133]
	v_pk_mul_f32 v[134:135], v[52:53], v[12:13]
	v_pk_mul_f32 v[36:37], v[36:37], v[154:155]
	v_pk_fma_f32 v[136:137], v[2:3], v[62:63], v[136:137]
	v_cvt_pk_bf16_f32 v170, v16, v17
	v_pk_mul_f32 v[16:17], v[34:35], s[66:67] op_sel_hi:[1,0]
	v_pk_mul_f32 v[12:13], v[48:49], v[12:13]
	v_pk_fma_f32 v[0:1], v[58:59], v[2:3], v[0:1] neg_lo:[0,0,1] neg_hi:[0,0,1]
	v_add_f32_e32 v2, v184, v185
	v_pk_mul_f32 v[50:51], v[50:51], v[138:139]
	v_pk_mul_f32 v[132:133], v[54:55], v[14:15]
	v_pk_fma_f32 v[134:135], v[8:9], v[48:49], v[134:135]
	v_pk_mul_f32 v[38:39], v[38:39], v[156:157]
	v_cvt_pk_bf16_f32 v171, v16, v17
	v_pk_mul_f32 v[16:17], v[36:37], s[66:67] op_sel_hi:[1,0]
	v_pk_fma_f32 v[8:9], v[52:53], v[8:9], v[12:13] neg_lo:[0,0,1] neg_hi:[0,0,1]
	v_pk_mul_f32 v[0:1], v[0:1], s[66:67] op_sel_hi:[1,0]
	v_fmamk_f32 v2, v2, 0x3c2aaaab, v240
	v_pk_fma_f32 v[132:133], v[10:11], v[50:51], v[132:133]
	v_pk_mul_f32 v[40:41], v[40:41], v[150:151]
	v_cvt_pk_bf16_f32 v172, v16, v17
	v_pk_mul_f32 v[16:17], v[38:39], s[66:67] op_sel_hi:[1,0]
	v_pk_mul_f32 v[8:9], v[8:9], s[66:67] op_sel_hi:[1,0]
	v_cvt_pk_bf16_f32 v181, v0, v1
	v_pk_mul_f32 v[0:1], v[134:135], s[66:67] op_sel_hi:[1,0]
	v_rsq_f32_e32 v2, v2
	v_pk_mul_f32 v[42:43], v[42:43], v[152:153]
	v_cvt_pk_bf16_f32 v173, v16, v17
	v_pk_mul_f32 v[16:17], v[40:41], s[66:67] op_sel_hi:[1,0]
	v_cvt_pk_bf16_f32 v178, v8, v9
	v_pk_mul_f32 v[8:9], v[50:51], v[14:15]
	v_cvt_pk_bf16_f32 v182, v0, v1
	v_pk_mul_f32 v[0:1], v[132:133], s[66:67] op_sel_hi:[1,0]
	v_pk_mul_f32 v[44:45], v[44:45], v[140:141]
	v_cvt_pk_bf16_f32 v174, v16, v17
	v_pk_mul_f32 v[16:17], v[42:43], s[66:67] op_sel_hi:[1,0]
	v_pk_fma_f32 v[8:9], v[54:55], v[10:11], v[8:9] neg_lo:[0,0,1] neg_hi:[0,0,1]
	v_cvt_pk_bf16_f32 v183, v0, v1
	v_pk_mul_f32 v[0:1], v[130:131], s[66:67] op_sel_hi:[1,0]
	v_pk_mul_f32 v[46:47], v[46:47], v[142:143]
	v_cvt_pk_bf16_f32 v175, v16, v17
	v_pk_mul_f32 v[16:17], v[44:45], s[66:67] op_sel_hi:[1,0]
	v_pk_mul_f32 v[8:9], v[8:9], s[66:67] op_sel_hi:[1,0]
	v_cvt_pk_bf16_f32 v184, v0, v1
	v_pk_mul_f32 v[0:1], v[136:137], s[66:67] op_sel_hi:[1,0]
	v_cvt_pk_bf16_f32 v176, v16, v17
	v_pk_mul_f32 v[16:17], v[46:47], s[66:67] op_sel_hi:[1,0]
	v_cvt_pk_bf16_f32 v179, v8, v9
	v_cvt_pk_bf16_f32 v185, v0, v1
	s_waitcnt vmcnt(0)
	v_pk_mul_f32 v[0:1], v[2:3], v[122:123] op_sel_hi:[0,1]
	v_pk_mul_f32 v[4:5], v[2:3], v[126:127] op_sel_hi:[0,1]
	v_pk_mul_f32 v[6:7], v[2:3], v[120:121] op_sel_hi:[0,1]
	v_pk_mul_f32 v[8:9], v[2:3], v[124:125] op_sel_hi:[0,1]
	v_pk_mul_f32 v[12:13], v[2:3], v[118:119] op_sel_hi:[0,1]
	v_pk_mul_f32 v[14:15], v[2:3], v[114:115] op_sel_hi:[0,1]
	v_pk_mul_f32 v[18:19], v[2:3], v[116:117] op_sel_hi:[0,1]
	v_pk_mul_f32 v[20:21], v[2:3], v[112:113] op_sel_hi:[0,1]
	v_pk_mul_f32 v[24:25], v[2:3], v[110:111] op_sel_hi:[0,1]
	v_pk_mul_f32 v[26:27], v[2:3], v[106:107] op_sel_hi:[0,1]
	v_pk_mul_f32 v[28:29], v[2:3], v[108:109] op_sel_hi:[0,1]
	v_pk_mul_f32 v[30:31], v[2:3], v[104:105] op_sel_hi:[0,1]
	v_pk_mul_f32 v[32:33], v[2:3], v[102:103] op_sel_hi:[0,1]
	v_pk_mul_f32 v[34:35], v[2:3], v[98:99] op_sel_hi:[0,1]
	v_pk_mul_f32 v[36:37], v[2:3], v[100:101] op_sel_hi:[0,1]
	v_pk_mul_f32 v[38:39], v[2:3], v[96:97] op_sel_hi:[0,1]
	v_pk_mul_f32 v[40:41], v[94:95], v[2:3] op_sel_hi:[1,0]
	v_pk_mul_f32 v[42:43], v[90:91], v[2:3] op_sel_hi:[1,0]
	v_pk_mul_f32 v[44:45], v[92:93], v[2:3] op_sel_hi:[1,0]
	v_pk_mul_f32 v[46:47], v[88:89], v[2:3] op_sel_hi:[1,0]
	v_pk_mul_f32 v[48:49], v[82:83], v[2:3] op_sel_hi:[1,0]
	v_pk_mul_f32 v[50:51], v[78:79], v[2:3] op_sel_hi:[1,0]
	v_pk_mul_f32 v[52:53], v[80:81], v[2:3] op_sel_hi:[1,0]
	v_pk_mul_f32 v[2:3], v[76:77], v[2:3] op_sel_hi:[1,0]
	v_pk_mul_f32 v[50:51], v[50:51], v[238:239]
	v_pk_mul_f32 v[2:3], v[2:3], v[236:237]
	v_pk_mul_f32 v[4:5], v[4:5], v[186:187]
	v_pk_mul_f32 v[2:3], v[2:3], s[66:67] op_sel_hi:[1,0]
	v_pk_mul_f32 v[52:53], v[52:53], v[232:233]
	v_cvt_pk_bf16_f32 v186, v2, v3
	v_pk_mul_f32 v[2:3], v[50:51], s[66:67] op_sel_hi:[1,0]
	v_pk_mul_f32 v[48:49], v[48:49], v[234:235]
	v_cvt_pk_bf16_f32 v187, v2, v3
	v_pk_mul_f32 v[2:3], v[52:53], s[66:67] op_sel_hi:[1,0]
	v_pk_mul_f32 v[0:1], v[0:1], v[188:189]
	v_pk_mul_f32 v[46:47], v[46:47], v[222:223]
	v_cvt_pk_bf16_f32 v188, v2, v3
	v_pk_mul_f32 v[2:3], v[48:49], s[66:67] op_sel_hi:[1,0]
	v_pk_mul_f32 v[42:43], v[42:43], v[224:225]
	v_cvt_pk_bf16_f32 v189, v2, v3
	v_pk_mul_f32 v[2:3], v[46:47], s[66:67] op_sel_hi:[1,0]
	v_pk_mul_f32 v[8:9], v[8:9], v[190:191]
	v_pk_mul_f32 v[44:45], v[44:45], v[218:219]
	v_cvt_pk_bf16_f32 v190, v2, v3
	v_pk_mul_f32 v[2:3], v[42:43], s[66:67] op_sel_hi:[1,0]
	v_pk_mul_f32 v[40:41], v[40:41], v[220:221]
	v_cvt_pk_bf16_f32 v191, v2, v3
	v_pk_mul_f32 v[2:3], v[44:45], s[66:67] op_sel_hi:[1,0]
	v_pk_mul_f32 v[6:7], v[6:7], v[192:193]
	v_pk_mul_f32 v[38:39], v[38:39], v[214:215]
	v_cvt_pk_bf16_f32 v192, v2, v3
	v_pk_mul_f32 v[2:3], v[40:41], s[66:67] op_sel_hi:[1,0]
	v_pk_mul_f32 v[34:35], v[34:35], v[216:217]
	v_cvt_pk_bf16_f32 v193, v2, v3
	v_pk_mul_f32 v[2:3], v[38:39], s[66:67] op_sel_hi:[1,0]
	v_pk_mul_f32 v[14:15], v[14:15], v[194:195]
	v_pk_mul_f32 v[36:37], v[36:37], v[210:211]
	v_cvt_pk_bf16_f32 v194, v2, v3
	v_pk_mul_f32 v[2:3], v[34:35], s[66:67] op_sel_hi:[1,0]
	v_pk_mul_f32 v[32:33], v[32:33], v[212:213]
	v_cvt_pk_bf16_f32 v195, v2, v3
	v_pk_mul_f32 v[2:3], v[36:37], s[66:67] op_sel_hi:[1,0]
	v_pk_mul_f32 v[12:13], v[12:13], v[196:197]
	v_pk_mul_f32 v[30:31], v[30:31], v[206:207]
	v_cvt_pk_bf16_f32 v196, v2, v3
	v_pk_mul_f32 v[2:3], v[32:33], s[66:67] op_sel_hi:[1,0]
	v_pk_mul_f32 v[26:27], v[26:27], v[208:209]
	v_cvt_pk_bf16_f32 v197, v2, v3
	v_pk_mul_f32 v[2:3], v[30:31], s[66:67] op_sel_hi:[1,0]
	v_pk_mul_f32 v[20:21], v[20:21], v[198:199]
	v_pk_mul_f32 v[28:29], v[28:29], v[202:203]
	v_cvt_pk_bf16_f32 v198, v2, v3
	v_pk_mul_f32 v[2:3], v[26:27], s[66:67] op_sel_hi:[1,0]
	v_pk_mul_f32 v[24:25], v[24:25], v[204:205]
	v_cvt_pk_bf16_f32 v199, v2, v3
	v_pk_mul_f32 v[2:3], v[28:29], s[66:67] op_sel_hi:[1,0]
	v_pk_mul_f32 v[18:19], v[18:19], v[200:201]
	v_cvt_pk_bf16_f32 v200, v2, v3
	v_pk_mul_f32 v[2:3], v[24:25], s[66:67] op_sel_hi:[1,0]
	v_pk_mul_f32 v[22:23], v[18:19], v[84:85]
	v_cvt_pk_bf16_f32 v201, v2, v3
	v_pk_mul_f32 v[2:3], v[20:21], v[84:85]
	v_pk_mul_f32 v[54:55], v[0:1], v[74:75]
	v_pk_fma_f32 v[2:3], v[18:19], v[68:69], v[2:3] neg_lo:[0,0,1] neg_hi:[0,0,1]
	v_cvt_pk_bf16_f32 v177, v16, v17
	v_pk_mul_f32 v[2:3], v[2:3], s[66:67] op_sel_hi:[1,0]
	v_pk_mul_f32 v[16:17], v[12:13], v[86:87]
	v_cvt_pk_bf16_f32 v202, v2, v3
	v_pk_mul_f32 v[2:3], v[14:15], v[86:87]
	v_pk_fma_f32 v[22:23], v[68:69], v[20:21], v[22:23]
	v_pk_fma_f32 v[2:3], v[12:13], v[70:71], v[2:3] neg_lo:[0,0,1] neg_hi:[0,0,1]
	v_pk_mul_f32 v[10:11], v[6:7], v[72:73]
	v_pk_mul_f32 v[2:3], v[2:3], s[66:67] op_sel_hi:[1,0]
	v_pk_fma_f32 v[16:17], v[70:71], v[14:15], v[16:17]
	v_cvt_pk_bf16_f32 v203, v2, v3
	v_pk_mul_f32 v[2:3], v[8:9], v[72:73]
	v_pk_fma_f32 v[10:11], v[64:65], v[8:9], v[10:11]
	v_pk_fma_f32 v[2:3], v[6:7], v[64:65], v[2:3] neg_lo:[0,0,1] neg_hi:[0,0,1]
	v_pk_fma_f32 v[54:55], v[66:67], v[4:5], v[54:55]
	v_pk_mul_f32 v[2:3], v[2:3], s[66:67] op_sel_hi:[1,0]
	s_mul_i32 s74, s2, 0x700000
	v_cvt_pk_bf16_f32 v204, v2, v3
	v_pk_mul_f32 v[2:3], v[4:5], v[74:75]
	v_lshrrev_b32_e32 v4, 1, v226
	v_pk_fma_f32 v[0:1], v[0:1], v[66:67], v[2:3] neg_lo:[0,0,1] neg_hi:[0,0,1]
	v_lshrrev_b32_e32 v2, 2, v226
	v_pk_mul_f32 v[0:1], v[0:1], s[66:67] op_sel_hi:[1,0]
	v_lshlrev_b32_e32 v3, 2, v227
	v_cvt_pk_bf16_f32 v205, v0, v1
	v_pk_mul_f32 v[0:1], v[22:23], s[66:67] op_sel_hi:[1,0]
	v_and_b32_e32 v4, 8, v4
	v_cvt_pk_bf16_f32 v206, v0, v1
	v_pk_mul_f32 v[0:1], v[16:17], s[66:67] op_sel_hi:[1,0]
	v_and_b32_e32 v3, 4, v3
	v_cvt_pk_bf16_f32 v207, v0, v1
	v_pk_mul_f32 v[0:1], v[10:11], s[66:67] op_sel_hi:[1,0]
	v_and_or_b32 v2, v2, 3, v4
	v_cvt_pk_bf16_f32 v208, v0, v1
	v_pk_mul_f32 v[0:1], v[54:55], s[66:67] op_sel_hi:[1,0]
	s_mul_hi_i32 s22, s2, 0x700000
	v_cvt_pk_bf16_f32 v209, v0, v1
	v_lshlrev_b32_e32 v0, 3, v227
	v_and_b32_e32 v0, 48, v0
	s_add_u32 s2, s6, s74
	v_lshlrev_b32_e32 v1, 3, v231
	v_or3_b32 v0, v2, v0, v3
	s_mul_i32 s75, s3, 0xc0
	s_addc_u32 s3, s7, s22
	s_lshl_b32 s86, s80, 8
	v_and_b32_e32 v5, 24, v1
	v_mul_u32_u24_e32 v0, 0x700, v0
	s_add_u32 s2, s2, s86
	v_or3_b32 v0, v0, v128, v5
	v_and_b32_e32 v8, 0x100, v1
	v_mov_b32_e32 v1, v161
	s_addc_u32 s3, s3, 0
	v_lshlrev_b32_e32 v2, 4, v231
	v_lshlrev_b32_e32 v3, 1, v231
	v_lshlrev_b64 v[0:1], 1, v[0:1]
	v_and_b32_e32 v6, 32, v3
	v_and_b32_e32 v7, 0xc0, v2
	v_lshl_add_u64 v[2:3], s[2:3], 0, v[0:1]
	s_mov_b64 s[2:3], 0x680
	s_mov_b32 m0, s81
	v_lshl_add_u64 v[2:3], v[2:3], 0, s[2:3]
	global_load_lds_dwordx4 v[2:3], off
	v_and_or_b32 v2, v226, 7, v4
	v_lshlrev_b32_e32 v2, 4, v2
	s_movk_i32 s2, 0x60
	v_bitop3_b32 v239, v230, v2, s2 bitop3:0x36
	s_movk_i32 s2, 0x80
	v_bitop3_b32 v247, v230, v2, s2 bitop3:0x36
	s_movk_i32 s2, 0xa0
	v_bitop3_b32 v249, v230, v2, s2 bitop3:0x36
	s_add_u32 s2, s45, s75
	s_addc_u32 s3, s44, 0
	s_add_u32 s2, s31, s2
	s_addc_u32 s3, s58, s3
	v_lshl_add_u64 v[232:233], v[160:161], 1, s[2:3]
	v_add_lshl_u32 v160, v229, v129, 1
	v_lshl_add_u64 v[234:235], s[2:3], 0, v[160:161]
	s_or_b32 s2, s74, s23
	s_waitcnt vmcnt(0)
	s_add_u32 s2, s59, s2
	v_xor_b32_e32 v226, v2, v230
	v_bitop3_b32 v227, v230, v2, 32 bitop3:0x36
	v_bitop3_b32 v238, v230, v2, 64 bitop3:0x36
	v_add3_u32 v2, v7, 0, v5
	s_addc_u32 s3, s78, s22
	v_mov_b32_e32 v229, 0
	v_add3_u32 v228, v2, v6, v8
	v_lshl_add_u64 v[236:237], s[2:3], 0, v[0:1]
	s_mov_b32 s22, 0
	s_mov_b64 s[74:75], 0
	v_mov_b32_e32 v160, 0
	v_mov_b32_e32 v32, 0
	v_mov_b32_e32 v33, v229
	v_mov_b32_e32 v34, v229
	v_mov_b32_e32 v35, v229
	v_mov_b32_e32 v36, v229
	v_mov_b32_e32 v37, v229
	v_mov_b32_e32 v38, v229
	v_mov_b32_e32 v39, v229
	v_mov_b32_e32 v40, v229
	v_mov_b32_e32 v41, v229
	v_mov_b32_e32 v42, v229
	v_mov_b32_e32 v43, v229
	v_mov_b32_e32 v44, v229
	v_mov_b32_e32 v45, v229
	v_mov_b32_e32 v46, v229
	v_mov_b32_e32 v47, v229
	v_mov_b32_e32 v48, 0
	v_mov_b32_e32 v49, v229
	v_mov_b32_e32 v50, v229
	v_mov_b32_e32 v51, v229
	v_mov_b32_e32 v52, v229
	v_mov_b32_e32 v53, v229
	v_mov_b32_e32 v54, v229
	v_mov_b32_e32 v55, v229
	v_mov_b32_e32 v56, v229
	v_mov_b32_e32 v57, v229
	v_mov_b32_e32 v58, v229
	v_mov_b32_e32 v59, v229
	v_mov_b32_e32 v60, v229
	v_mov_b32_e32 v61, v229
	v_mov_b32_e32 v62, v229
	v_mov_b32_e32 v63, v229
	v_mov_b32_e32 v0, 0
	v_mov_b32_e32 v1, v229
	v_mov_b32_e32 v2, v229
	v_mov_b32_e32 v3, v229
	v_mov_b32_e32 v4, v229
	v_mov_b32_e32 v5, v229
	v_mov_b32_e32 v6, v229
	v_mov_b32_e32 v7, v229
	v_mov_b32_e32 v8, v229
	v_mov_b32_e32 v9, v229
	v_mov_b32_e32 v10, v229
	v_mov_b32_e32 v11, v229
	v_mov_b32_e32 v12, v229
	v_mov_b32_e32 v13, v229
	v_mov_b32_e32 v14, v229
	v_mov_b32_e32 v15, v229
	v_mov_b32_e32 v16, 0
	v_mov_b32_e32 v17, v229
	v_mov_b32_e32 v18, v229
	v_mov_b32_e32 v19, v229
	v_mov_b32_e32 v20, v229
	v_mov_b32_e32 v21, v229
	v_mov_b32_e32 v22, v229
	v_mov_b32_e32 v23, v229
	v_mov_b32_e32 v24, v229
	v_mov_b32_e32 v25, v229
	v_mov_b32_e32 v26, v229
	v_mov_b32_e32 v27, v229
	v_mov_b32_e32 v28, v229
	v_mov_b32_e32 v29, v229
	v_mov_b32_e32 v30, v229
	v_mov_b32_e32 v31, v229
	s_waitcnt vmcnt(0) lgkmcnt(0)
	s_barrier
	s_branch .LBB0_602
	.p2align 6

.LBB0_630:
	s_or_b64 exec, exec, s[2:3]
	v_add_f32_e32 v164, v164, v165
	v_fmamk_f32 v164, v164, 0x3c800000, v240
	v_rsq_f32_e32 v164, v164
	s_lshr_b32 s2, s22, 2
	s_and_b32 s2, s2, 4
	s_lshl_b32 s58, s2, 5
	v_pk_mul_f32 v[40:41], v[164:165], v[40:41] op_sel_hi:[0,1]
	v_pk_mul_f32 v[44:45], v[164:165], v[44:45] op_sel_hi:[0,1]
	v_pk_mul_f32 v[20:21], v[20:21], v[164:165] op_sel_hi:[1,0]
	v_pk_mul_f32 v[42:43], v[164:165], v[42:43] op_sel_hi:[0,1]
	v_pk_mul_f32 v[40:41], v[40:41], v[134:135]
	v_pk_mul_f32 v[44:45], v[44:45], v[138:139]
	v_pk_mul_f32 v[34:35], v[164:165], v[34:35] op_sel_hi:[0,1]
	v_pk_mul_f32 v[20:21], v[20:21], v[156:157]
	v_pk_mul_f32 v[16:17], v[16:17], v[164:165] op_sel_hi:[1,0]
	v_pk_mul_f32 v[42:43], v[42:43], v[130:131]
	v_pk_mul_f32 v[130:131], v[40:41], v[4:5]
	v_pk_mul_f32 v[34:35], v[34:35], v[142:143]
	v_pk_mul_f32 v[16:17], v[16:17], v[162:163]
	v_pk_mul_f32 v[142:143], v[20:21], v[60:61]
	v_pk_mul_f32 v[4:5], v[44:45], v[4:5]
	v_pk_mul_f32 v[46:47], v[164:165], v[46:47] op_sel_hi:[0,1]
	v_pk_fma_f32 v[130:131], v[44:45], v[0:1], v[130:131]
	v_pk_fma_f32 v[142:143], v[16:17], v[56:57], v[142:143]
	v_pk_mul_f32 v[16:17], v[16:17], v[60:61]
	v_pk_fma_f32 v[0:1], v[40:41], v[0:1], v[4:5] neg_lo:[0,0,1] neg_hi:[0,0,1]
	v_pk_mul_f32 v[46:47], v[46:47], v[132:133]
	v_pk_mul_f32 v[26:27], v[26:27], v[164:165] op_sel_hi:[1,0]
	v_pk_mul_f32 v[18:19], v[18:19], v[164:165] op_sel_hi:[1,0]
	v_pk_fma_f32 v[16:17], v[20:21], v[56:57], v[16:17] neg_lo:[0,0,1] neg_hi:[0,0,1]
	v_pk_mul_f32 v[0:1], v[0:1], s[62:63] op_sel_hi:[1,0]
	v_pk_mul_f32 v[36:37], v[164:165], v[36:37] op_sel_hi:[0,1]
	v_pk_mul_f32 v[32:33], v[164:165], v[32:33] op_sel_hi:[0,1]
	v_pk_mul_f32 v[26:27], v[26:27], v[144:145]
	v_pk_mul_f32 v[22:23], v[22:23], v[164:165] op_sel_hi:[1,0]
	v_pk_mul_f32 v[18:19], v[18:19], v[158:159]
	v_pk_mul_f32 v[144:145], v[42:43], v[6:7]
	v_pk_mul_f32 v[16:17], v[16:17], s[62:63] op_sel_hi:[1,0]
	v_cvt_pk_bf16_f32 v172, v0, v1
	v_pk_mul_f32 v[0:1], v[46:47], v[6:7]
	v_pk_mul_f32 v[38:39], v[164:165], v[38:39] op_sel_hi:[0,1]
	v_pk_mul_f32 v[36:37], v[36:37], v[140:141]
	v_pk_mul_f32 v[32:33], v[32:33], v[146:147]
	v_pk_mul_f32 v[22:23], v[22:23], v[152:153]
	v_pk_fma_f32 v[144:145], v[46:47], v[2:3], v[144:145]
	v_cvt_pk_bf16_f32 v162, v16, v17
	v_pk_mul_f32 v[16:17], v[18:19], v[62:63]
	v_pk_fma_f32 v[0:1], v[42:43], v[2:3], v[0:1] neg_lo:[0,0,1] neg_hi:[0,0,1]
	v_add_f32_e32 v2, v176, v177
	v_pk_mul_f32 v[38:39], v[38:39], v[136:137]
	v_pk_mul_f32 v[134:135], v[36:37], v[12:13]
	v_pk_mul_f32 v[28:29], v[28:29], v[164:165] op_sel_hi:[1,0]
	v_pk_fma_f32 v[16:17], v[22:23], v[58:59], v[16:17] neg_lo:[0,0,1] neg_hi:[0,0,1]
	v_pk_mul_f32 v[12:13], v[32:33], v[12:13]
	v_fmamk_f32 v2, v2, 0x3c800000, v240
	v_pk_mul_f32 v[132:133], v[38:39], v[14:15]
	v_pk_fma_f32 v[134:135], v[32:33], v[8:9], v[134:135]
	v_pk_mul_f32 v[24:25], v[24:25], v[164:165] op_sel_hi:[1,0]
	v_pk_mul_f32 v[28:29], v[28:29], v[154:155]
	v_pk_mul_f32 v[16:17], v[16:17], s[62:63] op_sel_hi:[1,0]
	v_pk_fma_f32 v[8:9], v[36:37], v[8:9], v[12:13] neg_lo:[0,0,1] neg_hi:[0,0,1]
	v_pk_mul_f32 v[0:1], v[0:1], s[62:63] op_sel_hi:[1,0]
	v_rsq_f32_e32 v2, v2
	v_pk_fma_f32 v[132:133], v[34:35], v[10:11], v[132:133]
	v_pk_mul_f32 v[24:25], v[24:25], v[148:149]
	v_cvt_pk_bf16_f32 v163, v16, v17
	v_pk_mul_f32 v[16:17], v[28:29], v[52:53]
	v_pk_mul_f32 v[8:9], v[8:9], s[62:63] op_sel_hi:[1,0]
	v_cvt_pk_bf16_f32 v173, v0, v1
	v_pk_mul_f32 v[0:1], v[134:135], s[62:63] op_sel_hi:[1,0]
	v_pk_mul_f32 v[30:31], v[30:31], v[164:165] op_sel_hi:[1,0]
	v_pk_fma_f32 v[16:17], v[24:25], v[48:49], v[16:17] neg_lo:[0,0,1] neg_hi:[0,0,1]
	v_cvt_pk_bf16_f32 v170, v8, v9
	v_pk_mul_f32 v[8:9], v[34:35], v[14:15]
	v_cvt_pk_bf16_f32 v174, v0, v1
	v_pk_mul_f32 v[0:1], v[132:133], s[62:63] op_sel_hi:[1,0]
	v_pk_mul_f32 v[30:31], v[30:31], v[150:151]
	v_pk_mul_f32 v[16:17], v[16:17], s[62:63] op_sel_hi:[1,0]
	v_pk_fma_f32 v[8:9], v[38:39], v[10:11], v[8:9] neg_lo:[0,0,1] neg_hi:[0,0,1]
	v_cvt_pk_bf16_f32 v175, v0, v1
	v_pk_mul_f32 v[0:1], v[130:131], s[62:63] op_sel_hi:[1,0]
	v_pk_mul_f32 v[136:137], v[26:27], v[54:55]
	v_pk_mul_f32 v[140:141], v[22:23], v[62:63]
	v_cvt_pk_bf16_f32 v164, v16, v17
	v_pk_mul_f32 v[16:17], v[30:31], v[54:55]
	v_pk_mul_f32 v[8:9], v[8:9], s[62:63] op_sel_hi:[1,0]
	v_cvt_pk_bf16_f32 v176, v0, v1
	v_pk_mul_f32 v[0:1], v[144:145], s[62:63] op_sel_hi:[1,0]
	s_waitcnt vmcnt(0)
	v_pk_mul_f32 v[42:43], v[84:85], v[2:3] op_sel_hi:[1,0]
	v_pk_fma_f32 v[136:137], v[30:31], v[50:51], v[136:137]
	v_pk_mul_f32 v[138:139], v[24:25], v[52:53]
	v_pk_fma_f32 v[140:141], v[18:19], v[58:59], v[140:141]
	v_pk_fma_f32 v[16:17], v[26:27], v[50:51], v[16:17] neg_lo:[0,0,1] neg_hi:[0,0,1]
	v_cvt_pk_bf16_f32 v171, v8, v9
	v_cvt_pk_bf16_f32 v177, v0, v1
	v_pk_mul_f32 v[0:1], v[2:3], v[122:123] op_sel_hi:[0,1]
	v_pk_mul_f32 v[4:5], v[2:3], v[126:127] op_sel_hi:[0,1]
	v_pk_mul_f32 v[6:7], v[2:3], v[120:121] op_sel_hi:[0,1]
	v_pk_mul_f32 v[8:9], v[2:3], v[124:125] op_sel_hi:[0,1]
	v_pk_mul_f32 v[12:13], v[2:3], v[118:119] op_sel_hi:[0,1]
	v_pk_mul_f32 v[14:15], v[2:3], v[114:115] op_sel_hi:[0,1]
	v_pk_mul_f32 v[18:19], v[2:3], v[116:117] op_sel_hi:[0,1]
	v_pk_mul_f32 v[20:21], v[2:3], v[112:113] op_sel_hi:[0,1]
	v_pk_mul_f32 v[24:25], v[102:103], v[2:3] op_sel_hi:[1,0]
	v_pk_mul_f32 v[26:27], v[106:107], v[2:3] op_sel_hi:[1,0]
	v_pk_mul_f32 v[30:31], v[100:101], v[2:3] op_sel_hi:[1,0]
	v_pk_mul_f32 v[32:33], v[104:105], v[2:3] op_sel_hi:[1,0]
	v_pk_mul_f32 v[36:37], v[86:87], v[2:3] op_sel_hi:[1,0]
	v_pk_mul_f32 v[38:39], v[82:83], v[2:3] op_sel_hi:[1,0]
	v_pk_mul_f32 v[42:43], v[42:43], v[204:205]
	v_pk_mul_f32 v[2:3], v[80:81], v[2:3] op_sel_hi:[1,0]
	v_pk_mul_f32 v[44:45], v[42:43], v[108:109]
	v_pk_mul_f32 v[2:3], v[2:3], v[208:209]
	v_pk_mul_f32 v[38:39], v[38:39], v[206:207]
	v_pk_fma_f32 v[44:45], v[2:3], v[72:73], v[44:45]
	v_pk_mul_f32 v[2:3], v[2:3], v[108:109]
	v_pk_mul_f32 v[4:5], v[4:5], v[178:179]
	v_pk_fma_f32 v[2:3], v[42:43], v[72:73], v[2:3] neg_lo:[0,0,1] neg_hi:[0,0,1]
	v_pk_mul_f32 v[36:37], v[36:37], v[200:201]
	v_pk_mul_f32 v[2:3], v[2:3], s[62:63] op_sel_hi:[1,0]
	v_pk_mul_f32 v[32:33], v[32:33], v[202:203]
	v_cvt_pk_bf16_f32 v178, v2, v3
	v_pk_mul_f32 v[2:3], v[38:39], v[110:111]
	v_pk_mul_f32 v[30:31], v[30:31], v[196:197]
	v_pk_fma_f32 v[2:3], v[36:37], v[74:75], v[2:3] neg_lo:[0,0,1] neg_hi:[0,0,1]
	v_pk_mul_f32 v[26:27], v[26:27], v[198:199]
	v_pk_mul_f32 v[2:3], v[2:3], s[62:63] op_sel_hi:[1,0]
	v_pk_mul_f32 v[0:1], v[0:1], v[180:181]
	v_cvt_pk_bf16_f32 v179, v2, v3
	v_pk_mul_f32 v[2:3], v[32:33], v[92:93]
	v_pk_mul_f32 v[24:25], v[24:25], v[190:191]
	v_pk_fma_f32 v[2:3], v[30:31], v[64:65], v[2:3] neg_lo:[0,0,1] neg_hi:[0,0,1]
	v_pk_mul_f32 v[40:41], v[36:37], v[110:111]
	v_pk_mul_f32 v[2:3], v[2:3], s[62:63] op_sel_hi:[1,0]
	v_pk_mul_f32 v[34:35], v[30:31], v[92:93]
	v_cvt_pk_bf16_f32 v180, v2, v3
	v_pk_mul_f32 v[2:3], v[26:27], v[94:95]
	v_pk_fma_f32 v[40:41], v[38:39], v[74:75], v[40:41]
	v_pk_fma_f32 v[2:3], v[24:25], v[66:67], v[2:3] neg_lo:[0,0,1] neg_hi:[0,0,1]
	v_pk_fma_f32 v[138:139], v[28:29], v[48:49], v[138:139]
	v_pk_mul_f32 v[2:3], v[2:3], s[62:63] op_sel_hi:[1,0]
	v_pk_mul_f32 v[8:9], v[8:9], v[182:183]
	v_cvt_pk_bf16_f32 v181, v2, v3
	v_pk_mul_f32 v[2:3], v[44:45], s[62:63] op_sel_hi:[1,0]
	v_pk_mul_f32 v[28:29], v[24:25], v[94:95]
	v_pk_fma_f32 v[34:35], v[32:33], v[64:65], v[34:35]
	v_cvt_pk_bf16_f32 v182, v2, v3
	v_pk_mul_f32 v[2:3], v[40:41], s[62:63] op_sel_hi:[1,0]
	v_pk_fma_f32 v[28:29], v[26:27], v[66:67], v[28:29]
	v_cvt_pk_bf16_f32 v183, v2, v3
	v_pk_mul_f32 v[2:3], v[34:35], s[62:63] op_sel_hi:[1,0]
	v_pk_mul_f32 v[6:7], v[6:7], v[184:185]
	v_pk_mul_f32 v[20:21], v[20:21], v[192:193]
	v_cvt_pk_bf16_f32 v184, v2, v3
	v_pk_mul_f32 v[2:3], v[28:29], s[62:63] op_sel_hi:[1,0]
	v_pk_mul_f32 v[18:19], v[18:19], v[194:195]
	v_cvt_pk_bf16_f32 v185, v2, v3
	v_pk_mul_f32 v[2:3], v[20:21], v[96:97]
	v_pk_mul_f32 v[14:15], v[14:15], v[186:187]
	v_pk_fma_f32 v[2:3], v[18:19], v[88:89], v[2:3] neg_lo:[0,0,1] neg_hi:[0,0,1]
	v_pk_mul_f32 v[12:13], v[12:13], v[188:189]
	v_pk_mul_f32 v[2:3], v[2:3], s[62:63] op_sel_hi:[1,0]
	v_pk_mul_f32 v[16:17], v[16:17], s[62:63] op_sel_hi:[1,0]
	v_cvt_pk_bf16_f32 v186, v2, v3
	v_pk_mul_f32 v[2:3], v[14:15], v[98:99]
	v_cvt_pk_bf16_f32 v165, v16, v17
	v_pk_fma_f32 v[2:3], v[12:13], v[90:91], v[2:3] neg_lo:[0,0,1] neg_hi:[0,0,1]
	v_pk_mul_f32 v[16:17], v[142:143], s[62:63] op_sel_hi:[1,0]
	v_pk_mul_f32 v[2:3], v[2:3], s[62:63] op_sel_hi:[1,0]
	v_cvt_pk_bf16_f32 v166, v16, v17
	v_cvt_pk_bf16_f32 v187, v2, v3
	v_pk_mul_f32 v[2:3], v[8:9], v[76:77]
	v_pk_mul_f32 v[16:17], v[140:141], s[62:63] op_sel_hi:[1,0]
	v_pk_fma_f32 v[2:3], v[6:7], v[68:69], v[2:3] neg_lo:[0,0,1] neg_hi:[0,0,1]
	v_cvt_pk_bf16_f32 v167, v16, v17
	v_pk_mul_f32 v[2:3], v[2:3], s[62:63] op_sel_hi:[1,0]
	v_pk_mul_f32 v[16:17], v[138:139], s[62:63] op_sel_hi:[1,0]
	v_cvt_pk_bf16_f32 v188, v2, v3
	v_pk_mul_f32 v[2:3], v[4:5], v[78:79]
	v_cvt_pk_bf16_f32 v168, v16, v17
	v_pk_mul_f32 v[16:17], v[136:137], s[62:63] op_sel_hi:[1,0]
	v_pk_mul_f32 v[22:23], v[18:19], v[96:97]
	v_pk_mul_f32 v[46:47], v[0:1], v[78:79]
	v_pk_fma_f32 v[0:1], v[0:1], v[70:71], v[2:3] neg_lo:[0,0,1] neg_hi:[0,0,1]
	v_cvt_pk_bf16_f32 v169, v16, v17
	v_pk_mul_f32 v[16:17], v[12:13], v[98:99]
	v_pk_fma_f32 v[22:23], v[20:21], v[88:89], v[22:23]
	v_pk_mul_f32 v[0:1], v[0:1], s[62:63] op_sel_hi:[1,0]
	v_pk_mul_f32 v[10:11], v[6:7], v[76:77]
	v_pk_fma_f32 v[16:17], v[14:15], v[90:91], v[16:17]
	v_cvt_pk_bf16_f32 v189, v0, v1
	v_pk_mul_f32 v[0:1], v[22:23], s[62:63] op_sel_hi:[1,0]
	v_pk_fma_f32 v[10:11], v[8:9], v[68:69], v[10:11]
	v_cvt_pk_bf16_f32 v190, v0, v1
	v_pk_mul_f32 v[0:1], v[16:17], s[62:63] op_sel_hi:[1,0]
	v_pk_fma_f32 v[46:47], v[4:5], v[70:71], v[46:47]
	v_cvt_pk_bf16_f32 v191, v0, v1
	v_pk_mul_f32 v[0:1], v[10:11], s[62:63] op_sel_hi:[1,0]
	v_lshrrev_b32_e32 v4, 1, v212
	v_cvt_pk_bf16_f32 v192, v0, v1
	v_pk_mul_f32 v[0:1], v[46:47], s[62:63] op_sel_hi:[1,0]
	v_lshrrev_b32_e32 v2, 2, v212
	v_cvt_pk_bf16_f32 v193, v0, v1
	v_lshlrev_b32_e32 v0, 3, v213
	v_lshlrev_b32_e32 v3, 2, v213
	v_and_b32_e32 v4, 8, v4
	v_and_b32_e32 v0, 48, v0
	v_and_b32_e32 v3, 4, v3
	v_and_or_b32 v2, v2, 3, v4
	v_lshlrev_b32_e32 v1, 3, v211
	v_or3_b32 v0, v2, v0, v3
	s_lshl_b32 s2, s59, 1
	v_and_b32_e32 v5, 24, v1
	v_mul_u32_u24_e32 v0, 0xd00, v0
	s_add_u32 s2, s44, s2
	v_or3_b32 v0, v0, v128, v5
	v_and_b32_e32 v8, 0x100, v1
	v_mov_b32_e32 v1, v161
	s_addc_u32 s3, s45, 0
	v_lshlrev_b32_e32 v2, 4, v211
	v_lshlrev_b32_e32 v3, 1, v211
	v_lshlrev_b64 v[0:1], 1, v[0:1]
	v_and_b32_e32 v6, 32, v3
	v_and_b32_e32 v7, 0xc0, v2
	v_lshl_add_u64 v[2:3], s[2:3], 0, v[0:1]
	s_mov_b64 s[2:3], 0x1500
	s_mov_b32 m0, s23
	v_lshl_add_u64 v[2:3], v[2:3], 0, s[2:3]
	global_load_lds_dwordx4 v[2:3], off
	v_and_or_b32 v2, v212, 7, v4
	s_add_u32 s33, s33, s58
	v_lshlrev_b32_e32 v2, 4, v2
	s_movk_i32 s2, 0x60
	s_addc_u32 s31, s31, 0
	v_bitop3_b32 v225, v210, v2, s2 bitop3:0x36
	s_add_u32 s2, s6, s33
	s_addc_u32 s3, s7, s31
	v_lshl_add_u64 v[212:213], v[160:161], 1, s[2:3]
	v_add_lshl_u32 v160, v214, v129, 1
	s_waitcnt vmcnt(0)
	v_lshl_add_u64 v[214:215], s[2:3], 0, v[160:161]
	s_add_u32 s2, s10, s33
	v_xor_b32_e32 v222, v2, v210
	v_bitop3_b32 v223, v210, v2, 32 bitop3:0x36
	v_bitop3_b32 v224, v210, v2, 64 bitop3:0x36
	v_add3_u32 v2, v7, 0, v5
	s_addc_u32 s3, s11, s31
	v_mov_b32_e32 v227, 0
	v_lshl_add_u32 v221, v220, 8, 0
	v_add3_u32 v226, v2, v6, v8
	v_lshl_add_u64 v[216:217], s[2:3], 0, v[0:1]
	s_mov_b32 s31, 0
	s_mov_b64 s[90:91], 0
	v_mov_b32_e32 v160, 0
	v_mov_b32_e32 v32, 0
	v_mov_b32_e32 v33, v227
	v_mov_b32_e32 v34, v227
	v_mov_b32_e32 v35, v227
	v_mov_b32_e32 v36, v227
	v_mov_b32_e32 v37, v227
	v_mov_b32_e32 v38, v227
	v_mov_b32_e32 v39, v227
	v_mov_b32_e32 v40, v227
	v_mov_b32_e32 v41, v227
	v_mov_b32_e32 v42, v227
	v_mov_b32_e32 v43, v227
	v_mov_b32_e32 v44, v227
	v_mov_b32_e32 v45, v227
	v_mov_b32_e32 v46, v227
	v_mov_b32_e32 v47, v227
	v_mov_b32_e32 v48, 0
	v_mov_b32_e32 v49, v227
	v_mov_b32_e32 v50, v227
	v_mov_b32_e32 v51, v227
	v_mov_b32_e32 v52, v227
	v_mov_b32_e32 v53, v227
	v_mov_b32_e32 v54, v227
	v_mov_b32_e32 v55, v227
	v_mov_b32_e32 v56, v227
	v_mov_b32_e32 v57, v227
	v_mov_b32_e32 v58, v227
	v_mov_b32_e32 v59, v227
	v_mov_b32_e32 v60, v227
	v_mov_b32_e32 v61, v227
	v_mov_b32_e32 v62, v227
	v_mov_b32_e32 v63, v227
	v_mov_b32_e32 v0, 0
	v_mov_b32_e32 v1, v227
	v_mov_b32_e32 v2, v227
	v_mov_b32_e32 v3, v227
	v_mov_b32_e32 v4, v227
	v_mov_b32_e32 v5, v227
	v_mov_b32_e32 v6, v227
	v_mov_b32_e32 v7, v227
	v_mov_b32_e32 v8, v227
	v_mov_b32_e32 v9, v227
	v_mov_b32_e32 v10, v227
	v_mov_b32_e32 v11, v227
	v_mov_b32_e32 v12, v227
	v_mov_b32_e32 v13, v227
	v_mov_b32_e32 v14, v227
	v_mov_b32_e32 v15, v227
	v_mov_b32_e32 v16, 0
	v_mov_b32_e32 v17, v227
	v_mov_b32_e32 v18, v227
	v_mov_b32_e32 v19, v227
	v_mov_b32_e32 v20, v227
	v_mov_b32_e32 v21, v227
	v_mov_b32_e32 v22, v227
	v_mov_b32_e32 v23, v227
	v_mov_b32_e32 v24, v227
	v_mov_b32_e32 v25, v227
	v_mov_b32_e32 v26, v227
	v_mov_b32_e32 v27, v227
	v_mov_b32_e32 v28, v227
	v_mov_b32_e32 v29, v227
	v_mov_b32_e32 v30, v227
	v_mov_b32_e32 v31, v227
	s_waitcnt vmcnt(0) lgkmcnt(0)
	s_barrier
	s_branch .LBB0_632
	.p2align 6

.LBB0_658:
	v_readlane_b32 s2, v254, 57
	s_bfe_u32 s22, s31, 0x20003
	v_readlane_b32 s4, v255, 42
	v_mov_b32_e32 v0, s2
	v_readlane_b32 s2, v254, 58
	ds_read_b32 v0, v0
	v_readlane_b32 s5, v255, 43
	v_mov_b32_e32 v1, s2
	ds_read_b32 v1, v1
	s_ashr_i32 s2, s31, 5
	s_ashr_i32 s3, s2, 31
	s_waitcnt lgkmcnt(1)
	v_readfirstlane_b32 s18, v0
	s_lshl_b64 s[10:11], s[2:3], 11
	s_waitcnt lgkmcnt(0)
	v_readfirstlane_b32 s19, v1
	s_add_u32 s18, s18, s4
	s_addc_u32 s19, s19, s5
	s_lshl_b32 s23, s31, 8
	s_and_b32 s23, s23, 0x700
	s_or_b32 s10, s10, s23
	s_mulk_i32 s11, 0x1a00
	s_mul_hi_u32 s33, s10, 0x1a00
	s_add_i32 s33, s33, s11
	s_mulk_i32 s10, 0x1a00
	s_add_u32 s10, s83, s10
	s_addc_u32 s11, s95, s33
	s_lshl_b32 s33, s22, 8
	s_add_u32 s10, s10, s33
	s_addc_u32 s11, s11, 0
	s_add_u32 s46, s10, 0x1600
	v_readlane_b32 s10, v253, 20
	v_mbcnt_lo_u32_b32 v194, -1, 0
	v_mbcnt_hi_u32_b32 v194, -1, v194
	s_addc_u32 s47, s11, 0
	v_and_b32_e32 v223, 31, v194
	v_add_u32_e32 v225, s10, v194
	v_bfe_u32 v224, v225, 6, 3
	v_lshl_or_b32 v2, v224, 5, v223
	v_mul_u32_u24_e32 v0, 0xd00, v2
	v_bfe_u32 v222, v194, 5, 1
	v_lshlrev_b32_e32 v160, 1, v0
	v_lshl_add_u64 v[0:1], s[46:47], 0, v[160:161]
	v_lshlrev_b32_e32 v160, 4, v222
	v_lshl_add_u64 v[0:1], v[0:1], 0, v[160:161]
	global_load_dwordx4 v[150:153], v[0:1], off offset:96
	global_load_dwordx4 v[154:157], v[0:1], off offset:224
	global_load_dwordx4 v[168:171], v[0:1], off offset:64
	global_load_dwordx4 v[172:175], v[0:1], off offset:192
	global_load_dwordx4 v[132:135], v[0:1], off
	global_load_dwordx4 v[184:187], v[0:1], off offset:32
	global_load_dwordx4 v[128:131], v[0:1], off offset:128
	global_load_dwordx4 v[188:191], v[0:1], off offset:160
	v_or_b32_e32 v2, s23, v2
	v_mov_b32_e32 v3, v161
	v_and_b32_e32 v0, 32, v194
	v_lshlrev_b32_e32 v2, 8, v2
	v_mov_b32_e32 v1, v161
	global_load_dwordx4 v[44:47], v0, s[18:19]
	global_load_dwordx4 v[68:71], v0, s[18:19] offset:16
	global_load_dwordx4 v[80:83], v0, s[18:19] offset:64
	global_load_dwordx4 v[88:91], v0, s[18:19] offset:80
	global_load_dwordx4 v[96:99], v0, s[18:19] offset:128
	global_load_dwordx4 v[104:107], v0, s[18:19] offset:144
	global_load_dwordx4 v[112:115], v0, s[18:19] offset:192
	global_load_dwordx4 v[120:123], v0, s[18:19] offset:208
	global_load_dwordx4 v[56:59], v0, s[18:19] offset:256
	global_load_dwordx4 v[76:79], v0, s[18:19] offset:272
	global_load_dwordx4 v[84:87], v0, s[18:19] offset:320
	global_load_dwordx4 v[92:95], v0, s[18:19] offset:336
	global_load_dwordx4 v[100:103], v0, s[18:19] offset:384
	global_load_dwordx4 v[108:111], v0, s[18:19] offset:400
	global_load_dwordx4 v[116:119], v0, s[18:19] offset:448
	global_load_dwordx4 v[124:127], v0, s[18:19] offset:464
	v_lshl_add_u64 v[4:5], s[34:35], 0, v[2:3]
	v_lshl_add_u64 v[2:3], s[36:37], 0, v[2:3]
	v_lshl_add_u64 v[4:5], v[4:5], 0, v[0:1]
	v_lshl_add_u64 v[6:7], v[2:3], 0, v[0:1]
	global_load_dwordx4 v[64:67], v[4:5], off
	global_load_dwordx4 v[52:55], v[4:5], off offset:16
	global_load_dwordx4 v[72:75], v[6:7], off
	global_load_dwordx4 v[60:63], v[6:7], off offset:16
	global_load_dwordx4 v[40:43], v[4:5], off offset:64
	global_load_dwordx4 v[32:35], v[4:5], off offset:80
	global_load_dwordx4 v[48:51], v[6:7], off offset:64
	global_load_dwordx4 v[36:39], v[6:7], off offset:80
	global_load_dwordx4 v[24:27], v[4:5], off offset:128
	global_load_dwordx4 v[16:19], v[4:5], off offset:144
	global_load_dwordx4 v[28:31], v[6:7], off offset:128
	global_load_dwordx4 v[20:23], v[6:7], off offset:144
	global_load_dwordx4 v[8:11], v[4:5], off offset:192
	global_load_dwordx4 v[0:3], v[4:5], off offset:208
	global_load_dwordx4 v[12:15], v[6:7], off offset:192
	s_nop 0
	global_load_dwordx4 v[4:7], v[6:7], off offset:208
	s_lshl_b64 s[2:3], s[2:3], 19
	s_add_u32 s2, s6, s2
	s_addc_u32 s3, s7, s3
	s_lshl_b32 s10, s22, 9
	s_add_u32 s18, s2, s10
	s_mov_b32 s2, 0x3e0293ee
	v_mov_b32_e32 v243, 0x3c0881c4
	s_addc_u32 s19, s3, 0
	v_and_b32_e32 v230, 63, v194
	s_waitcnt vmcnt(39)
	v_lshlrev_b32_e32 v136, 16, v153
	v_and_b32_e32 v137, 0xffff0000, v153
	s_waitcnt vmcnt(38)
	v_lshlrev_b32_e32 v138, 16, v157
	v_and_b32_e32 v139, 0xffff0000, v157
	s_waitcnt vmcnt(35)
	v_and_b32_e32 v197, 0xffff0000, v132
	v_lshlrev_b32_e32 v140, 16, v152
	v_and_b32_e32 v141, 0xffff0000, v152
	v_lshlrev_b32_e32 v144, 16, v156
	v_and_b32_e32 v145, 0xffff0000, v156
	v_lshlrev_b32_e32 v142, 16, v151
	v_and_b32_e32 v143, 0xffff0000, v151
	v_lshlrev_b32_e32 v146, 16, v155
	v_and_b32_e32 v147, 0xffff0000, v155
	v_lshlrev_b32_e32 v148, 16, v150
	v_and_b32_e32 v149, 0xffff0000, v150
	v_lshlrev_b32_e32 v152, 16, v154
	v_and_b32_e32 v153, 0xffff0000, v154
	v_lshlrev_b32_e32 v150, 16, v171
	v_and_b32_e32 v151, 0xffff0000, v171
	v_lshlrev_b32_e32 v154, 16, v175
	v_and_b32_e32 v155, 0xffff0000, v175
	v_lshlrev_b32_e32 v156, 16, v170
	v_and_b32_e32 v157, 0xffff0000, v170
	v_lshlrev_b32_e32 v162, 16, v174
	v_and_b32_e32 v163, 0xffff0000, v174
	v_lshlrev_b32_e32 v158, 16, v169
	v_and_b32_e32 v159, 0xffff0000, v169
	v_lshlrev_b32_e32 v164, 16, v173
	v_and_b32_e32 v165, 0xffff0000, v173
	v_lshlrev_b32_e32 v166, 16, v168
	v_and_b32_e32 v167, 0xffff0000, v168
	v_lshlrev_b32_e32 v170, 16, v172
	v_and_b32_e32 v171, 0xffff0000, v172
	s_waitcnt vmcnt(34)
	v_lshlrev_b32_e32 v168, 16, v187
	v_and_b32_e32 v169, 0xffff0000, v187
	s_waitcnt vmcnt(32)
	v_lshlrev_b32_e32 v172, 16, v191
	v_and_b32_e32 v173, 0xffff0000, v191
	v_lshlrev_b32_e32 v174, 16, v186
	v_and_b32_e32 v175, 0xffff0000, v186
	v_lshlrev_b32_e32 v178, 16, v190
	v_and_b32_e32 v179, 0xffff0000, v190
	v_lshlrev_b32_e32 v176, 16, v185
	v_and_b32_e32 v177, 0xffff0000, v185
	v_lshlrev_b32_e32 v180, 16, v189
	v_and_b32_e32 v181, 0xffff0000, v189
	v_lshlrev_b32_e32 v182, 16, v184
	v_and_b32_e32 v183, 0xffff0000, v184
	v_lshlrev_b32_e32 v186, 16, v188
	v_and_b32_e32 v187, 0xffff0000, v188
	v_lshlrev_b32_e32 v184, 16, v135
	v_and_b32_e32 v185, 0xffff0000, v135
	v_lshlrev_b32_e32 v188, 16, v131
	v_and_b32_e32 v189, 0xffff0000, v131
	v_lshlrev_b32_e32 v190, 16, v134
	v_and_b32_e32 v191, 0xffff0000, v134
	v_lshlrev_b32_e32 v134, 16, v130
	v_and_b32_e32 v135, 0xffff0000, v130
	v_lshlrev_b32_e32 v130, 16, v133
	v_and_b32_e32 v131, 0xffff0000, v133
	v_lshlrev_b32_e32 v196, 16, v132
	v_lshlrev_b32_e32 v132, 16, v128
	v_and_b32_e32 v133, 0xffff0000, v128
	v_mul_f32_e32 v128, v197, v197
	v_lshlrev_b32_e32 v192, 16, v129
	v_and_b32_e32 v193, 0xffff0000, v129
	v_pk_fma_f32 v[128:129], v[196:197], v[196:197], v[128:129] op_sel_hi:[1,1,0]
	v_mul_f32_e32 v198, v131, v131
	v_pk_fma_f32 v[128:129], v[130:131], v[130:131], v[128:129]
	s_nop 0
	v_pk_add_f32 v[128:129], v[198:199], v[128:129] op_sel_hi:[0,1]
	v_pk_fma_f32 v[128:129], v[190:191], v[190:191], v[128:129]
	v_mul_f32_e32 v198, v191, v191
	v_pk_add_f32 v[128:129], v[198:199], v[128:129] op_sel_hi:[0,1]
	v_pk_fma_f32 v[128:129], v[184:185], v[184:185], v[128:129]
	v_mul_f32_e32 v198, v185, v185
	v_pk_add_f32 v[128:129], v[198:199], v[128:129] op_sel_hi:[0,1]
	v_pk_fma_f32 v[128:129], v[182:183], v[182:183], v[128:129]
	v_mul_f32_e32 v198, v183, v183
	v_pk_add_f32 v[128:129], v[198:199], v[128:129] op_sel_hi:[0,1]
	v_pk_fma_f32 v[128:129], v[176:177], v[176:177], v[128:129]
	v_mul_f32_e32 v198, v177, v177
	v_pk_add_f32 v[128:129], v[198:199], v[128:129] op_sel_hi:[0,1]
	v_pk_fma_f32 v[128:129], v[174:175], v[174:175], v[128:129]
	v_mul_f32_e32 v198, v175, v175
	v_pk_add_f32 v[128:129], v[198:199], v[128:129] op_sel_hi:[0,1]
	v_pk_fma_f32 v[128:129], v[168:169], v[168:169], v[128:129]
	v_mul_f32_e32 v198, v169, v169
	v_pk_add_f32 v[128:129], v[198:199], v[128:129] op_sel_hi:[0,1]
	v_pk_fma_f32 v[128:129], v[166:167], v[166:167], v[128:129]
	v_mul_f32_e32 v198, v167, v167
	v_pk_add_f32 v[128:129], v[198:199], v[128:129] op_sel_hi:[0,1]
	v_pk_fma_f32 v[128:129], v[158:159], v[158:159], v[128:129]
	v_mul_f32_e32 v198, v159, v159
	v_pk_add_f32 v[128:129], v[198:199], v[128:129] op_sel_hi:[0,1]
	v_pk_fma_f32 v[128:129], v[156:157], v[156:157], v[128:129]
	v_mul_f32_e32 v198, v157, v157
	v_pk_add_f32 v[128:129], v[198:199], v[128:129] op_sel_hi:[0,1]
	v_pk_fma_f32 v[128:129], v[150:151], v[150:151], v[128:129]
	v_mul_f32_e32 v198, v151, v151
	v_pk_add_f32 v[128:129], v[198:199], v[128:129] op_sel_hi:[0,1]
	v_pk_fma_f32 v[128:129], v[148:149], v[148:149], v[128:129]
	v_mul_f32_e32 v198, v149, v149
	v_pk_add_f32 v[128:129], v[198:199], v[128:129] op_sel_hi:[0,1]
	v_pk_fma_f32 v[128:129], v[142:143], v[142:143], v[128:129]
	v_mul_f32_e32 v198, v143, v143
	v_pk_add_f32 v[128:129], v[198:199], v[128:129] op_sel_hi:[0,1]
	v_pk_fma_f32 v[128:129], v[140:141], v[140:141], v[128:129]
	v_mul_f32_e32 v198, v141, v141
	v_pk_add_f32 v[128:129], v[198:199], v[128:129] op_sel_hi:[0,1]
	v_pk_fma_f32 v[128:129], v[136:137], v[136:137], v[128:129]
	v_mul_f32_e32 v198, v137, v137
	v_pk_add_f32 v[128:129], v[198:199], v[128:129] op_sel_hi:[0,1]
	v_pk_fma_f32 v[128:129], v[132:133], v[132:133], v[128:129]
	v_mul_f32_e32 v198, v133, v133
	v_pk_add_f32 v[128:129], v[198:199], v[128:129] op_sel_hi:[0,1]
	v_pk_fma_f32 v[128:129], v[192:193], v[192:193], v[128:129]
	v_mul_f32_e32 v198, v193, v193
	v_pk_add_f32 v[128:129], v[198:199], v[128:129] op_sel_hi:[0,1]
	v_pk_fma_f32 v[128:129], v[134:135], v[134:135], v[128:129]
	v_mul_f32_e32 v198, v135, v135
	v_pk_add_f32 v[128:129], v[198:199], v[128:129] op_sel_hi:[0,1]
	v_pk_fma_f32 v[128:129], v[188:189], v[188:189], v[128:129]
	v_mul_f32_e32 v198, v189, v189
	v_pk_add_f32 v[128:129], v[198:199], v[128:129] op_sel_hi:[0,1]
	v_pk_fma_f32 v[128:129], v[186:187], v[186:187], v[128:129]
	v_mul_f32_e32 v198, v187, v187
	v_pk_add_f32 v[128:129], v[198:199], v[128:129] op_sel_hi:[0,1]
	v_pk_fma_f32 v[128:129], v[180:181], v[180:181], v[128:129]
	v_mul_f32_e32 v198, v181, v181
	v_pk_add_f32 v[128:129], v[198:199], v[128:129] op_sel_hi:[0,1]
	v_pk_fma_f32 v[128:129], v[178:179], v[178:179], v[128:129]
	v_mul_f32_e32 v198, v179, v179
	v_pk_add_f32 v[128:129], v[198:199], v[128:129] op_sel_hi:[0,1]
	v_pk_fma_f32 v[128:129], v[172:173], v[172:173], v[128:129]
	v_mul_f32_e32 v198, v173, v173
	v_pk_add_f32 v[128:129], v[198:199], v[128:129] op_sel_hi:[0,1]
	v_pk_fma_f32 v[128:129], v[170:171], v[170:171], v[128:129]
	v_mul_f32_e32 v198, v171, v171
	v_pk_add_f32 v[128:129], v[198:199], v[128:129] op_sel_hi:[0,1]
	v_pk_fma_f32 v[128:129], v[164:165], v[164:165], v[128:129]
	v_mul_f32_e32 v198, v165, v165
	v_pk_add_f32 v[128:129], v[198:199], v[128:129] op_sel_hi:[0,1]
	v_pk_fma_f32 v[128:129], v[162:163], v[162:163], v[128:129]
	v_mul_f32_e32 v198, v163, v163
	v_pk_add_f32 v[128:129], v[198:199], v[128:129] op_sel_hi:[0,1]
	v_pk_fma_f32 v[128:129], v[154:155], v[154:155], v[128:129]
	v_mul_f32_e32 v198, v155, v155
	v_pk_add_f32 v[128:129], v[198:199], v[128:129] op_sel_hi:[0,1]
	v_pk_fma_f32 v[128:129], v[152:153], v[152:153], v[128:129]
	v_mul_f32_e32 v198, v153, v153
	v_pk_add_f32 v[128:129], v[198:199], v[128:129] op_sel_hi:[0,1]
	v_pk_fma_f32 v[128:129], v[146:147], v[146:147], v[128:129]
	v_mul_f32_e32 v198, v147, v147
	v_pk_add_f32 v[128:129], v[198:199], v[128:129] op_sel_hi:[0,1]
	v_pk_fma_f32 v[128:129], v[144:145], v[144:145], v[128:129]
	v_mul_f32_e32 v198, v145, v145
	v_pk_add_f32 v[128:129], v[198:199], v[128:129] op_sel_hi:[0,1]
	v_pk_fma_f32 v[128:129], v[138:139], v[138:139], v[128:129]
	v_mul_f32_e32 v198, v139, v139
	v_pk_add_f32 v[128:129], v[198:199], v[128:129] op_sel_hi:[0,1]
	v_mov_b32_e32 v129, v128
	s_nop 1
	v_permlane32_swap_b32_e32 v128, v129
	v_add_f32_e32 v128, v128, v129
	v_fmamk_f32 v128, v128, 0x3c000000, v240
	v_rsq_f32_e32 v128, v128
	s_waitcnt vmcnt(24)
	v_pk_mul_f32 v[120:121], v[128:129], v[120:121] op_sel_hi:[0,1]
	s_waitcnt vmcnt(16)
	v_pk_mul_f32 v[124:125], v[128:129], v[124:125] op_sel_hi:[0,1]
	v_pk_mul_f32 v[122:123], v[128:129], v[122:123] op_sel_hi:[0,1]
	v_pk_mul_f32 v[120:121], v[120:121], v[140:141]
	v_pk_mul_f32 v[124:125], v[124:125], v[144:145]
	v_pk_mul_f32 v[122:123], v[122:123], v[136:137]
	s_waitcnt vmcnt(0)
	v_pk_mul_f32 v[136:137], v[120:121], v[4:5]
	v_pk_mul_f32 v[4:5], v[124:125], v[4:5]
	v_pk_mul_f32 v[126:127], v[128:129], v[126:127] op_sel_hi:[0,1]
	v_pk_fma_f32 v[136:137], v[124:125], v[0:1], v[136:137]
	v_pk_mul_f32 v[44:45], v[44:45], v[128:129] op_sel_hi:[1,0]
	v_pk_fma_f32 v[0:1], v[120:121], v[0:1], v[4:5] neg_lo:[0,0,1] neg_hi:[0,0,1]
	v_pk_mul_f32 v[126:127], v[126:127], v[138:139]
	v_pk_mul_f32 v[82:83], v[82:83], v[128:129] op_sel_hi:[1,0]
	v_pk_mul_f32 v[44:45], v[44:45], v[196:197]
	v_pk_mul_f32 v[56:57], v[128:129], v[56:57] op_sel_hi:[0,1]
	v_pk_mul_f32 v[0:1], v[0:1], s[2:3] op_sel_hi:[1,0]
	v_pk_mul_f32 v[114:115], v[128:129], v[114:115] op_sel_hi:[0,1]
	v_pk_mul_f32 v[118:119], v[128:129], v[118:119] op_sel_hi:[0,1]
	v_pk_mul_f32 v[112:113], v[128:129], v[112:113] op_sel_hi:[0,1]
	v_pk_mul_f32 v[116:117], v[128:129], v[116:117] op_sel_hi:[0,1]
	v_pk_mul_f32 v[106:107], v[128:129], v[106:107] op_sel_hi:[0,1]
	v_pk_mul_f32 v[110:111], v[128:129], v[110:111] op_sel_hi:[0,1]
	v_pk_mul_f32 v[104:105], v[128:129], v[104:105] op_sel_hi:[0,1]
	v_pk_mul_f32 v[108:109], v[128:129], v[108:109] op_sel_hi:[0,1]
	v_pk_mul_f32 v[98:99], v[128:129], v[98:99] op_sel_hi:[0,1]
	v_pk_mul_f32 v[102:103], v[128:129], v[102:103] op_sel_hi:[0,1]
	v_pk_mul_f32 v[96:97], v[128:129], v[96:97] op_sel_hi:[0,1]
	v_pk_mul_f32 v[100:101], v[128:129], v[100:101] op_sel_hi:[0,1]
	v_pk_mul_f32 v[90:91], v[90:91], v[128:129] op_sel_hi:[1,0]
	v_pk_mul_f32 v[94:95], v[128:129], v[94:95] op_sel_hi:[0,1]
	v_pk_mul_f32 v[88:89], v[88:89], v[128:129] op_sel_hi:[1,0]
	v_pk_mul_f32 v[92:93], v[128:129], v[92:93] op_sel_hi:[0,1]
	v_pk_mul_f32 v[82:83], v[82:83], v[176:177]
	v_pk_mul_f32 v[86:87], v[128:129], v[86:87] op_sel_hi:[0,1]
	v_pk_mul_f32 v[80:81], v[80:81], v[128:129] op_sel_hi:[1,0]
	v_pk_mul_f32 v[84:85], v[128:129], v[84:85] op_sel_hi:[0,1]
	v_pk_mul_f32 v[70:71], v[70:71], v[128:129] op_sel_hi:[1,0]
	v_pk_mul_f32 v[78:79], v[128:129], v[78:79] op_sel_hi:[0,1]
	v_pk_mul_f32 v[68:69], v[68:69], v[128:129] op_sel_hi:[1,0]
	v_pk_mul_f32 v[76:77], v[128:129], v[76:77] op_sel_hi:[0,1]
	v_pk_mul_f32 v[46:47], v[46:47], v[128:129] op_sel_hi:[1,0]
	v_pk_mul_f32 v[58:59], v[128:129], v[58:59] op_sel_hi:[0,1]
	v_pk_mul_f32 v[56:57], v[56:57], v[132:133]
	v_pk_mul_f32 v[128:129], v[44:45], v[72:73]
	v_cvt_pk_bf16_f32 v176, v0, v1
	v_pk_mul_f32 v[0:1], v[126:127], v[6:7]
	v_pk_mul_f32 v[46:47], v[46:47], v[130:131]
	v_pk_fma_f32 v[128:129], v[56:57], v[64:65], v[128:129]
	v_pk_mul_f32 v[56:57], v[56:57], v[72:73]
	v_pk_fma_f32 v[0:1], v[122:123], v[2:3], v[0:1] neg_lo:[0,0,1] neg_hi:[0,0,1]
	v_pk_mul_f32 v[68:69], v[68:69], v[190:191]
	v_pk_mul_f32 v[58:59], v[58:59], v[192:193]
	v_pk_mul_f32 v[130:131], v[46:47], v[74:75]
	v_pk_fma_f32 v[44:45], v[44:45], v[64:65], v[56:57] neg_lo:[0,0,1] neg_hi:[0,0,1]
	v_pk_mul_f32 v[0:1], v[0:1], s[2:3] op_sel_hi:[1,0]
	v_pk_mul_f32 v[70:71], v[70:71], v[184:185]
	v_pk_mul_f32 v[76:77], v[76:77], v[134:135]
	v_pk_mul_f32 v[134:135], v[68:69], v[60:61]
	v_pk_fma_f32 v[130:131], v[58:59], v[66:67], v[130:131]
	v_pk_mul_f32 v[44:45], v[44:45], s[2:3] op_sel_hi:[1,0]
	v_cvt_pk_bf16_f32 v177, v0, v1
	v_pk_mul_f32 v[0:1], v[128:129], s[2:3] op_sel_hi:[1,0]
	v_pk_mul_f32 v[108:109], v[108:109], v[162:163]
	v_pk_mul_f32 v[98:99], v[98:99], v[158:159]
	v_pk_mul_f32 v[92:93], v[92:93], v[178:179]
	v_pk_mul_f32 v[80:81], v[80:81], v[182:183]
	v_pk_mul_f32 v[78:79], v[78:79], v[188:189]
	v_pk_mul_f32 v[158:159], v[70:71], v[62:63]
	v_pk_fma_f32 v[134:135], v[76:77], v[52:53], v[134:135]
	v_cvt_pk_bf16_f32 v162, v44, v45
	v_pk_mul_f32 v[44:45], v[58:59], v[74:75]
	v_cvt_pk_bf16_f32 v178, v0, v1
	v_pk_mul_f32 v[0:1], v[130:131], s[2:3] op_sel_hi:[1,0]
	v_pk_mul_f32 v[104:105], v[104:105], v[156:157]
	v_pk_mul_f32 v[84:85], v[84:85], v[186:187]
	v_pk_mul_f32 v[156:157], v[80:81], v[48:49]
	v_pk_fma_f32 v[158:159], v[78:79], v[54:55], v[158:159]
	v_pk_fma_f32 v[44:45], v[46:47], v[66:67], v[44:45] neg_lo:[0,0,1] neg_hi:[0,0,1]
	v_cvt_pk_bf16_f32 v179, v0, v1
	v_pk_mul_f32 v[0:1], v[134:135], s[2:3] op_sel_hi:[1,0]
	v_pk_mul_f32 v[110:111], v[110:111], v[154:155]
	v_pk_mul_f32 v[88:89], v[88:89], v[174:175]
	v_pk_mul_f32 v[86:87], v[86:87], v[180:181]
	v_pk_mul_f32 v[154:155], v[82:83], v[50:51]
	v_pk_fma_f32 v[156:157], v[84:85], v[40:41], v[156:157]
	v_pk_mul_f32 v[44:45], v[44:45], s[2:3] op_sel_hi:[1,0]
	v_cvt_pk_bf16_f32 v180, v0, v1
	v_pk_mul_f32 v[0:1], v[158:159], s[2:3] op_sel_hi:[1,0]
	v_pk_mul_f32 v[116:117], v[116:117], v[152:153]
	v_pk_mul_f32 v[90:91], v[90:91], v[168:169]
	v_pk_mul_f32 v[152:153], v[88:89], v[36:37]
	v_pk_fma_f32 v[154:155], v[86:87], v[42:43], v[154:155]
	v_cvt_pk_bf16_f32 v163, v44, v45
	v_pk_mul_f32 v[44:45], v[76:77], v[60:61]
	v_cvt_pk_bf16_f32 v181, v0, v1
	v_pk_mul_f32 v[0:1], v[156:157], s[2:3] op_sel_hi:[1,0]
	v_pk_mul_f32 v[106:107], v[106:107], v[150:151]
	v_pk_mul_f32 v[96:97], v[96:97], v[166:167]
	v_pk_mul_f32 v[94:95], v[94:95], v[172:173]
	v_pk_mul_f32 v[150:151], v[90:91], v[38:39]
	v_pk_fma_f32 v[152:153], v[92:93], v[32:33], v[152:153]
	v_pk_fma_f32 v[44:45], v[68:69], v[52:53], v[44:45] neg_lo:[0,0,1] neg_hi:[0,0,1]
	v_cvt_pk_bf16_f32 v182, v0, v1
	v_pk_mul_f32 v[0:1], v[154:155], s[2:3] op_sel_hi:[1,0]
	v_pk_mul_f32 v[112:113], v[112:113], v[148:149]
	v_pk_mul_f32 v[100:101], v[100:101], v[170:171]
	v_pk_mul_f32 v[148:149], v[96:97], v[28:29]
	v_pk_fma_f32 v[150:151], v[94:95], v[34:35], v[150:151]
	v_pk_mul_f32 v[44:45], v[44:45], s[2:3] op_sel_hi:[1,0]
	v_cvt_pk_bf16_f32 v183, v0, v1
	v_pk_mul_f32 v[0:1], v[152:153], s[2:3] op_sel_hi:[1,0]
	v_pk_mul_f32 v[118:119], v[118:119], v[146:147]
	v_pk_mul_f32 v[102:103], v[102:103], v[164:165]
	v_pk_mul_f32 v[146:147], v[98:99], v[30:31]
	v_pk_fma_f32 v[148:149], v[100:101], v[24:25], v[148:149]
	v_cvt_pk_bf16_f32 v164, v44, v45
	v_pk_mul_f32 v[44:45], v[78:79], v[62:63]
	v_cvt_pk_bf16_f32 v184, v0, v1
	v_pk_mul_f32 v[0:1], v[150:151], s[2:3] op_sel_hi:[1,0]
	v_pk_mul_f32 v[144:145], v[104:105], v[20:21]
	v_pk_fma_f32 v[146:147], v[102:103], v[26:27], v[146:147]
	v_pk_fma_f32 v[44:45], v[70:71], v[54:55], v[44:45] neg_lo:[0,0,1] neg_hi:[0,0,1]
	v_cvt_pk_bf16_f32 v185, v0, v1
	v_pk_mul_f32 v[0:1], v[148:149], s[2:3] op_sel_hi:[1,0]
	v_pk_mul_f32 v[114:115], v[114:115], v[142:143]
	v_pk_mul_f32 v[142:143], v[106:107], v[22:23]
	v_pk_fma_f32 v[144:145], v[108:109], v[16:17], v[144:145]
	v_pk_mul_f32 v[44:45], v[44:45], s[2:3] op_sel_hi:[1,0]
	v_cvt_pk_bf16_f32 v186, v0, v1
	v_pk_mul_f32 v[0:1], v[146:147], s[2:3] op_sel_hi:[1,0]
	v_pk_mul_f32 v[140:141], v[112:113], v[12:13]
	v_pk_fma_f32 v[142:143], v[110:111], v[18:19], v[142:143]
	v_cvt_pk_bf16_f32 v165, v44, v45
	v_pk_mul_f32 v[44:45], v[84:85], v[48:49]
	v_pk_mul_f32 v[36:37], v[92:93], v[36:37]
	v_pk_mul_f32 v[28:29], v[100:101], v[28:29]
	v_pk_mul_f32 v[20:21], v[108:109], v[20:21]
	v_pk_mul_f32 v[12:13], v[116:117], v[12:13]
	v_cvt_pk_bf16_f32 v187, v0, v1
	v_pk_mul_f32 v[0:1], v[144:145], s[2:3] op_sel_hi:[1,0]
	v_pk_mul_f32 v[138:139], v[114:115], v[14:15]
	v_pk_fma_f32 v[140:141], v[116:117], v[8:9], v[140:141]
	v_pk_fma_f32 v[40:41], v[80:81], v[40:41], v[44:45] neg_lo:[0,0,1] neg_hi:[0,0,1]
	v_pk_fma_f32 v[32:33], v[88:89], v[32:33], v[36:37] neg_lo:[0,0,1] neg_hi:[0,0,1]
	v_pk_fma_f32 v[24:25], v[96:97], v[24:25], v[28:29] neg_lo:[0,0,1] neg_hi:[0,0,1]
	v_pk_fma_f32 v[16:17], v[104:105], v[16:17], v[20:21] neg_lo:[0,0,1] neg_hi:[0,0,1]
	v_pk_fma_f32 v[8:9], v[112:113], v[8:9], v[12:13] neg_lo:[0,0,1] neg_hi:[0,0,1]
	v_cvt_pk_bf16_f32 v188, v0, v1
	v_pk_mul_f32 v[0:1], v[142:143], s[2:3] op_sel_hi:[1,0]
	v_pk_fma_f32 v[138:139], v[118:119], v[10:11], v[138:139]
	v_pk_mul_f32 v[40:41], v[40:41], s[2:3] op_sel_hi:[1,0]
	v_pk_mul_f32 v[32:33], v[32:33], s[2:3] op_sel_hi:[1,0]
	v_pk_mul_f32 v[24:25], v[24:25], s[2:3] op_sel_hi:[1,0]
	v_pk_mul_f32 v[16:17], v[16:17], s[2:3] op_sel_hi:[1,0]
	v_pk_mul_f32 v[8:9], v[8:9], s[2:3] op_sel_hi:[1,0]
	v_cvt_pk_bf16_f32 v189, v0, v1
	v_pk_mul_f32 v[0:1], v[140:141], s[2:3] op_sel_hi:[1,0]
	v_pk_mul_f32 v[132:133], v[122:123], v[6:7]
	v_cvt_pk_bf16_f32 v166, v40, v41
	v_pk_mul_f32 v[40:41], v[86:87], v[50:51]
	v_cvt_pk_bf16_f32 v168, v32, v33
	v_pk_mul_f32 v[32:33], v[94:95], v[38:39]
	v_cvt_pk_bf16_f32 v170, v24, v25
	v_pk_mul_f32 v[24:25], v[102:103], v[30:31]
	v_cvt_pk_bf16_f32 v172, v16, v17
	v_pk_mul_f32 v[16:17], v[110:111], v[22:23]
	v_cvt_pk_bf16_f32 v174, v8, v9
	v_pk_mul_f32 v[8:9], v[118:119], v[14:15]
	v_cvt_pk_bf16_f32 v190, v0, v1
	v_pk_mul_f32 v[0:1], v[138:139], s[2:3] op_sel_hi:[1,0]
	v_pk_fma_f32 v[132:133], v[126:127], v[2:3], v[132:133]
	v_pk_fma_f32 v[40:41], v[82:83], v[42:43], v[40:41] neg_lo:[0,0,1] neg_hi:[0,0,1]
	v_pk_fma_f32 v[32:33], v[90:91], v[34:35], v[32:33] neg_lo:[0,0,1] neg_hi:[0,0,1]
	v_pk_fma_f32 v[24:25], v[98:99], v[26:27], v[24:25] neg_lo:[0,0,1] neg_hi:[0,0,1]
	v_pk_fma_f32 v[16:17], v[106:107], v[18:19], v[16:17] neg_lo:[0,0,1] neg_hi:[0,0,1]
	v_pk_fma_f32 v[8:9], v[114:115], v[10:11], v[8:9] neg_lo:[0,0,1] neg_hi:[0,0,1]
	v_cvt_pk_bf16_f32 v191, v0, v1
	v_pk_mul_f32 v[0:1], v[136:137], s[2:3] op_sel_hi:[1,0]
	v_pk_mul_f32 v[40:41], v[40:41], s[2:3] op_sel_hi:[1,0]
	v_pk_mul_f32 v[32:33], v[32:33], s[2:3] op_sel_hi:[1,0]
	v_pk_mul_f32 v[24:25], v[24:25], s[2:3] op_sel_hi:[1,0]
	v_pk_mul_f32 v[16:17], v[16:17], s[2:3] op_sel_hi:[1,0]
	v_pk_mul_f32 v[8:9], v[8:9], s[2:3] op_sel_hi:[1,0]
	v_cvt_pk_bf16_f32 v192, v0, v1
	v_pk_mul_f32 v[0:1], v[132:133], s[2:3] op_sel_hi:[1,0]
	v_cvt_pk_bf16_f32 v167, v40, v41
	v_cvt_pk_bf16_f32 v169, v32, v33
	v_cvt_pk_bf16_f32 v171, v24, v25
	v_cvt_pk_bf16_f32 v173, v16, v17
	v_cvt_pk_bf16_f32 v175, v8, v9
	v_cvt_pk_bf16_f32 v193, v0, v1
	v_lshlrev_b32_e32 v16, 3, v194
	v_bfe_u32 v18, v225, 4, 5
	v_and_b32_e32 v17, 0x78, v16
	v_or_b32_e32 v19, 32, v18
	v_lshl_or_b32 v0, v18, 10, v17
	v_lshl_or_b32 v4, v19, 10, v17
	v_lshlrev_b32_e32 v210, 1, v0
	v_lshlrev_b32_e32 v212, 1, v4
	global_load_dwordx4 v[0:3], v210, s[18:19]
	global_load_dwordx4 v[4:7], v212, s[18:19]
	global_load_dwordx4 v[8:11], v210, s[18:19] offset:256
	global_load_dwordx4 v[12:15], v212, s[18:19] offset:256
	v_lshrrev_b32_e32 v20, 5, v225
	v_lshrrev_b32_e32 v21, 3, v225
	v_lshlrev_b32_e32 v23, 4, v194
	v_and_b32_e32 v25, 7, v194
	v_lshrrev_b32_e32 v26, 1, v194
	v_and_b32_e32 v27, 8, v20
	v_and_b32_e32 v21, 8, v21
	v_lshlrev_b32_e32 v22, 3, v230
	v_lshlrev_b32_e32 v24, 1, v194
	v_and_b32_e32 v20, 4, v20
	v_and_b32_e32 v23, 0xc0, v23
	v_and_or_b32 v238, v26, 8, v25
	v_lshlrev_b32_e32 v17, 1, v17
	v_and_or_b32 v25, v18, 7, v27
	v_lshlrev_b32_e32 v26, 8, v19
	v_and_or_b32 v27, v18, 16, v21
	v_and_or_b32 v19, v19, 48, v21
	v_lshlrev_b32_e32 v28, 8, v18
	v_bfe_u32 v16, v16, 5, 2
	v_and_b32_e32 v24, 32, v24
	v_and_b32_e32 v29, 0x100, v22
	v_and_or_b32 v18, v18, 3, v20
	v_and_or_b32 v20, v22, 24, v23
	v_lshlrev_b32_e32 v21, 4, v25
	v_and_b32_e32 v22, 48, v17
	v_lshrrev_b32_e32 v23, 1, v27
	v_lshrrev_b32_e32 v19, 1, v19
	v_readlane_b32 s4, v255, 44
	v_or3_b32 v236, v20, v24, v29
	v_bitop3_b32 v20, v21, v28, v17 bitop3:0xde
	v_bitop3_b32 v17, v21, v26, v17 bitop3:0xde
	v_or_b32_e32 v21, v23, v16
	v_lshl_or_b32 v18, v18, 6, v22
	v_or_b32_e32 v16, v19, v16
	s_waitcnt vmcnt(0)
	v_readlane_b32 s5, v255, 45
	v_lshl_or_b32 v19, v21, 9, v18
	v_lshl_or_b32 v16, v16, 9, v18
	s_mov_b64 s[2:3], -1
	s_and_b64 vcc, exec, s[4:5]
	v_add_u32_e32 v231, 0, v236
	v_add_u32_e32 v232, 0, v20
	v_add_u32_e32 v233, 0, v17
	v_add_u32_e32 v234, 0, v19
	v_add_u32_e32 v235, 0, v16
	v_lshl_add_u32 v237, v223, 8, 0
	s_waitcnt vmcnt(3)
	ds_write_b128 v232, v[0:3] offset:32768
	s_waitcnt vmcnt(2)
	ds_write_b128 v233, v[4:7] offset:32768
	s_waitcnt vmcnt(1)
	ds_write_b128 v234, v[8:11]
	s_waitcnt vmcnt(0)
	ds_write_b128 v235, v[12:15]
	s_waitcnt lgkmcnt(0)
	s_barrier
	s_cbranch_vccnz .LBB0_684
	s_add_i32 s2, 0, 0x4000
	v_add_u32_e32 v239, s2, v236
	v_lshlrev_b32_e32 v0, 4, v238
	s_movk_i32 s2, 0x60
	v_bitop3_b32 v19, v160, v0, s2 bitop3:0x36
	s_movk_i32 s2, 0x80
	v_bitop3_b32 v20, v160, v0, s2 bitop3:0x36
	s_movk_i32 s2, 0xa0
	v_bitop3_b32 v21, v160, v0, s2 bitop3:0x36
	s_movk_i32 s2, 0xc0
	v_bitop3_b32 v22, v160, v0, s2 bitop3:0x36
	s_movk_i32 s2, 0xe0
	v_bitop3_b32 v23, v160, v0, s2 bitop3:0x36
	s_add_u32 s2, s18, 0x40000
	s_addc_u32 s3, s19, 0
	s_add_u32 s10, s18, 0x40100
	v_xor_b32_e32 v16, v0, v160
	v_bitop3_b32 v17, v160, v0, 32 bitop3:0x36
	v_bitop3_b32 v18, v160, v0, 64 bitop3:0x36
	s_addc_u32 s11, s19, 0
	v_mov_b32_e32 v213, v161
	v_mov_b32_e32 v14, v161
	v_mov_b32_e32 v15, v161
	v_mov_b32_e32 v211, v161
	v_lshl_add_u64 v[216:217], s[2:3], 0, v[212:213]
	v_lshl_add_u64 v[220:221], s[10:11], 0, v[212:213]
	v_mov_b32_e32 v0, v161
	v_mov_b32_e32 v1, v161
	v_mov_b32_e32 v2, v161
	v_mov_b32_e32 v3, v161
	v_mov_b32_e32 v4, v161
	v_mov_b32_e32 v5, v161
	v_mov_b32_e32 v6, v161
	v_mov_b32_e32 v7, v161
	v_mov_b32_e32 v8, v161
	v_mov_b32_e32 v9, v161
	v_mov_b32_e32 v10, v161
	v_mov_b32_e32 v11, v161
	v_mov_b32_e32 v12, v161
	v_mov_b32_e32 v13, v161
	v_add_u32_e32 v213, v237, v16
	v_add_u32_e32 v241, v237, v17
	v_add_u32_e32 v244, v237, v18
	v_add_u32_e32 v246, v237, v19
	v_add_u32_e32 v247, v237, v20
	v_add_u32_e32 v249, v237, v21
	v_add_u32_e32 v226, v237, v22
	v_add_u32_e32 v227, v237, v23
	v_mov_b64_e32 v[30:31], v[14:15]
	v_mov_b64_e32 v[46:47], v[14:15]
	v_mov_b64_e32 v[62:63], v[14:15]
	v_lshl_add_u64 v[214:215], s[2:3], 0, v[210:211]
	v_lshl_add_u64 v[218:219], s[10:11], 0, v[210:211]
	v_mov_b32_e32 v211, 0
	s_mov_b64 s[2:3], 0x10000
	s_mov_b64 s[48:49], -1
	v_mov_b64_e32 v[28:29], v[12:13]
	v_mov_b64_e32 v[26:27], v[10:11]
	v_mov_b64_e32 v[24:25], v[8:9]
	v_mov_b64_e32 v[22:23], v[6:7]
	v_mov_b64_e32 v[20:21], v[4:5]
	v_mov_b64_e32 v[18:19], v[2:3]
	v_mov_b64_e32 v[16:17], v[0:1]
	v_mov_b64_e32 v[44:45], v[12:13]
	v_mov_b64_e32 v[42:43], v[10:11]
	v_mov_b64_e32 v[40:41], v[8:9]
	v_mov_b64_e32 v[38:39], v[6:7]
	v_mov_b64_e32 v[36:37], v[4:5]
	v_mov_b64_e32 v[34:35], v[2:3]
	v_mov_b64_e32 v[32:33], v[0:1]
	v_mov_b64_e32 v[60:61], v[12:13]
	v_mov_b64_e32 v[58:59], v[10:11]
	v_mov_b64_e32 v[56:57], v[8:9]
	v_mov_b64_e32 v[54:55], v[6:7]
	v_mov_b64_e32 v[52:53], v[4:5]
	v_mov_b64_e32 v[50:51], v[2:3]
	v_mov_b64_e32 v[48:49], v[0:1]
	s_branch .LBB0_661
	.p2align 6

.LBB0_684:
	s_and_b64 vcc, exec, s[2:3]
	s_cbranch_vccz .LBB0_707
	v_lshlrev_b32_e32 v0, 4, v238
	s_movk_i32 s2, 0x60
	v_bitop3_b32 v4, v160, v0, s2 bitop3:0x36
	s_movk_i32 s2, 0x80
	v_bitop3_b32 v5, v160, v0, s2 bitop3:0x36
	s_movk_i32 s2, 0xa0
	v_bitop3_b32 v6, v160, v0, s2 bitop3:0x36
	s_movk_i32 s2, 0xc0
	v_bitop3_b32 v7, v160, v0, s2 bitop3:0x36
	s_movk_i32 s2, 0xe0
	v_xor_b32_e32 v1, v0, v160
	v_bitop3_b32 v2, v160, v0, 32 bitop3:0x36
	v_bitop3_b32 v3, v160, v0, 64 bitop3:0x36
	v_bitop3_b32 v0, v160, v0, s2 bitop3:0x36
	s_add_u32 s2, s18, 0x40000
	s_addc_u32 s3, s19, 0
	s_add_u32 s10, s18, 0x40100
	s_addc_u32 s11, s19, 0
	v_mov_b32_e32 v211, v161
	s_add_i32 s22, 0, 0x4000
	v_lshl_add_u64 v[158:159], s[2:3], 0, v[210:211]
	v_mov_b32_e32 v213, v161
	s_waitcnt vmcnt(1)
	v_lshl_add_u64 v[200:201], s[10:11], 0, v[210:211]
	v_mov_b32_e32 v211, 0
	v_add_u32_e32 v160, s22, v236
	v_lshl_add_u64 v[198:199], s[2:3], 0, v[212:213]
	v_lshl_add_u64 v[202:203], s[10:11], 0, v[212:213]
	s_mov_b64 s[2:3], 0x10000
	s_mov_b64 s[48:49], -1
	v_add_u32_e32 v204, v237, v1
	v_add_u32_e32 v205, v237, v2
	s_waitcnt vmcnt(0)
	v_add_u32_e32 v206, v237, v3
	v_add_u32_e32 v207, v237, v4
	v_add_u32_e32 v208, v237, v5
	v_add_u32_e32 v209, v237, v6
	v_add_u32_e32 v213, v237, v7
	v_add_u32_e32 v214, v237, v0
	v_mov_b32_e32 v0, 0
	v_mov_b32_e32 v1, v211
	v_mov_b32_e32 v2, v211
	v_mov_b32_e32 v3, v211
	v_mov_b32_e32 v4, v211
	v_mov_b32_e32 v5, v211
	v_mov_b32_e32 v6, v211
	v_mov_b32_e32 v7, v211
	v_mov_b32_e32 v8, v211
	v_mov_b32_e32 v9, v211
	v_mov_b32_e32 v10, v211
	v_mov_b32_e32 v11, v211
	v_mov_b32_e32 v12, v211
	v_mov_b32_e32 v13, v211
	v_mov_b32_e32 v14, v211
	v_mov_b32_e32 v15, v211
	v_mov_b32_e32 v16, 0
	v_mov_b32_e32 v17, v211
	v_mov_b32_e32 v18, v211
	v_mov_b32_e32 v19, v211
	v_mov_b32_e32 v20, v211
	v_mov_b32_e32 v21, v211
	v_mov_b32_e32 v22, v211
	v_mov_b32_e32 v23, v211
	v_mov_b32_e32 v24, v211
	v_mov_b32_e32 v25, v211
	v_mov_b32_e32 v26, v211
	v_mov_b32_e32 v27, v211
	v_mov_b32_e32 v28, v211
	v_mov_b32_e32 v29, v211
	v_mov_b32_e32 v30, v211
	v_mov_b32_e32 v31, v211
	v_mov_b32_e32 v32, 0
	v_mov_b32_e32 v33, v211
	v_mov_b32_e32 v34, v211
	v_mov_b32_e32 v35, v211
	v_mov_b32_e32 v36, v211
	v_mov_b32_e32 v37, v211
	v_mov_b32_e32 v38, v211
	v_mov_b32_e32 v39, v211
	v_mov_b32_e32 v40, v211
	v_mov_b32_e32 v41, v211
	v_mov_b32_e32 v42, v211
	v_mov_b32_e32 v43, v211
	v_mov_b32_e32 v44, v211
	v_mov_b32_e32 v45, v211
	v_mov_b32_e32 v46, v211
	v_mov_b32_e32 v47, v211
	v_mov_b32_e32 v48, 0
	v_mov_b32_e32 v49, v211
	v_mov_b32_e32 v50, v211
	v_mov_b32_e32 v51, v211
	v_mov_b32_e32 v52, v211
	v_mov_b32_e32 v53, v211
	v_mov_b32_e32 v54, v211
	v_mov_b32_e32 v55, v211
	v_mov_b32_e32 v56, v211
	v_mov_b32_e32 v57, v211
	v_mov_b32_e32 v58, v211
	v_mov_b32_e32 v59, v211
	v_mov_b32_e32 v60, v211
	v_mov_b32_e32 v61, v211
	v_mov_b32_e32 v62, v211
	v_mov_b32_e32 v63, v211
	s_branch .LBB0_687
	.p2align 6

.LBB0_776:
	s_ashr_i32 s45, s44, 31
	s_lshl_b64 s[22:23], s[44:45], 18
	s_add_u32 s48, s6, s22
	s_addc_u32 s49, s7, s23
	s_ashr_i32 s47, s46, 31
	s_lshl_b64 s[22:23], s[46:47], 18
	s_add_u32 s50, s31, s22
	v_mov_b32_e32 v35, 0
	s_addc_u32 s51, s33, s23
	s_andn2_b64 vcc, exec, s[40:41]
	v_mov_b32_e32 v34, v35
	v_mov_b32_e32 v33, v35
	v_mov_b32_e32 v32, v35
	v_mov_b32_e32 v39, v35
	v_mov_b32_e32 v38, v35
	v_mov_b32_e32 v37, v35
	v_mov_b32_e32 v36, v35
	v_mov_b32_e32 v51, v35
	v_mov_b32_e32 v50, v35
	v_mov_b32_e32 v49, v35
	v_mov_b32_e32 v48, v35
	v_mov_b32_e32 v55, v35
	v_mov_b32_e32 v54, v35
	v_mov_b32_e32 v53, v35
	v_mov_b32_e32 v52, v35
	v_mov_b32_e32 v159, v35
	v_mov_b32_e32 v158, v35
	v_mov_b32_e32 v157, v35
	v_mov_b32_e32 v156, v35
	v_mov_b32_e32 v155, v35
	v_mov_b32_e32 v154, v35
	v_mov_b32_e32 v153, v35
	v_mov_b32_e32 v152, v35
	v_mov_b32_e32 v143, v35
	v_mov_b32_e32 v142, v35
	v_mov_b32_e32 v141, v35
	v_mov_b32_e32 v140, v35
	v_mov_b32_e32 v139, v35
	v_mov_b32_e32 v138, v35
	v_mov_b32_e32 v137, v35
	v_mov_b32_e32 v136, v35
	v_mov_b32_e32 v127, v35
	v_mov_b32_e32 v126, v35
	v_mov_b32_e32 v125, v35
	v_mov_b32_e32 v124, v35
	v_mov_b32_e32 v123, v35
	v_mov_b32_e32 v122, v35
	v_mov_b32_e32 v121, v35
	v_mov_b32_e32 v120, v35
	v_mov_b32_e32 v111, v35
	v_mov_b32_e32 v110, v35
	v_mov_b32_e32 v109, v35
	v_mov_b32_e32 v108, v35
	v_mov_b32_e32 v107, v35
	v_mov_b32_e32 v106, v35
	v_mov_b32_e32 v105, v35
	v_mov_b32_e32 v104, v35
	v_mov_b32_e32 v151, v35
	v_mov_b32_e32 v150, v35
	v_mov_b32_e32 v149, v35
	v_mov_b32_e32 v148, v35
	v_mov_b32_e32 v147, v35
	v_mov_b32_e32 v146, v35
	v_mov_b32_e32 v145, v35
	v_mov_b32_e32 v144, v35
	v_mov_b32_e32 v135, v35
	v_mov_b32_e32 v134, v35
	v_mov_b32_e32 v133, v35
	v_mov_b32_e32 v132, v35
	v_mov_b32_e32 v131, v35
	v_mov_b32_e32 v130, v35
	v_mov_b32_e32 v129, v35
	v_mov_b32_e32 v128, v35
	v_mov_b32_e32 v119, v35
	v_mov_b32_e32 v118, v35
	v_mov_b32_e32 v117, v35
	v_mov_b32_e32 v116, v35
	v_mov_b32_e32 v115, v35
	v_mov_b32_e32 v114, v35
	v_mov_b32_e32 v113, v35
	v_mov_b32_e32 v112, v35
	v_mov_b32_e32 v103, v35
	v_mov_b32_e32 v102, v35
	v_mov_b32_e32 v101, v35
	v_mov_b32_e32 v100, v35
	v_mov_b32_e32 v99, v35
	v_mov_b32_e32 v98, v35
	v_mov_b32_e32 v97, v35
	v_mov_b32_e32 v96, v35
	v_mov_b32_e32 v95, v35
	v_mov_b32_e32 v94, v35
	v_mov_b32_e32 v93, v35
	v_mov_b32_e32 v92, v35
	v_mov_b32_e32 v91, v35
	v_mov_b32_e32 v90, v35
	v_mov_b32_e32 v89, v35
	v_mov_b32_e32 v88, v35
	v_mov_b32_e32 v79, v35
	v_mov_b32_e32 v78, v35
	v_mov_b32_e32 v77, v35
	v_mov_b32_e32 v76, v35
	v_mov_b32_e32 v75, v35
	v_mov_b32_e32 v74, v35
	v_mov_b32_e32 v73, v35
	v_mov_b32_e32 v72, v35
	v_mov_b32_e32 v63, v35
	v_mov_b32_e32 v62, v35
	v_mov_b32_e32 v61, v35
	v_mov_b32_e32 v60, v35
	v_mov_b32_e32 v59, v35
	v_mov_b32_e32 v58, v35
	v_mov_b32_e32 v57, v35
	v_mov_b32_e32 v56, v35
	v_mov_b32_e32 v47, v35
	v_mov_b32_e32 v46, v35
	v_mov_b32_e32 v45, v35
	v_mov_b32_e32 v44, v35
	v_mov_b32_e32 v43, v35
	v_mov_b32_e32 v42, v35
	v_mov_b32_e32 v41, v35
	v_mov_b32_e32 v40, v35
	v_mov_b32_e32 v87, v35
	v_mov_b32_e32 v86, v35
	v_mov_b32_e32 v85, v35
	v_mov_b32_e32 v84, v35
	v_mov_b32_e32 v83, v35
	v_mov_b32_e32 v82, v35
	v_mov_b32_e32 v81, v35
	v_mov_b32_e32 v80, v35
	v_mov_b32_e32 v71, v35
	v_mov_b32_e32 v70, v35
	v_mov_b32_e32 v69, v35
	v_mov_b32_e32 v68, v35
	v_mov_b32_e32 v67, v35
	v_mov_b32_e32 v66, v35
	v_mov_b32_e32 v65, v35
	v_mov_b32_e32 v64, v35
	s_cbranch_vccnz .LBB0_779
	s_and_b64 s[22:23], s[38:39], exec
	s_cselect_b32 s45, s49, s19
	s_cselect_b32 s47, s48, s18
	s_cselect_b32 s92, s51, s3
	s_cselect_b32 s93, s50, s2
	s_add_u32 s18, s18, 0x20080
	s_addc_u32 s19, s19, 0
	s_add_u32 s95, s2, 0x100
	v_mov_b32_e32 v64, 0
	s_addc_u32 vcc_lo, s3, 0
	s_mov_b32 s2, 0
	v_mov_b32_e32 v65, v64
	v_mov_b32_e32 v66, v64
	v_mov_b32_e32 v67, v64
	v_mov_b32_e32 v68, v64
	v_mov_b32_e32 v69, v64
	v_mov_b32_e32 v70, v64
	v_mov_b32_e32 v71, v64
	v_mov_b32_e32 v80, v64
	v_mov_b32_e32 v81, v64
	v_mov_b32_e32 v82, v64
	v_mov_b32_e32 v83, v64
	v_mov_b32_e32 v84, v64
	v_mov_b32_e32 v85, v64
	v_mov_b32_e32 v86, v64
	v_mov_b32_e32 v87, v64
	v_mov_b32_e32 v40, v64
	v_mov_b32_e32 v41, v64
	v_mov_b32_e32 v42, v64
	v_mov_b32_e32 v43, v64
	v_mov_b32_e32 v44, v64
	v_mov_b32_e32 v45, v64
	v_mov_b32_e32 v46, v64
	v_mov_b32_e32 v47, v64
	v_mov_b32_e32 v56, v64
	v_mov_b32_e32 v57, v64
	v_mov_b32_e32 v58, v64
	v_mov_b32_e32 v59, v64
	v_mov_b32_e32 v60, v64
	v_mov_b32_e32 v61, v64
	v_mov_b32_e32 v62, v64
	v_mov_b32_e32 v63, v64
	v_mov_b32_e32 v72, v64
	v_mov_b32_e32 v73, v64
	v_mov_b32_e32 v74, v64
	v_mov_b32_e32 v75, v64
	v_mov_b32_e32 v76, v64
	v_mov_b32_e32 v77, v64
	v_mov_b32_e32 v78, v64
	v_mov_b32_e32 v79, v64
	v_mov_b32_e32 v88, v64
	v_mov_b32_e32 v89, v64
	v_mov_b32_e32 v90, v64
	v_mov_b32_e32 v91, v64
	v_mov_b32_e32 v92, v64
	v_mov_b32_e32 v93, v64
	v_mov_b32_e32 v94, v64
	v_mov_b32_e32 v95, v64
	v_mov_b32_e32 v96, v64
	v_mov_b32_e32 v97, v64
	v_mov_b32_e32 v98, v64
	v_mov_b32_e32 v99, v64
	v_mov_b32_e32 v100, v64
	v_mov_b32_e32 v101, v64
	v_mov_b32_e32 v102, v64
	v_mov_b32_e32 v103, v64
	v_mov_b32_e32 v112, v64
	v_mov_b32_e32 v113, v64
	v_mov_b32_e32 v114, v64
	v_mov_b32_e32 v115, v64
	v_mov_b32_e32 v116, v64
	v_mov_b32_e32 v117, v64
	v_mov_b32_e32 v118, v64
	v_mov_b32_e32 v119, v64
	v_mov_b32_e32 v128, v64
	v_mov_b32_e32 v129, v64
	v_mov_b32_e32 v130, v64
	v_mov_b32_e32 v131, v64
	v_mov_b32_e32 v132, v64
	v_mov_b32_e32 v133, v64
	v_mov_b32_e32 v134, v64
	v_mov_b32_e32 v135, v64
	v_mov_b32_e32 v144, v64
	v_mov_b32_e32 v145, v64
	v_mov_b32_e32 v146, v64
	v_mov_b32_e32 v147, v64
	v_mov_b32_e32 v148, v64
	v_mov_b32_e32 v149, v64
	v_mov_b32_e32 v150, v64
	v_mov_b32_e32 v151, v64
	v_mov_b32_e32 v104, v64
	v_mov_b32_e32 v105, v64
	v_mov_b32_e32 v106, v64
	v_mov_b32_e32 v107, v64
	v_mov_b32_e32 v108, v64
	v_mov_b32_e32 v109, v64
	v_mov_b32_e32 v110, v64
	v_mov_b32_e32 v111, v64
	v_mov_b32_e32 v120, v64
	v_mov_b32_e32 v121, v64
	v_mov_b32_e32 v122, v64
	v_mov_b32_e32 v123, v64
	v_mov_b32_e32 v124, v64
	v_mov_b32_e32 v125, v64
	v_mov_b32_e32 v126, v64
	v_mov_b32_e32 v127, v64
	v_mov_b32_e32 v136, v64
	v_mov_b32_e32 v137, v64
	v_mov_b32_e32 v138, v64
	v_mov_b32_e32 v139, v64
	v_mov_b32_e32 v140, v64
	v_mov_b32_e32 v141, v64
	v_mov_b32_e32 v142, v64
	v_mov_b32_e32 v143, v64
	v_mov_b32_e32 v152, v64
	v_mov_b32_e32 v153, v64
	v_mov_b32_e32 v154, v64
	v_mov_b32_e32 v155, v64
	v_mov_b32_e32 v156, v64
	v_mov_b32_e32 v157, v64
	v_mov_b32_e32 v158, v64
	v_mov_b32_e32 v159, v64
	v_mov_b32_e32 v52, v64
	v_mov_b32_e32 v53, v64
	v_mov_b32_e32 v54, v64
	v_mov_b32_e32 v55, v64
	v_mov_b32_e32 v48, v64
	v_mov_b32_e32 v49, v64
	v_mov_b32_e32 v50, v64
	v_mov_b32_e32 v51, v64
	v_mov_b32_e32 v36, v64
	v_mov_b32_e32 v37, v64
	v_mov_b32_e32 v38, v64
	v_mov_b32_e32 v39, v64
	v_mov_b32_e32 v32, v64
	v_mov_b32_e32 v33, v64
	v_mov_b32_e32 v34, v64
	v_mov_b32_e32 v35, v64
	s_mov_b64 s[4:5], 0x30080
	.p2align 6

.LBB0_863:
	s_lshl_b32 s39, s54, 10
	s_lshl_b32 s44, s86, 8
	s_add_i32 s44, s44, s39
	s_ashr_i32 s45, s44, 31
	s_lshl_b64 s[44:45], s[44:45], 10
	s_add_u32 s74, s31, s44
	s_addc_u32 s75, s33, s45
	s_andn2_b64 vcc, exec, s[48:49]
	s_cbranch_vccnz .LBB0_866
	s_and_b64 s[42:43], s[42:43], exec
	s_cselect_b32 s39, s75, s3
	s_cselect_b32 s42, s74, s2
	s_add_u32 s22, s22, 0xd0080
	s_addc_u32 s23, s23, 0
	s_add_u32 s43, s2, 0x100
	s_addc_u32 s44, s3, 0
	s_mov_b32 s2, 0
	s_mov_b64 s[4:5], 0xd0000
	s_mov_b64 s[12:13], 0x68000
	s_mov_b64 s[64:65], 0x30080
	s_mov_b64 s[72:73], 0x138000
	s_mov_b64 s[88:89], 0x68080
	.p2align 6

.LBB0_1069:
	s_ashr_i32 s19, s18, 31
	s_lshl_b64 s[38:39], s[18:19], 19
	s_add_u32 s50, s31, s38
	s_addc_u32 s51, s33, s39
	s_ashr_i32 s49, s48, 31
	s_lshl_b64 s[38:39], s[48:49], 19
	s_add_u32 s54, s58, s38
	v_mov_b32_e32 v3, 0
	s_addc_u32 s55, s59, s39
	s_andn2_b64 vcc, exec, s[44:45]
	v_mov_b32_e32 v2, v3
	v_mov_b32_e32 v1, v3
	v_mov_b32_e32 v0, v3
	v_mov_b32_e32 v7, v3
	v_mov_b32_e32 v6, v3
	v_mov_b32_e32 v5, v3
	v_mov_b32_e32 v4, v3
	v_mov_b32_e32 v19, v3
	v_mov_b32_e32 v18, v3
	v_mov_b32_e32 v17, v3
	v_mov_b32_e32 v16, v3
	v_mov_b32_e32 v23, v3
	v_mov_b32_e32 v22, v3
	v_mov_b32_e32 v21, v3
	v_mov_b32_e32 v20, v3
	v_mov_b32_e32 v127, v3
	v_mov_b32_e32 v126, v3
	v_mov_b32_e32 v125, v3
	v_mov_b32_e32 v124, v3
	v_mov_b32_e32 v123, v3
	v_mov_b32_e32 v122, v3
	v_mov_b32_e32 v121, v3
	v_mov_b32_e32 v120, v3
	v_mov_b32_e32 v111, v3
	v_mov_b32_e32 v110, v3
	v_mov_b32_e32 v109, v3
	v_mov_b32_e32 v108, v3
	v_mov_b32_e32 v107, v3
	v_mov_b32_e32 v106, v3
	v_mov_b32_e32 v105, v3
	v_mov_b32_e32 v104, v3
	v_mov_b32_e32 v95, v3
	v_mov_b32_e32 v94, v3
	v_mov_b32_e32 v93, v3
	v_mov_b32_e32 v92, v3
	v_mov_b32_e32 v91, v3
	v_mov_b32_e32 v90, v3
	v_mov_b32_e32 v89, v3
	v_mov_b32_e32 v88, v3
	v_mov_b32_e32 v79, v3
	v_mov_b32_e32 v78, v3
	v_mov_b32_e32 v77, v3
	v_mov_b32_e32 v76, v3
	v_mov_b32_e32 v75, v3
	v_mov_b32_e32 v74, v3
	v_mov_b32_e32 v73, v3
	v_mov_b32_e32 v72, v3
	v_mov_b32_e32 v119, v3
	v_mov_b32_e32 v118, v3
	v_mov_b32_e32 v117, v3
	v_mov_b32_e32 v116, v3
	v_mov_b32_e32 v115, v3
	v_mov_b32_e32 v114, v3
	v_mov_b32_e32 v113, v3
	v_mov_b32_e32 v112, v3
	v_mov_b32_e32 v103, v3
	v_mov_b32_e32 v102, v3
	v_mov_b32_e32 v101, v3
	v_mov_b32_e32 v100, v3
	v_mov_b32_e32 v99, v3
	v_mov_b32_e32 v98, v3
	v_mov_b32_e32 v97, v3
	v_mov_b32_e32 v96, v3
	v_mov_b32_e32 v87, v3
	v_mov_b32_e32 v86, v3
	v_mov_b32_e32 v85, v3
	v_mov_b32_e32 v84, v3
	v_mov_b32_e32 v83, v3
	v_mov_b32_e32 v82, v3
	v_mov_b32_e32 v81, v3
	v_mov_b32_e32 v80, v3
	v_mov_b32_e32 v71, v3
	v_mov_b32_e32 v70, v3
	v_mov_b32_e32 v69, v3
	v_mov_b32_e32 v68, v3
	v_mov_b32_e32 v67, v3
	v_mov_b32_e32 v66, v3
	v_mov_b32_e32 v65, v3
	v_mov_b32_e32 v64, v3
	v_mov_b32_e32 v63, v3
	v_mov_b32_e32 v62, v3
	v_mov_b32_e32 v61, v3
	v_mov_b32_e32 v60, v3
	v_mov_b32_e32 v59, v3
	v_mov_b32_e32 v58, v3
	v_mov_b32_e32 v57, v3
	v_mov_b32_e32 v56, v3
	v_mov_b32_e32 v47, v3
	v_mov_b32_e32 v46, v3
	v_mov_b32_e32 v45, v3
	v_mov_b32_e32 v44, v3
	v_mov_b32_e32 v43, v3
	v_mov_b32_e32 v42, v3
	v_mov_b32_e32 v41, v3
	v_mov_b32_e32 v40, v3
	v_mov_b32_e32 v31, v3
	v_mov_b32_e32 v30, v3
	v_mov_b32_e32 v29, v3
	v_mov_b32_e32 v28, v3
	v_mov_b32_e32 v27, v3
	v_mov_b32_e32 v26, v3
	v_mov_b32_e32 v25, v3
	v_mov_b32_e32 v24, v3
	v_mov_b32_e32 v15, v3
	v_mov_b32_e32 v14, v3
	v_mov_b32_e32 v13, v3
	v_mov_b32_e32 v12, v3
	v_mov_b32_e32 v11, v3
	v_mov_b32_e32 v10, v3
	v_mov_b32_e32 v9, v3
	v_mov_b32_e32 v8, v3
	v_mov_b32_e32 v55, v3
	v_mov_b32_e32 v54, v3
	v_mov_b32_e32 v53, v3
	v_mov_b32_e32 v52, v3
	v_mov_b32_e32 v51, v3
	v_mov_b32_e32 v50, v3
	v_mov_b32_e32 v49, v3
	v_mov_b32_e32 v48, v3
	v_mov_b32_e32 v39, v3
	v_mov_b32_e32 v38, v3
	v_mov_b32_e32 v37, v3
	v_mov_b32_e32 v36, v3
	v_mov_b32_e32 v35, v3
	v_mov_b32_e32 v34, v3
	v_mov_b32_e32 v33, v3
	v_mov_b32_e32 v32, v3
	s_cbranch_vccnz .LBB0_1072
	s_and_b64 s[38:39], s[40:41], exec
	s_cselect_b32 s19, s51, s23
	s_cselect_b32 s38, s50, s22
	s_cselect_b32 s39, s55, s3
	s_cselect_b32 s49, s54, s2
	s_add_u32 s74, s22, 0x40080
	s_addc_u32 s75, s23, 0
	s_add_u32 s22, s2, 0x100
	v_mov_b32_e32 v32, 0
	s_addc_u32 s23, s3, 0
	s_mov_b32 s2, 0
	v_mov_b32_e32 v33, v32
	v_mov_b32_e32 v34, v32
	v_mov_b32_e32 v35, v32
	v_mov_b32_e32 v36, v32
	v_mov_b32_e32 v37, v32
	v_mov_b32_e32 v38, v32
	v_mov_b32_e32 v39, v32
	v_mov_b32_e32 v48, v32
	v_mov_b32_e32 v49, v32
	v_mov_b32_e32 v50, v32
	v_mov_b32_e32 v51, v32
	v_mov_b32_e32 v52, v32
	v_mov_b32_e32 v53, v32
	v_mov_b32_e32 v54, v32
	v_mov_b32_e32 v55, v32
	v_mov_b32_e32 v8, v32
	v_mov_b32_e32 v9, v32
	v_mov_b32_e32 v10, v32
	v_mov_b32_e32 v11, v32
	v_mov_b32_e32 v12, v32
	v_mov_b32_e32 v13, v32
	v_mov_b32_e32 v14, v32
	v_mov_b32_e32 v15, v32
	v_mov_b32_e32 v24, v32
	v_mov_b32_e32 v25, v32
	v_mov_b32_e32 v26, v32
	v_mov_b32_e32 v27, v32
	v_mov_b32_e32 v28, v32
	v_mov_b32_e32 v29, v32
	v_mov_b32_e32 v30, v32
	v_mov_b32_e32 v31, v32
	v_mov_b32_e32 v40, v32
	v_mov_b32_e32 v41, v32
	v_mov_b32_e32 v42, v32
	v_mov_b32_e32 v43, v32
	v_mov_b32_e32 v44, v32
	v_mov_b32_e32 v45, v32
	v_mov_b32_e32 v46, v32
	v_mov_b32_e32 v47, v32
	v_mov_b32_e32 v56, v32
	v_mov_b32_e32 v57, v32
	v_mov_b32_e32 v58, v32
	v_mov_b32_e32 v59, v32
	v_mov_b32_e32 v60, v32
	v_mov_b32_e32 v61, v32
	v_mov_b32_e32 v62, v32
	v_mov_b32_e32 v63, v32
	v_mov_b32_e32 v64, v32
	v_mov_b32_e32 v65, v32
	v_mov_b32_e32 v66, v32
	v_mov_b32_e32 v67, v32
	v_mov_b32_e32 v68, v32
	v_mov_b32_e32 v69, v32
	v_mov_b32_e32 v70, v32
	v_mov_b32_e32 v71, v32
	v_mov_b32_e32 v80, v32
	v_mov_b32_e32 v81, v32
	v_mov_b32_e32 v82, v32
	v_mov_b32_e32 v83, v32
	v_mov_b32_e32 v84, v32
	v_mov_b32_e32 v85, v32
	v_mov_b32_e32 v86, v32
	v_mov_b32_e32 v87, v32
	v_mov_b32_e32 v96, v32
	v_mov_b32_e32 v97, v32
	v_mov_b32_e32 v98, v32
	v_mov_b32_e32 v99, v32
	v_mov_b32_e32 v100, v32
	v_mov_b32_e32 v101, v32
	v_mov_b32_e32 v102, v32
	v_mov_b32_e32 v103, v32
	v_mov_b32_e32 v112, v32
	v_mov_b32_e32 v113, v32
	v_mov_b32_e32 v114, v32
	v_mov_b32_e32 v115, v32
	v_mov_b32_e32 v116, v32
	v_mov_b32_e32 v117, v32
	v_mov_b32_e32 v118, v32
	v_mov_b32_e32 v119, v32
	v_mov_b32_e32 v72, v32
	v_mov_b32_e32 v73, v32
	v_mov_b32_e32 v74, v32
	v_mov_b32_e32 v75, v32
	v_mov_b32_e32 v76, v32
	v_mov_b32_e32 v77, v32
	v_mov_b32_e32 v78, v32
	v_mov_b32_e32 v79, v32
	v_mov_b32_e32 v88, v32
	v_mov_b32_e32 v89, v32
	v_mov_b32_e32 v90, v32
	v_mov_b32_e32 v91, v32
	v_mov_b32_e32 v92, v32
	v_mov_b32_e32 v93, v32
	v_mov_b32_e32 v94, v32
	v_mov_b32_e32 v95, v32
	v_mov_b32_e32 v104, v32
	v_mov_b32_e32 v105, v32
	v_mov_b32_e32 v106, v32
	v_mov_b32_e32 v107, v32
	v_mov_b32_e32 v108, v32
	v_mov_b32_e32 v109, v32
	v_mov_b32_e32 v110, v32
	v_mov_b32_e32 v111, v32
	v_mov_b32_e32 v120, v32
	v_mov_b32_e32 v121, v32
	v_mov_b32_e32 v122, v32
	v_mov_b32_e32 v123, v32
	v_mov_b32_e32 v124, v32
	v_mov_b32_e32 v125, v32
	v_mov_b32_e32 v126, v32
	v_mov_b32_e32 v127, v32
	v_mov_b32_e32 v20, v32
	v_mov_b32_e32 v21, v32
	v_mov_b32_e32 v22, v32
	v_mov_b32_e32 v23, v32
	v_mov_b32_e32 v16, v32
	v_mov_b32_e32 v17, v32
	v_mov_b32_e32 v18, v32
	v_mov_b32_e32 v19, v32
	v_mov_b32_e32 v4, v32
	v_mov_b32_e32 v5, v32
	v_mov_b32_e32 v6, v32
	v_mov_b32_e32 v7, v32
	v_mov_b32_e32 v0, v32
	v_mov_b32_e32 v1, v32
	v_mov_b32_e32 v2, v32
	v_mov_b32_e32 v3, v32
	.p2align 6

.LBB0_1092:
	s_ashr_i32 s47, s46, 31
	s_lshl_b64 s[38:39], s[46:47], 19
	s_add_u32 s50, s31, s38
	s_addc_u32 s51, s33, s39
	s_ashr_i32 s49, s48, 31
	s_lshl_b64 s[38:39], s[48:49], 19
	s_add_u32 s54, s58, s38
	v_mov_b32_e32 v3, 0
	s_addc_u32 s55, s59, s39
	s_andn2_b64 vcc, exec, s[42:43]
	v_mov_b32_e32 v2, v3
	v_mov_b32_e32 v1, v3
	v_mov_b32_e32 v0, v3
	v_mov_b32_e32 v7, v3
	v_mov_b32_e32 v6, v3
	v_mov_b32_e32 v5, v3
	v_mov_b32_e32 v4, v3
	v_mov_b32_e32 v19, v3
	v_mov_b32_e32 v18, v3
	v_mov_b32_e32 v17, v3
	v_mov_b32_e32 v16, v3
	v_mov_b32_e32 v23, v3
	v_mov_b32_e32 v22, v3
	v_mov_b32_e32 v21, v3
	v_mov_b32_e32 v20, v3
	v_mov_b32_e32 v127, v3
	v_mov_b32_e32 v126, v3
	v_mov_b32_e32 v125, v3
	v_mov_b32_e32 v124, v3
	v_mov_b32_e32 v123, v3
	v_mov_b32_e32 v122, v3
	v_mov_b32_e32 v121, v3
	v_mov_b32_e32 v120, v3
	v_mov_b32_e32 v111, v3
	v_mov_b32_e32 v110, v3
	v_mov_b32_e32 v109, v3
	v_mov_b32_e32 v108, v3
	v_mov_b32_e32 v107, v3
	v_mov_b32_e32 v106, v3
	v_mov_b32_e32 v105, v3
	v_mov_b32_e32 v104, v3
	v_mov_b32_e32 v95, v3
	v_mov_b32_e32 v94, v3
	v_mov_b32_e32 v93, v3
	v_mov_b32_e32 v92, v3
	v_mov_b32_e32 v91, v3
	v_mov_b32_e32 v90, v3
	v_mov_b32_e32 v89, v3
	v_mov_b32_e32 v88, v3
	v_mov_b32_e32 v79, v3
	v_mov_b32_e32 v78, v3
	v_mov_b32_e32 v77, v3
	v_mov_b32_e32 v76, v3
	v_mov_b32_e32 v75, v3
	v_mov_b32_e32 v74, v3
	v_mov_b32_e32 v73, v3
	v_mov_b32_e32 v72, v3
	v_mov_b32_e32 v119, v3
	v_mov_b32_e32 v118, v3
	v_mov_b32_e32 v117, v3
	v_mov_b32_e32 v116, v3
	v_mov_b32_e32 v115, v3
	v_mov_b32_e32 v114, v3
	v_mov_b32_e32 v113, v3
	v_mov_b32_e32 v112, v3
	v_mov_b32_e32 v103, v3
	v_mov_b32_e32 v102, v3
	v_mov_b32_e32 v101, v3
	v_mov_b32_e32 v100, v3
	v_mov_b32_e32 v99, v3
	v_mov_b32_e32 v98, v3
	v_mov_b32_e32 v97, v3
	v_mov_b32_e32 v96, v3
	v_mov_b32_e32 v87, v3
	v_mov_b32_e32 v86, v3
	v_mov_b32_e32 v85, v3
	v_mov_b32_e32 v84, v3
	v_mov_b32_e32 v83, v3
	v_mov_b32_e32 v82, v3
	v_mov_b32_e32 v81, v3
	v_mov_b32_e32 v80, v3
	v_mov_b32_e32 v71, v3
	v_mov_b32_e32 v70, v3
	v_mov_b32_e32 v69, v3
	v_mov_b32_e32 v68, v3
	v_mov_b32_e32 v67, v3
	v_mov_b32_e32 v66, v3
	v_mov_b32_e32 v65, v3
	v_mov_b32_e32 v64, v3
	v_mov_b32_e32 v63, v3
	v_mov_b32_e32 v62, v3
	v_mov_b32_e32 v61, v3
	v_mov_b32_e32 v60, v3
	v_mov_b32_e32 v59, v3
	v_mov_b32_e32 v58, v3
	v_mov_b32_e32 v57, v3
	v_mov_b32_e32 v56, v3
	v_mov_b32_e32 v47, v3
	v_mov_b32_e32 v46, v3
	v_mov_b32_e32 v45, v3
	v_mov_b32_e32 v44, v3
	v_mov_b32_e32 v43, v3
	v_mov_b32_e32 v42, v3
	v_mov_b32_e32 v41, v3
	v_mov_b32_e32 v40, v3
	v_mov_b32_e32 v31, v3
	v_mov_b32_e32 v30, v3
	v_mov_b32_e32 v29, v3
	v_mov_b32_e32 v28, v3
	v_mov_b32_e32 v27, v3
	v_mov_b32_e32 v26, v3
	v_mov_b32_e32 v25, v3
	v_mov_b32_e32 v24, v3
	v_mov_b32_e32 v15, v3
	v_mov_b32_e32 v14, v3
	v_mov_b32_e32 v13, v3
	v_mov_b32_e32 v12, v3
	v_mov_b32_e32 v11, v3
	v_mov_b32_e32 v10, v3
	v_mov_b32_e32 v9, v3
	v_mov_b32_e32 v8, v3
	v_mov_b32_e32 v55, v3
	v_mov_b32_e32 v54, v3
	v_mov_b32_e32 v53, v3
	v_mov_b32_e32 v52, v3
	v_mov_b32_e32 v51, v3
	v_mov_b32_e32 v50, v3
	v_mov_b32_e32 v49, v3
	v_mov_b32_e32 v48, v3
	v_mov_b32_e32 v39, v3
	v_mov_b32_e32 v38, v3
	v_mov_b32_e32 v37, v3
	v_mov_b32_e32 v36, v3
	v_mov_b32_e32 v35, v3
	v_mov_b32_e32 v34, v3
	v_mov_b32_e32 v33, v3
	v_mov_b32_e32 v32, v3
	s_cbranch_vccnz .LBB0_1095
	s_and_b64 s[38:39], s[40:41], exec
	s_cselect_b32 s38, s51, s23
	s_cselect_b32 s39, s50, s22
	s_cselect_b32 s47, s55, s3
	s_cselect_b32 s49, s54, s2
	s_add_u32 s74, s22, 0x40080
	s_addc_u32 s75, s23, 0
	s_add_u32 s22, s2, 0x100
	v_mov_b32_e32 v32, 0
	s_addc_u32 s23, s3, 0
	s_mov_b32 s2, 0
	v_mov_b32_e32 v33, v32
	v_mov_b32_e32 v34, v32
	v_mov_b32_e32 v35, v32
	v_mov_b32_e32 v36, v32
	v_mov_b32_e32 v37, v32
	v_mov_b32_e32 v38, v32
	v_mov_b32_e32 v39, v32
	v_mov_b32_e32 v48, v32
	v_mov_b32_e32 v49, v32
	v_mov_b32_e32 v50, v32
	v_mov_b32_e32 v51, v32
	v_mov_b32_e32 v52, v32
	v_mov_b32_e32 v53, v32
	v_mov_b32_e32 v54, v32
	v_mov_b32_e32 v55, v32
	v_mov_b32_e32 v8, v32
	v_mov_b32_e32 v9, v32
	v_mov_b32_e32 v10, v32
	v_mov_b32_e32 v11, v32
	v_mov_b32_e32 v12, v32
	v_mov_b32_e32 v13, v32
	v_mov_b32_e32 v14, v32
	v_mov_b32_e32 v15, v32
	v_mov_b32_e32 v24, v32
	v_mov_b32_e32 v25, v32
	v_mov_b32_e32 v26, v32
	v_mov_b32_e32 v27, v32
	v_mov_b32_e32 v28, v32
	v_mov_b32_e32 v29, v32
	v_mov_b32_e32 v30, v32
	v_mov_b32_e32 v31, v32
	v_mov_b32_e32 v40, v32
	v_mov_b32_e32 v41, v32
	v_mov_b32_e32 v42, v32
	v_mov_b32_e32 v43, v32
	v_mov_b32_e32 v44, v32
	v_mov_b32_e32 v45, v32
	v_mov_b32_e32 v46, v32
	v_mov_b32_e32 v47, v32
	v_mov_b32_e32 v56, v32
	v_mov_b32_e32 v57, v32
	v_mov_b32_e32 v58, v32
	v_mov_b32_e32 v59, v32
	v_mov_b32_e32 v60, v32
	v_mov_b32_e32 v61, v32
	v_mov_b32_e32 v62, v32
	v_mov_b32_e32 v63, v32
	v_mov_b32_e32 v64, v32
	v_mov_b32_e32 v65, v32
	v_mov_b32_e32 v66, v32
	v_mov_b32_e32 v67, v32
	v_mov_b32_e32 v68, v32
	v_mov_b32_e32 v69, v32
	v_mov_b32_e32 v70, v32
	v_mov_b32_e32 v71, v32
	v_mov_b32_e32 v80, v32
	v_mov_b32_e32 v81, v32
	v_mov_b32_e32 v82, v32
	v_mov_b32_e32 v83, v32
	v_mov_b32_e32 v84, v32
	v_mov_b32_e32 v85, v32
	v_mov_b32_e32 v86, v32
	v_mov_b32_e32 v87, v32
	v_mov_b32_e32 v96, v32
	v_mov_b32_e32 v97, v32
	v_mov_b32_e32 v98, v32
	v_mov_b32_e32 v99, v32
	v_mov_b32_e32 v100, v32
	v_mov_b32_e32 v101, v32
	v_mov_b32_e32 v102, v32
	v_mov_b32_e32 v103, v32
	v_mov_b32_e32 v112, v32
	v_mov_b32_e32 v113, v32
	v_mov_b32_e32 v114, v32
	v_mov_b32_e32 v115, v32
	v_mov_b32_e32 v116, v32
	v_mov_b32_e32 v117, v32
	v_mov_b32_e32 v118, v32
	v_mov_b32_e32 v119, v32
	v_mov_b32_e32 v72, v32
	v_mov_b32_e32 v73, v32
	v_mov_b32_e32 v74, v32
	v_mov_b32_e32 v75, v32
	v_mov_b32_e32 v76, v32
	v_mov_b32_e32 v77, v32
	v_mov_b32_e32 v78, v32
	v_mov_b32_e32 v79, v32
	v_mov_b32_e32 v88, v32
	v_mov_b32_e32 v89, v32
	v_mov_b32_e32 v90, v32
	v_mov_b32_e32 v91, v32
	v_mov_b32_e32 v92, v32
	v_mov_b32_e32 v93, v32
	v_mov_b32_e32 v94, v32
	v_mov_b32_e32 v95, v32
	v_mov_b32_e32 v104, v32
	v_mov_b32_e32 v105, v32
	v_mov_b32_e32 v106, v32
	v_mov_b32_e32 v107, v32
	v_mov_b32_e32 v108, v32
	v_mov_b32_e32 v109, v32
	v_mov_b32_e32 v110, v32
	v_mov_b32_e32 v111, v32
	v_mov_b32_e32 v120, v32
	v_mov_b32_e32 v121, v32
	v_mov_b32_e32 v122, v32
	v_mov_b32_e32 v123, v32
	v_mov_b32_e32 v124, v32
	v_mov_b32_e32 v125, v32
	v_mov_b32_e32 v126, v32
	v_mov_b32_e32 v127, v32
	v_mov_b32_e32 v20, v32
	v_mov_b32_e32 v21, v32
	v_mov_b32_e32 v22, v32
	v_mov_b32_e32 v23, v32
	v_mov_b32_e32 v16, v32
	v_mov_b32_e32 v17, v32
	v_mov_b32_e32 v18, v32
	v_mov_b32_e32 v19, v32
	v_mov_b32_e32 v4, v32
	v_mov_b32_e32 v5, v32
	v_mov_b32_e32 v6, v32
	v_mov_b32_e32 v7, v32
	v_mov_b32_e32 v0, v32
	v_mov_b32_e32 v1, v32
	v_mov_b32_e32 v2, v32
	v_mov_b32_e32 v3, v32
	.p2align 6

.LBB0_1230:
	s_ashr_i32 s45, s44, 31
	s_lshl_b64 s[38:39], s[44:45], 19
	s_add_u32 s48, s10, s38
	s_addc_u32 s49, s11, s39
	s_ashr_i32 s47, s46, 31
	s_lshl_b64 s[38:39], s[46:47], 19
	s_add_u32 s50, s6, s38
	v_mov_b32_e32 v3, 0
	s_addc_u32 s51, s7, s39
	s_andn2_b64 vcc, exec, s[40:41]
	v_mov_b32_e32 v2, v3
	v_mov_b32_e32 v1, v3
	v_mov_b32_e32 v0, v3
	v_mov_b32_e32 v11, v3
	v_mov_b32_e32 v10, v3
	v_mov_b32_e32 v9, v3
	v_mov_b32_e32 v8, v3
	v_mov_b32_e32 v19, v3
	v_mov_b32_e32 v18, v3
	v_mov_b32_e32 v17, v3
	v_mov_b32_e32 v16, v3
	v_mov_b32_e32 v27, v3
	v_mov_b32_e32 v26, v3
	v_mov_b32_e32 v25, v3
	v_mov_b32_e32 v24, v3
	v_mov_b32_e32 v127, v3
	v_mov_b32_e32 v126, v3
	v_mov_b32_e32 v125, v3
	v_mov_b32_e32 v124, v3
	v_mov_b32_e32 v119, v3
	v_mov_b32_e32 v118, v3
	v_mov_b32_e32 v117, v3
	v_mov_b32_e32 v116, v3
	v_mov_b32_e32 v111, v3
	v_mov_b32_e32 v110, v3
	v_mov_b32_e32 v109, v3
	v_mov_b32_e32 v108, v3
	v_mov_b32_e32 v103, v3
	v_mov_b32_e32 v102, v3
	v_mov_b32_e32 v101, v3
	v_mov_b32_e32 v100, v3
	v_mov_b32_e32 v95, v3
	v_mov_b32_e32 v94, v3
	v_mov_b32_e32 v93, v3
	v_mov_b32_e32 v92, v3
	v_mov_b32_e32 v87, v3
	v_mov_b32_e32 v86, v3
	v_mov_b32_e32 v85, v3
	v_mov_b32_e32 v84, v3
	v_mov_b32_e32 v79, v3
	v_mov_b32_e32 v78, v3
	v_mov_b32_e32 v77, v3
	v_mov_b32_e32 v76, v3
	v_mov_b32_e32 v71, v3
	v_mov_b32_e32 v70, v3
	v_mov_b32_e32 v69, v3
	v_mov_b32_e32 v68, v3
	v_mov_b32_e32 v123, v3
	v_mov_b32_e32 v122, v3
	v_mov_b32_e32 v121, v3
	v_mov_b32_e32 v120, v3
	v_mov_b32_e32 v115, v3
	v_mov_b32_e32 v114, v3
	v_mov_b32_e32 v113, v3
	v_mov_b32_e32 v112, v3
	v_mov_b32_e32 v107, v3
	v_mov_b32_e32 v106, v3
	v_mov_b32_e32 v105, v3
	v_mov_b32_e32 v104, v3
	v_mov_b32_e32 v99, v3
	v_mov_b32_e32 v98, v3
	v_mov_b32_e32 v97, v3
	v_mov_b32_e32 v96, v3
	v_mov_b32_e32 v91, v3
	v_mov_b32_e32 v90, v3
	v_mov_b32_e32 v89, v3
	v_mov_b32_e32 v88, v3
	v_mov_b32_e32 v83, v3
	v_mov_b32_e32 v82, v3
	v_mov_b32_e32 v81, v3
	v_mov_b32_e32 v80, v3
	v_mov_b32_e32 v75, v3
	v_mov_b32_e32 v74, v3
	v_mov_b32_e32 v73, v3
	v_mov_b32_e32 v72, v3
	v_mov_b32_e32 v67, v3
	v_mov_b32_e32 v66, v3
	v_mov_b32_e32 v65, v3
	v_mov_b32_e32 v64, v3
	v_mov_b32_e32 v63, v3
	v_mov_b32_e32 v62, v3
	v_mov_b32_e32 v61, v3
	v_mov_b32_e32 v60, v3
	v_mov_b32_e32 v55, v3
	v_mov_b32_e32 v54, v3
	v_mov_b32_e32 v53, v3
	v_mov_b32_e32 v52, v3
	v_mov_b32_e32 v47, v3
	v_mov_b32_e32 v46, v3
	v_mov_b32_e32 v45, v3
	v_mov_b32_e32 v44, v3
	v_mov_b32_e32 v39, v3
	v_mov_b32_e32 v38, v3
	v_mov_b32_e32 v37, v3
	v_mov_b32_e32 v36, v3
	v_mov_b32_e32 v31, v3
	v_mov_b32_e32 v30, v3
	v_mov_b32_e32 v29, v3
	v_mov_b32_e32 v28, v3
	v_mov_b32_e32 v23, v3
	v_mov_b32_e32 v22, v3
	v_mov_b32_e32 v21, v3
	v_mov_b32_e32 v20, v3
	v_mov_b32_e32 v15, v3
	v_mov_b32_e32 v14, v3
	v_mov_b32_e32 v13, v3
	v_mov_b32_e32 v12, v3
	v_mov_b32_e32 v7, v3
	v_mov_b32_e32 v6, v3
	v_mov_b32_e32 v5, v3
	v_mov_b32_e32 v4, v3
	v_mov_b32_e32 v59, v3
	v_mov_b32_e32 v58, v3
	v_mov_b32_e32 v57, v3
	v_mov_b32_e32 v56, v3
	v_mov_b32_e32 v51, v3
	v_mov_b32_e32 v50, v3
	v_mov_b32_e32 v49, v3
	v_mov_b32_e32 v48, v3
	v_mov_b32_e32 v43, v3
	v_mov_b32_e32 v42, v3
	v_mov_b32_e32 v41, v3
	v_mov_b32_e32 v40, v3
	v_mov_b32_e32 v35, v3
	v_mov_b32_e32 v34, v3
	v_mov_b32_e32 v33, v3
	v_mov_b32_e32 v32, v3
	s_cbranch_vccnz .LBB0_1233
	s_and_b64 s[38:39], s[36:37], exec
	s_cselect_b32 s38, s49, s23
	s_cselect_b32 s39, s48, s22
	s_cselect_b32 s45, s51, s3
	s_cselect_b32 s47, s50, s2
	s_add_u32 s54, s22, 0x40080
	s_addc_u32 s55, s23, 0
	s_add_u32 s22, s2, 0x100
	v_mov_b32_e32 v32, 0
	s_addc_u32 s23, s3, 0
	s_mov_b32 s2, 0
	v_mov_b32_e32 v33, v32
	v_mov_b32_e32 v34, v32
	v_mov_b32_e32 v35, v32
	v_mov_b32_e32 v40, v32
	v_mov_b32_e32 v41, v32
	v_mov_b32_e32 v42, v32
	v_mov_b32_e32 v43, v32
	v_mov_b32_e32 v48, v32
	v_mov_b32_e32 v49, v32
	v_mov_b32_e32 v50, v32
	v_mov_b32_e32 v51, v32
	v_mov_b32_e32 v56, v32
	v_mov_b32_e32 v57, v32
	v_mov_b32_e32 v58, v32
	v_mov_b32_e32 v59, v32
	v_mov_b32_e32 v4, v32
	v_mov_b32_e32 v5, v32
	v_mov_b32_e32 v6, v32
	v_mov_b32_e32 v7, v32
	v_mov_b32_e32 v12, v32
	v_mov_b32_e32 v13, v32
	v_mov_b32_e32 v14, v32
	v_mov_b32_e32 v15, v32
	v_mov_b32_e32 v20, v32
	v_mov_b32_e32 v21, v32
	v_mov_b32_e32 v22, v32
	v_mov_b32_e32 v23, v32
	v_mov_b32_e32 v28, v32
	v_mov_b32_e32 v29, v32
	v_mov_b32_e32 v30, v32
	v_mov_b32_e32 v31, v32
	v_mov_b32_e32 v36, v32
	v_mov_b32_e32 v37, v32
	v_mov_b32_e32 v38, v32
	v_mov_b32_e32 v39, v32
	v_mov_b32_e32 v44, v32
	v_mov_b32_e32 v45, v32
	v_mov_b32_e32 v46, v32
	v_mov_b32_e32 v47, v32
	v_mov_b32_e32 v52, v32
	v_mov_b32_e32 v53, v32
	v_mov_b32_e32 v54, v32
	v_mov_b32_e32 v55, v32
	v_mov_b32_e32 v60, v32
	v_mov_b32_e32 v61, v32
	v_mov_b32_e32 v62, v32
	v_mov_b32_e32 v63, v32
	v_mov_b32_e32 v64, v32
	v_mov_b32_e32 v65, v32
	v_mov_b32_e32 v66, v32
	v_mov_b32_e32 v67, v32
	v_mov_b32_e32 v72, v32
	v_mov_b32_e32 v73, v32
	v_mov_b32_e32 v74, v32
	v_mov_b32_e32 v75, v32
	v_mov_b32_e32 v80, v32
	v_mov_b32_e32 v81, v32
	v_mov_b32_e32 v82, v32
	v_mov_b32_e32 v83, v32
	v_mov_b32_e32 v88, v32
	v_mov_b32_e32 v89, v32
	v_mov_b32_e32 v90, v32
	v_mov_b32_e32 v91, v32
	v_mov_b32_e32 v96, v32
	v_mov_b32_e32 v97, v32
	v_mov_b32_e32 v98, v32
	v_mov_b32_e32 v99, v32
	v_mov_b32_e32 v104, v32
	v_mov_b32_e32 v105, v32
	v_mov_b32_e32 v106, v32
	v_mov_b32_e32 v107, v32
	v_mov_b32_e32 v112, v32
	v_mov_b32_e32 v113, v32
	v_mov_b32_e32 v114, v32
	v_mov_b32_e32 v115, v32
	v_mov_b32_e32 v120, v32
	v_mov_b32_e32 v121, v32
	v_mov_b32_e32 v122, v32
	v_mov_b32_e32 v123, v32
	v_mov_b32_e32 v68, v32
	v_mov_b32_e32 v69, v32
	v_mov_b32_e32 v70, v32
	v_mov_b32_e32 v71, v32
	v_mov_b32_e32 v76, v32
	v_mov_b32_e32 v77, v32
	v_mov_b32_e32 v78, v32
	v_mov_b32_e32 v79, v32
	v_mov_b32_e32 v84, v32
	v_mov_b32_e32 v85, v32
	v_mov_b32_e32 v86, v32
	v_mov_b32_e32 v87, v32
	v_mov_b32_e32 v92, v32
	v_mov_b32_e32 v93, v32
	v_mov_b32_e32 v94, v32
	v_mov_b32_e32 v95, v32
	v_mov_b32_e32 v100, v32
	v_mov_b32_e32 v101, v32
	v_mov_b32_e32 v102, v32
	v_mov_b32_e32 v103, v32
	v_mov_b32_e32 v108, v32
	v_mov_b32_e32 v109, v32
	v_mov_b32_e32 v110, v32
	v_mov_b32_e32 v111, v32
	v_mov_b32_e32 v116, v32
	v_mov_b32_e32 v117, v32
	v_mov_b32_e32 v118, v32
	v_mov_b32_e32 v119, v32
	v_mov_b32_e32 v124, v32
	v_mov_b32_e32 v125, v32
	v_mov_b32_e32 v126, v32
	v_mov_b32_e32 v127, v32
	v_mov_b32_e32 v24, v32
	v_mov_b32_e32 v25, v32
	v_mov_b32_e32 v26, v32
	v_mov_b32_e32 v27, v32
	v_mov_b32_e32 v16, v32
	v_mov_b32_e32 v17, v32
	v_mov_b32_e32 v18, v32
	v_mov_b32_e32 v19, v32
	v_mov_b32_e32 v8, v32
	v_mov_b32_e32 v9, v32
	v_mov_b32_e32 v10, v32
	v_mov_b32_e32 v11, v32
	v_mov_b32_e32 v0, v32
	v_mov_b32_e32 v1, v32
	v_mov_b32_e32 v2, v32
	v_mov_b32_e32 v3, v32
	.p2align 6

.LBB0_1309:
	v_mov_b32_e32 v3, 0
	s_andn2_b64 vcc, exec, s[42:43]
	v_mov_b32_e32 v2, v3
	v_mov_b32_e32 v1, v3
	v_mov_b32_e32 v0, v3
	v_mov_b32_e32 v7, v3
	v_mov_b32_e32 v6, v3
	v_mov_b32_e32 v5, v3
	v_mov_b32_e32 v4, v3
	v_mov_b32_e32 v19, v3
	v_mov_b32_e32 v18, v3
	v_mov_b32_e32 v17, v3
	v_mov_b32_e32 v16, v3
	v_mov_b32_e32 v23, v3
	v_mov_b32_e32 v22, v3
	v_mov_b32_e32 v21, v3
	v_mov_b32_e32 v20, v3
	v_mov_b32_e32 v127, v3
	v_mov_b32_e32 v126, v3
	v_mov_b32_e32 v125, v3
	v_mov_b32_e32 v124, v3
	v_mov_b32_e32 v123, v3
	v_mov_b32_e32 v122, v3
	v_mov_b32_e32 v121, v3
	v_mov_b32_e32 v120, v3
	v_mov_b32_e32 v111, v3
	v_mov_b32_e32 v110, v3
	v_mov_b32_e32 v109, v3
	v_mov_b32_e32 v108, v3
	v_mov_b32_e32 v107, v3
	v_mov_b32_e32 v106, v3
	v_mov_b32_e32 v105, v3
	v_mov_b32_e32 v104, v3
	v_mov_b32_e32 v95, v3
	v_mov_b32_e32 v94, v3
	v_mov_b32_e32 v93, v3
	v_mov_b32_e32 v92, v3
	v_mov_b32_e32 v91, v3
	v_mov_b32_e32 v90, v3
	v_mov_b32_e32 v89, v3
	v_mov_b32_e32 v88, v3
	v_mov_b32_e32 v79, v3
	v_mov_b32_e32 v78, v3
	v_mov_b32_e32 v77, v3
	v_mov_b32_e32 v76, v3
	v_mov_b32_e32 v75, v3
	v_mov_b32_e32 v74, v3
	v_mov_b32_e32 v73, v3
	v_mov_b32_e32 v72, v3
	v_mov_b32_e32 v119, v3
	v_mov_b32_e32 v118, v3
	v_mov_b32_e32 v117, v3
	v_mov_b32_e32 v116, v3
	v_mov_b32_e32 v115, v3
	v_mov_b32_e32 v114, v3
	v_mov_b32_e32 v113, v3
	v_mov_b32_e32 v112, v3
	v_mov_b32_e32 v103, v3
	v_mov_b32_e32 v102, v3
	v_mov_b32_e32 v101, v3
	v_mov_b32_e32 v100, v3
	v_mov_b32_e32 v99, v3
	v_mov_b32_e32 v98, v3
	v_mov_b32_e32 v97, v3
	v_mov_b32_e32 v96, v3
	v_mov_b32_e32 v87, v3
	v_mov_b32_e32 v86, v3
	v_mov_b32_e32 v85, v3
	v_mov_b32_e32 v84, v3
	v_mov_b32_e32 v83, v3
	v_mov_b32_e32 v82, v3
	v_mov_b32_e32 v81, v3
	v_mov_b32_e32 v80, v3
	v_mov_b32_e32 v71, v3
	v_mov_b32_e32 v70, v3
	v_mov_b32_e32 v69, v3
	v_mov_b32_e32 v68, v3
	v_mov_b32_e32 v67, v3
	v_mov_b32_e32 v66, v3
	v_mov_b32_e32 v65, v3
	v_mov_b32_e32 v64, v3
	v_mov_b32_e32 v63, v3
	v_mov_b32_e32 v62, v3
	v_mov_b32_e32 v61, v3
	v_mov_b32_e32 v60, v3
	v_mov_b32_e32 v59, v3
	v_mov_b32_e32 v58, v3
	v_mov_b32_e32 v57, v3
	v_mov_b32_e32 v56, v3
	v_mov_b32_e32 v47, v3
	v_mov_b32_e32 v46, v3
	v_mov_b32_e32 v45, v3
	v_mov_b32_e32 v44, v3
	v_mov_b32_e32 v43, v3
	v_mov_b32_e32 v42, v3
	v_mov_b32_e32 v41, v3
	v_mov_b32_e32 v40, v3
	v_mov_b32_e32 v31, v3
	v_mov_b32_e32 v30, v3
	v_mov_b32_e32 v29, v3
	v_mov_b32_e32 v28, v3
	v_mov_b32_e32 v27, v3
	v_mov_b32_e32 v26, v3
	v_mov_b32_e32 v25, v3
	v_mov_b32_e32 v24, v3
	v_mov_b32_e32 v15, v3
	v_mov_b32_e32 v14, v3
	v_mov_b32_e32 v13, v3
	v_mov_b32_e32 v12, v3
	v_mov_b32_e32 v11, v3
	v_mov_b32_e32 v10, v3
	v_mov_b32_e32 v9, v3
	v_mov_b32_e32 v8, v3
	v_mov_b32_e32 v55, v3
	v_mov_b32_e32 v54, v3
	v_mov_b32_e32 v53, v3
	v_mov_b32_e32 v52, v3
	v_mov_b32_e32 v51, v3
	v_mov_b32_e32 v50, v3
	v_mov_b32_e32 v49, v3
	v_mov_b32_e32 v48, v3
	v_mov_b32_e32 v39, v3
	v_mov_b32_e32 v38, v3
	v_mov_b32_e32 v37, v3
	v_mov_b32_e32 v36, v3
	v_mov_b32_e32 v35, v3
	v_mov_b32_e32 v34, v3
	v_mov_b32_e32 v33, v3
	v_mov_b32_e32 v32, v3
	s_cbranch_vccnz .LBB0_1312
	s_add_u32 s46, s22, 0xe0080
	s_addc_u32 s47, s23, 0
	s_add_u32 s22, s2, 0x100
	v_mov_b32_e32 v32, 0
	s_addc_u32 s23, s3, 0
	s_mov_b32 s2, 0
	v_mov_b32_e32 v33, v32
	v_mov_b32_e32 v34, v32
	v_mov_b32_e32 v35, v32
	v_mov_b32_e32 v36, v32
	v_mov_b32_e32 v37, v32
	v_mov_b32_e32 v38, v32
	v_mov_b32_e32 v39, v32
	v_mov_b32_e32 v48, v32
	v_mov_b32_e32 v49, v32
	v_mov_b32_e32 v50, v32
	v_mov_b32_e32 v51, v32
	v_mov_b32_e32 v52, v32
	v_mov_b32_e32 v53, v32
	v_mov_b32_e32 v54, v32
	v_mov_b32_e32 v55, v32
	v_mov_b32_e32 v8, v32
	v_mov_b32_e32 v9, v32
	v_mov_b32_e32 v10, v32
	v_mov_b32_e32 v11, v32
	v_mov_b32_e32 v12, v32
	v_mov_b32_e32 v13, v32
	v_mov_b32_e32 v14, v32
	v_mov_b32_e32 v15, v32
	v_mov_b32_e32 v24, v32
	v_mov_b32_e32 v25, v32
	v_mov_b32_e32 v26, v32
	v_mov_b32_e32 v27, v32
	v_mov_b32_e32 v28, v32
	v_mov_b32_e32 v29, v32
	v_mov_b32_e32 v30, v32
	v_mov_b32_e32 v31, v32
	v_mov_b32_e32 v40, v32
	v_mov_b32_e32 v41, v32
	v_mov_b32_e32 v42, v32
	v_mov_b32_e32 v43, v32
	v_mov_b32_e32 v44, v32
	v_mov_b32_e32 v45, v32
	v_mov_b32_e32 v46, v32
	v_mov_b32_e32 v47, v32
	v_mov_b32_e32 v56, v32
	v_mov_b32_e32 v57, v32
	v_mov_b32_e32 v58, v32
	v_mov_b32_e32 v59, v32
	v_mov_b32_e32 v60, v32
	v_mov_b32_e32 v61, v32
	v_mov_b32_e32 v62, v32
	v_mov_b32_e32 v63, v32
	v_mov_b32_e32 v64, v32
	v_mov_b32_e32 v65, v32
	v_mov_b32_e32 v66, v32
	v_mov_b32_e32 v67, v32
	v_mov_b32_e32 v68, v32
	v_mov_b32_e32 v69, v32
	v_mov_b32_e32 v70, v32
	v_mov_b32_e32 v71, v32
	v_mov_b32_e32 v80, v32
	v_mov_b32_e32 v81, v32
	v_mov_b32_e32 v82, v32
	v_mov_b32_e32 v83, v32
	v_mov_b32_e32 v84, v32
	v_mov_b32_e32 v85, v32
	v_mov_b32_e32 v86, v32
	v_mov_b32_e32 v87, v32
	v_mov_b32_e32 v96, v32
	v_mov_b32_e32 v97, v32
	v_mov_b32_e32 v98, v32
	v_mov_b32_e32 v99, v32
	v_mov_b32_e32 v100, v32
	v_mov_b32_e32 v101, v32
	v_mov_b32_e32 v102, v32
	v_mov_b32_e32 v103, v32
	v_mov_b32_e32 v112, v32
	v_mov_b32_e32 v113, v32
	v_mov_b32_e32 v114, v32
	v_mov_b32_e32 v115, v32
	v_mov_b32_e32 v116, v32
	v_mov_b32_e32 v117, v32
	v_mov_b32_e32 v118, v32
	v_mov_b32_e32 v119, v32
	v_mov_b32_e32 v72, v32
	v_mov_b32_e32 v73, v32
	v_mov_b32_e32 v74, v32
	v_mov_b32_e32 v75, v32
	v_mov_b32_e32 v76, v32
	v_mov_b32_e32 v77, v32
	v_mov_b32_e32 v78, v32
	v_mov_b32_e32 v79, v32
	v_mov_b32_e32 v88, v32
	v_mov_b32_e32 v89, v32
	v_mov_b32_e32 v90, v32
	v_mov_b32_e32 v91, v32
	v_mov_b32_e32 v92, v32
	v_mov_b32_e32 v93, v32
	v_mov_b32_e32 v94, v32
	v_mov_b32_e32 v95, v32
	v_mov_b32_e32 v104, v32
	v_mov_b32_e32 v105, v32
	v_mov_b32_e32 v106, v32
	v_mov_b32_e32 v107, v32
	v_mov_b32_e32 v108, v32
	v_mov_b32_e32 v109, v32
	v_mov_b32_e32 v110, v32
	v_mov_b32_e32 v111, v32
	v_mov_b32_e32 v120, v32
	v_mov_b32_e32 v121, v32
	v_mov_b32_e32 v122, v32
	v_mov_b32_e32 v123, v32
	v_mov_b32_e32 v124, v32
	v_mov_b32_e32 v125, v32
	v_mov_b32_e32 v126, v32
	v_mov_b32_e32 v127, v32
	v_mov_b32_e32 v20, v32
	v_mov_b32_e32 v21, v32
	v_mov_b32_e32 v22, v32
	v_mov_b32_e32 v23, v32
	v_mov_b32_e32 v16, v32
	v_mov_b32_e32 v17, v32
	v_mov_b32_e32 v18, v32
	v_mov_b32_e32 v19, v32
	v_mov_b32_e32 v4, v32
	v_mov_b32_e32 v5, v32
	v_mov_b32_e32 v6, v32
	v_mov_b32_e32 v7, v32
	v_mov_b32_e32 v0, v32
	v_mov_b32_e32 v1, v32
	v_mov_b32_e32 v2, v32
	v_mov_b32_e32 v3, v32
	s_mov_b64 s[4:5], 0xe0000
	s_mov_b64 s[12:13], 0x150000
	s_mov_b64 s[64:65], 0x70080
	s_mov_b64 s[72:73], 0xe0080
	s_mov_b64 s[86:87], 0x150080
	s_mov_b64 s[84:85], 0x70000
	.p2align 6

.LBB0_1534:
	s_ashr_i32 s49, s48, 31
	s_lshl_b64 s[34:35], s[48:49], 18
	s_add_u32 s54, s63, s34
	v_mov_b32_e32 v47, 0
	s_addc_u32 s55, s77, s35
	s_andn2_b64 vcc, exec, s[42:43]
	v_mov_b32_e32 v46, v47
	v_mov_b32_e32 v45, v47
	v_mov_b32_e32 v44, v47
	v_mov_b32_e32 v43, v47
	v_mov_b32_e32 v42, v47
	v_mov_b32_e32 v41, v47
	v_mov_b32_e32 v40, v47
	v_mov_b32_e32 v55, v47
	v_mov_b32_e32 v54, v47
	v_mov_b32_e32 v53, v47
	v_mov_b32_e32 v52, v47
	v_mov_b32_e32 v63, v47
	v_mov_b32_e32 v62, v47
	v_mov_b32_e32 v61, v47
	v_mov_b32_e32 v60, v47
	v_mov_b32_e32 v155, v47
	v_mov_b32_e32 v154, v47
	v_mov_b32_e32 v153, v47
	v_mov_b32_e32 v152, v47
	v_mov_b32_e32 v147, v47
	v_mov_b32_e32 v146, v47
	v_mov_b32_e32 v145, v47
	v_mov_b32_e32 v144, v47
	v_mov_b32_e32 v139, v47
	v_mov_b32_e32 v138, v47
	v_mov_b32_e32 v137, v47
	v_mov_b32_e32 v136, v47
	v_mov_b32_e32 v131, v47
	v_mov_b32_e32 v130, v47
	v_mov_b32_e32 v129, v47
	v_mov_b32_e32 v128, v47
	v_mov_b32_e32 v123, v47
	v_mov_b32_e32 v122, v47
	v_mov_b32_e32 v121, v47
	v_mov_b32_e32 v120, v47
	v_mov_b32_e32 v115, v47
	v_mov_b32_e32 v114, v47
	v_mov_b32_e32 v113, v47
	v_mov_b32_e32 v112, v47
	v_mov_b32_e32 v107, v47
	v_mov_b32_e32 v106, v47
	v_mov_b32_e32 v105, v47
	v_mov_b32_e32 v104, v47
	v_mov_b32_e32 v99, v47
	v_mov_b32_e32 v98, v47
	v_mov_b32_e32 v97, v47
	v_mov_b32_e32 v96, v47
	v_mov_b32_e32 v159, v47
	v_mov_b32_e32 v158, v47
	v_mov_b32_e32 v157, v47
	v_mov_b32_e32 v156, v47
	v_mov_b32_e32 v151, v47
	v_mov_b32_e32 v150, v47
	v_mov_b32_e32 v149, v47
	v_mov_b32_e32 v148, v47
	v_mov_b32_e32 v143, v47
	v_mov_b32_e32 v142, v47
	v_mov_b32_e32 v141, v47
	v_mov_b32_e32 v140, v47
	v_mov_b32_e32 v135, v47
	v_mov_b32_e32 v134, v47
	v_mov_b32_e32 v133, v47
	v_mov_b32_e32 v132, v47
	v_mov_b32_e32 v127, v47
	v_mov_b32_e32 v126, v47
	v_mov_b32_e32 v125, v47
	v_mov_b32_e32 v124, v47
	v_mov_b32_e32 v119, v47
	v_mov_b32_e32 v118, v47
	v_mov_b32_e32 v117, v47
	v_mov_b32_e32 v116, v47
	v_mov_b32_e32 v111, v47
	v_mov_b32_e32 v110, v47
	v_mov_b32_e32 v109, v47
	v_mov_b32_e32 v108, v47
	v_mov_b32_e32 v103, v47
	v_mov_b32_e32 v102, v47
	v_mov_b32_e32 v101, v47
	v_mov_b32_e32 v100, v47
	v_mov_b32_e32 v91, v47
	v_mov_b32_e32 v90, v47
	v_mov_b32_e32 v89, v47
	v_mov_b32_e32 v88, v47
	v_mov_b32_e32 v83, v47
	v_mov_b32_e32 v82, v47
	v_mov_b32_e32 v81, v47
	v_mov_b32_e32 v80, v47
	v_mov_b32_e32 v75, v47
	v_mov_b32_e32 v74, v47
	v_mov_b32_e32 v73, v47
	v_mov_b32_e32 v72, v47
	v_mov_b32_e32 v67, v47
	v_mov_b32_e32 v66, v47
	v_mov_b32_e32 v65, v47
	v_mov_b32_e32 v64, v47
	v_mov_b32_e32 v59, v47
	v_mov_b32_e32 v58, v47
	v_mov_b32_e32 v57, v47
	v_mov_b32_e32 v56, v47
	v_mov_b32_e32 v51, v47
	v_mov_b32_e32 v50, v47
	v_mov_b32_e32 v49, v47
	v_mov_b32_e32 v48, v47
	v_mov_b32_e32 v39, v47
	v_mov_b32_e32 v38, v47
	v_mov_b32_e32 v37, v47
	v_mov_b32_e32 v36, v47
	v_mov_b32_e32 v35, v47
	v_mov_b32_e32 v34, v47
	v_mov_b32_e32 v33, v47
	v_mov_b32_e32 v32, v47
	v_mov_b32_e32 v95, v47
	v_mov_b32_e32 v94, v47
	v_mov_b32_e32 v93, v47
	v_mov_b32_e32 v92, v47
	v_mov_b32_e32 v87, v47
	v_mov_b32_e32 v86, v47
	v_mov_b32_e32 v85, v47
	v_mov_b32_e32 v84, v47
	v_mov_b32_e32 v79, v47
	v_mov_b32_e32 v78, v47
	v_mov_b32_e32 v77, v47
	v_mov_b32_e32 v76, v47
	v_mov_b32_e32 v71, v47
	v_mov_b32_e32 v70, v47
	v_mov_b32_e32 v69, v47
	v_mov_b32_e32 v68, v47
	s_cbranch_vccnz .LBB0_1537
	s_and_b64 s[34:35], s[38:39], exec
	s_cselect_b32 s47, s55, s23
	s_cselect_b32 s49, s54, s22
	s_add_u32 vcc_lo, s2, 0x100
	s_addc_u32 vcc_hi, s3, 0
	s_add_u32 s38, s22, 0x20080
	v_mov_b32_e32 v68, 0
	s_addc_u32 s39, s23, 0
	s_mov_b32 s2, 0
	v_mov_b32_e32 v69, v68
	v_mov_b32_e32 v70, v68
	v_mov_b32_e32 v71, v68
	v_mov_b32_e32 v76, v68
	v_mov_b32_e32 v77, v68
	v_mov_b32_e32 v78, v68
	v_mov_b32_e32 v79, v68
	v_mov_b32_e32 v84, v68
	v_mov_b32_e32 v85, v68
	v_mov_b32_e32 v86, v68
	v_mov_b32_e32 v87, v68
	v_mov_b32_e32 v92, v68
	v_mov_b32_e32 v93, v68
	v_mov_b32_e32 v94, v68
	v_mov_b32_e32 v95, v68
	v_mov_b32_e32 v32, v68
	v_mov_b32_e32 v33, v68
	v_mov_b32_e32 v34, v68
	v_mov_b32_e32 v35, v68
	v_mov_b32_e32 v36, v68
	v_mov_b32_e32 v37, v68
	v_mov_b32_e32 v38, v68
	v_mov_b32_e32 v39, v68
	v_mov_b32_e32 v48, v68
	v_mov_b32_e32 v49, v68
	v_mov_b32_e32 v50, v68
	v_mov_b32_e32 v51, v68
	v_mov_b32_e32 v56, v68
	v_mov_b32_e32 v57, v68
	v_mov_b32_e32 v58, v68
	v_mov_b32_e32 v59, v68
	v_mov_b32_e32 v64, v68
	v_mov_b32_e32 v65, v68
	v_mov_b32_e32 v66, v68
	v_mov_b32_e32 v67, v68
	v_mov_b32_e32 v72, v68
	v_mov_b32_e32 v73, v68
	v_mov_b32_e32 v74, v68
	v_mov_b32_e32 v75, v68
	v_mov_b32_e32 v80, v68
	v_mov_b32_e32 v81, v68
	v_mov_b32_e32 v82, v68
	v_mov_b32_e32 v83, v68
	v_mov_b32_e32 v88, v68
	v_mov_b32_e32 v89, v68
	v_mov_b32_e32 v90, v68
	v_mov_b32_e32 v91, v68
	v_mov_b32_e32 v100, v68
	v_mov_b32_e32 v101, v68
	v_mov_b32_e32 v102, v68
	v_mov_b32_e32 v103, v68
	v_mov_b32_e32 v108, v68
	v_mov_b32_e32 v109, v68
	v_mov_b32_e32 v110, v68
	v_mov_b32_e32 v111, v68
	v_mov_b32_e32 v116, v68
	v_mov_b32_e32 v117, v68
	v_mov_b32_e32 v118, v68
	v_mov_b32_e32 v119, v68
	v_mov_b32_e32 v124, v68
	v_mov_b32_e32 v125, v68
	v_mov_b32_e32 v126, v68
	v_mov_b32_e32 v127, v68
	v_mov_b32_e32 v132, v68
	v_mov_b32_e32 v133, v68
	v_mov_b32_e32 v134, v68
	v_mov_b32_e32 v135, v68
	v_mov_b32_e32 v140, v68
	v_mov_b32_e32 v141, v68
	v_mov_b32_e32 v142, v68
	v_mov_b32_e32 v143, v68
	v_mov_b32_e32 v148, v68
	v_mov_b32_e32 v149, v68
	v_mov_b32_e32 v150, v68
	v_mov_b32_e32 v151, v68
	v_mov_b32_e32 v156, v68
	v_mov_b32_e32 v157, v68
	v_mov_b32_e32 v158, v68
	v_mov_b32_e32 v159, v68
	v_mov_b32_e32 v96, v68
	v_mov_b32_e32 v97, v68
	v_mov_b32_e32 v98, v68
	v_mov_b32_e32 v99, v68
	v_mov_b32_e32 v104, v68
	v_mov_b32_e32 v105, v68
	v_mov_b32_e32 v106, v68
	v_mov_b32_e32 v107, v68
	v_mov_b32_e32 v112, v68
	v_mov_b32_e32 v113, v68
	v_mov_b32_e32 v114, v68
	v_mov_b32_e32 v115, v68
	v_mov_b32_e32 v120, v68
	v_mov_b32_e32 v121, v68
	v_mov_b32_e32 v122, v68
	v_mov_b32_e32 v123, v68
	v_mov_b32_e32 v128, v68
	v_mov_b32_e32 v129, v68
	v_mov_b32_e32 v130, v68
	v_mov_b32_e32 v131, v68
	v_mov_b32_e32 v136, v68
	v_mov_b32_e32 v137, v68
	v_mov_b32_e32 v138, v68
	v_mov_b32_e32 v139, v68
	v_mov_b32_e32 v144, v68
	v_mov_b32_e32 v145, v68
	v_mov_b32_e32 v146, v68
	v_mov_b32_e32 v147, v68
	v_mov_b32_e32 v152, v68
	v_mov_b32_e32 v153, v68
	v_mov_b32_e32 v154, v68
	v_mov_b32_e32 v155, v68
	v_mov_b32_e32 v60, v68
	v_mov_b32_e32 v61, v68
	v_mov_b32_e32 v62, v68
	v_mov_b32_e32 v63, v68
	v_mov_b32_e32 v52, v68
	v_mov_b32_e32 v53, v68
	v_mov_b32_e32 v54, v68
	v_mov_b32_e32 v55, v68
	v_mov_b32_e32 v40, v68
	v_mov_b32_e32 v41, v68
	v_mov_b32_e32 v42, v68
	v_mov_b32_e32 v43, v68
	v_mov_b32_e32 v44, v68
	v_mov_b32_e32 v45, v68
	v_mov_b32_e32 v46, v68
	v_mov_b32_e32 v47, v68
	s_mov_b64 s[4:5], 0x30080
	.p2align 6

.LBB0_1617:
	v_mov_b32_e32 v35, 0
	s_andn2_b64 vcc, exec, s[42:43]
	v_mov_b32_e32 v34, v35
	v_mov_b32_e32 v33, v35
	v_mov_b32_e32 v32, v35
	v_mov_b32_e32 v39, v35
	v_mov_b32_e32 v38, v35
	v_mov_b32_e32 v37, v35
	v_mov_b32_e32 v36, v35
	v_mov_b32_e32 v51, v35
	v_mov_b32_e32 v50, v35
	v_mov_b32_e32 v49, v35
	v_mov_b32_e32 v48, v35
	v_mov_b32_e32 v55, v35
	v_mov_b32_e32 v54, v35
	v_mov_b32_e32 v53, v35
	v_mov_b32_e32 v52, v35
	v_mov_b32_e32 v7, v35
	v_mov_b32_e32 v6, v35
	v_mov_b32_e32 v17, v35
	v_mov_b32_e32 v16, v35
	v_mov_b32_e32 v23, v35
	v_mov_b32_e32 v22, v35
	v_mov_b32_e32 v31, v35
	v_mov_b32_e32 v30, v35
	v_mov_b32_e32 v5, v35
	v_mov_b32_e32 v4, v35
	v_mov_b32_e32 v13, v35
	v_mov_b32_e32 v12, v35
	v_mov_b32_e32 v21, v35
	v_mov_b32_e32 v20, v35
	v_mov_b32_e32 v29, v35
	v_mov_b32_e32 v28, v35
	v_mov_b32_e32 v3, v35
	v_mov_b32_e32 v2, v35
	v_mov_b32_e32 v11, v35
	v_mov_b32_e32 v10, v35
	v_mov_b32_e32 v19, v35
	v_mov_b32_e32 v18, v35
	v_mov_b32_e32 v27, v35
	v_mov_b32_e32 v26, v35
	v_mov_b32_e32 v1, v35
	v_mov_b32_e32 v0, v35
	v_mov_b32_e32 v9, v35
	v_mov_b32_e32 v8, v35
	v_mov_b32_e32 v15, v35
	v_mov_b32_e32 v14, v35
	v_mov_b32_e32 v25, v35
	v_mov_b32_e32 v24, v35
	v_mov_b32_e32 v143, v35
	v_mov_b32_e32 v142, v35
	v_mov_b32_e32 v141, v35
	v_mov_b32_e32 v140, v35
	v_mov_b32_e32 v135, v35
	v_mov_b32_e32 v134, v35
	v_mov_b32_e32 v133, v35
	v_mov_b32_e32 v132, v35
	v_mov_b32_e32 v127, v35
	v_mov_b32_e32 v126, v35
	v_mov_b32_e32 v125, v35
	v_mov_b32_e32 v124, v35
	v_mov_b32_e32 v119, v35
	v_mov_b32_e32 v118, v35
	v_mov_b32_e32 v117, v35
	v_mov_b32_e32 v116, v35
	v_mov_b32_e32 v111, v35
	v_mov_b32_e32 v110, v35
	v_mov_b32_e32 v109, v35
	v_mov_b32_e32 v108, v35
	v_mov_b32_e32 v107, v35
	v_mov_b32_e32 v106, v35
	v_mov_b32_e32 v105, v35
	v_mov_b32_e32 v104, v35
	v_mov_b32_e32 v103, v35
	v_mov_b32_e32 v102, v35
	v_mov_b32_e32 v101, v35
	v_mov_b32_e32 v100, v35
	v_mov_b32_e32 v99, v35
	v_mov_b32_e32 v98, v35
	v_mov_b32_e32 v97, v35
	v_mov_b32_e32 v96, v35
	v_mov_b32_e32 v95, v35
	v_mov_b32_e32 v94, v35
	v_mov_b32_e32 v93, v35
	v_mov_b32_e32 v92, v35
	v_mov_b32_e32 v91, v35
	v_mov_b32_e32 v90, v35
	v_mov_b32_e32 v89, v35
	v_mov_b32_e32 v88, v35
	v_mov_b32_e32 v79, v35
	v_mov_b32_e32 v78, v35
	v_mov_b32_e32 v77, v35
	v_mov_b32_e32 v76, v35
	v_mov_b32_e32 v75, v35
	v_mov_b32_e32 v74, v35
	v_mov_b32_e32 v73, v35
	v_mov_b32_e32 v72, v35
	v_mov_b32_e32 v63, v35
	v_mov_b32_e32 v62, v35
	v_mov_b32_e32 v61, v35
	v_mov_b32_e32 v60, v35
	v_mov_b32_e32 v59, v35
	v_mov_b32_e32 v58, v35
	v_mov_b32_e32 v57, v35
	v_mov_b32_e32 v56, v35
	v_mov_b32_e32 v47, v35
	v_mov_b32_e32 v46, v35
	v_mov_b32_e32 v45, v35
	v_mov_b32_e32 v44, v35
	v_mov_b32_e32 v43, v35
	v_mov_b32_e32 v42, v35
	v_mov_b32_e32 v41, v35
	v_mov_b32_e32 v40, v35
	v_mov_b32_e32 v87, v35
	v_mov_b32_e32 v86, v35
	v_mov_b32_e32 v85, v35
	v_mov_b32_e32 v84, v35
	v_mov_b32_e32 v83, v35
	v_mov_b32_e32 v82, v35
	v_mov_b32_e32 v81, v35
	v_mov_b32_e32 v80, v35
	v_mov_b32_e32 v71, v35
	v_mov_b32_e32 v70, v35
	v_mov_b32_e32 v69, v35
	v_mov_b32_e32 v68, v35
	v_mov_b32_e32 v67, v35
	v_mov_b32_e32 v66, v35
	v_mov_b32_e32 v65, v35
	v_mov_b32_e32 v64, v35
	s_cbranch_vccnz .LBB0_1621
	s_add_u32 vcc_lo, s2, 0x100
	s_addc_u32 vcc_hi, s3, 0
	s_add_u32 s48, s22, 0x70080
	v_mov_b32_e32 v64, 0
	s_addc_u32 s49, s23, 0
	s_mov_b32 s2, 0
	v_mov_b32_e32 v65, v64
	v_mov_b32_e32 v66, v64
	v_mov_b32_e32 v67, v64
	v_mov_b32_e32 v68, v64
	v_mov_b32_e32 v69, v64
	v_mov_b32_e32 v70, v64
	v_mov_b32_e32 v71, v64
	v_mov_b32_e32 v80, v64
	v_mov_b32_e32 v81, v64
	v_mov_b32_e32 v82, v64
	v_mov_b32_e32 v83, v64
	v_mov_b32_e32 v84, v64
	v_mov_b32_e32 v85, v64
	v_mov_b32_e32 v86, v64
	v_mov_b32_e32 v87, v64
	v_mov_b32_e32 v40, v64
	v_mov_b32_e32 v41, v64
	v_mov_b32_e32 v42, v64
	v_mov_b32_e32 v43, v64
	v_mov_b32_e32 v44, v64
	v_mov_b32_e32 v45, v64
	v_mov_b32_e32 v46, v64
	v_mov_b32_e32 v47, v64
	v_mov_b32_e32 v56, v64
	v_mov_b32_e32 v57, v64
	v_mov_b32_e32 v58, v64
	v_mov_b32_e32 v59, v64
	v_mov_b32_e32 v60, v64
	v_mov_b32_e32 v61, v64
	v_mov_b32_e32 v62, v64
	v_mov_b32_e32 v63, v64
	v_mov_b32_e32 v72, v64
	v_mov_b32_e32 v73, v64
	v_mov_b32_e32 v74, v64
	v_mov_b32_e32 v75, v64
	v_mov_b32_e32 v76, v64
	v_mov_b32_e32 v77, v64
	v_mov_b32_e32 v78, v64
	v_mov_b32_e32 v79, v64
	v_mov_b32_e32 v88, v64
	v_mov_b32_e32 v89, v64
	v_mov_b32_e32 v90, v64
	v_mov_b32_e32 v91, v64
	v_mov_b32_e32 v92, v64
	v_mov_b32_e32 v93, v64
	v_mov_b32_e32 v94, v64
	v_mov_b32_e32 v95, v64
	v_mov_b32_e32 v96, v64
	v_mov_b32_e32 v97, v64
	v_mov_b32_e32 v98, v64
	v_mov_b32_e32 v99, v64
	v_mov_b32_e32 v100, v64
	v_mov_b32_e32 v101, v64
	v_mov_b32_e32 v102, v64
	v_mov_b32_e32 v103, v64
	v_mov_b32_e32 v104, v64
	v_mov_b32_e32 v105, v64
	v_mov_b32_e32 v106, v64
	v_mov_b32_e32 v107, v64
	v_mov_b32_e32 v108, v64
	v_mov_b32_e32 v109, v64
	v_mov_b32_e32 v110, v64
	v_mov_b32_e32 v111, v64
	v_mov_b32_e32 v116, v64
	v_mov_b32_e32 v117, v64
	v_mov_b32_e32 v118, v64
	v_mov_b32_e32 v119, v64
	v_mov_b32_e32 v124, v64
	v_mov_b32_e32 v125, v64
	v_mov_b32_e32 v126, v64
	v_mov_b32_e32 v127, v64
	v_mov_b32_e32 v132, v64
	v_mov_b32_e32 v133, v64
	v_mov_b32_e32 v134, v64
	v_mov_b32_e32 v135, v64
	v_mov_b32_e32 v140, v64
	v_mov_b32_e32 v141, v64
	v_mov_b32_e32 v142, v64
	v_mov_b32_e32 v143, v64
	v_mov_b32_e32 v112, v64
	v_mov_b32_e32 v113, v64
	v_mov_b32_e32 v114, v64
	v_mov_b32_e32 v115, v64
	v_mov_b32_e32 v120, v64
	v_mov_b32_e32 v121, v64
	v_mov_b32_e32 v122, v64
	v_mov_b32_e32 v123, v64
	v_mov_b32_e32 v128, v64
	v_mov_b32_e32 v129, v64
	v_mov_b32_e32 v130, v64
	v_mov_b32_e32 v131, v64
	v_mov_b32_e32 v136, v64
	v_mov_b32_e32 v137, v64
	v_mov_b32_e32 v138, v64
	v_mov_b32_e32 v139, v64
	v_mov_b32_e32 v144, v64
	v_mov_b32_e32 v145, v64
	v_mov_b32_e32 v146, v64
	v_mov_b32_e32 v147, v64
	v_mov_b32_e32 v148, v64
	v_mov_b32_e32 v149, v64
	v_mov_b32_e32 v150, v64
	v_mov_b32_e32 v151, v64
	v_mov_b32_e32 v152, v64
	v_mov_b32_e32 v153, v64
	v_mov_b32_e32 v154, v64
	v_mov_b32_e32 v155, v64
	v_mov_b32_e32 v156, v64
	v_mov_b32_e32 v157, v64
	v_mov_b32_e32 v158, v64
	v_mov_b32_e32 v159, v64
	v_mov_b32_e32 v52, v64
	v_mov_b32_e32 v53, v64
	v_mov_b32_e32 v54, v64
	v_mov_b32_e32 v55, v64
	v_mov_b32_e32 v48, v64
	v_mov_b32_e32 v49, v64
	v_mov_b32_e32 v50, v64
	v_mov_b32_e32 v51, v64
	v_mov_b32_e32 v36, v64
	v_mov_b32_e32 v37, v64
	v_mov_b32_e32 v38, v64
	v_mov_b32_e32 v39, v64
	v_mov_b32_e32 v32, v64
	v_mov_b32_e32 v33, v64
	v_mov_b32_e32 v34, v64
	v_mov_b32_e32 v35, v64
	s_mov_b64 s[4:5], 0x70080
	s_mov_b64 s[12:13], 0xa8000
	s_mov_b64 s[64:65], 0x38080
	s_mov_b64 s[72:73], 0xa8080
	s_mov_b64 s[84:85], 0x70000
	.p2align 6

.LBB0_1703:
	s_ashr_i32 s51, s50, 31
	s_lshl_b64 s[18:19], s[50:51], 18
	s_add_u32 s74, s59, s18
	v_mov_b32_e32 v47, 0
	s_addc_u32 s75, s63, s19
	s_andn2_b64 vcc, exec, s[44:45]
	v_mov_b32_e32 v46, v47
	v_mov_b32_e32 v45, v47
	v_mov_b32_e32 v44, v47
	v_mov_b32_e32 v43, v47
	v_mov_b32_e32 v42, v47
	v_mov_b32_e32 v41, v47
	v_mov_b32_e32 v40, v47
	v_mov_b32_e32 v55, v47
	v_mov_b32_e32 v54, v47
	v_mov_b32_e32 v53, v47
	v_mov_b32_e32 v52, v47
	v_mov_b32_e32 v63, v47
	v_mov_b32_e32 v62, v47
	v_mov_b32_e32 v61, v47
	v_mov_b32_e32 v60, v47
	v_mov_b32_e32 v155, v47
	v_mov_b32_e32 v154, v47
	v_mov_b32_e32 v153, v47
	v_mov_b32_e32 v152, v47
	v_mov_b32_e32 v147, v47
	v_mov_b32_e32 v146, v47
	v_mov_b32_e32 v145, v47
	v_mov_b32_e32 v144, v47
	v_mov_b32_e32 v139, v47
	v_mov_b32_e32 v138, v47
	v_mov_b32_e32 v137, v47
	v_mov_b32_e32 v136, v47
	v_mov_b32_e32 v131, v47
	v_mov_b32_e32 v130, v47
	v_mov_b32_e32 v129, v47
	v_mov_b32_e32 v128, v47
	v_mov_b32_e32 v123, v47
	v_mov_b32_e32 v122, v47
	v_mov_b32_e32 v121, v47
	v_mov_b32_e32 v120, v47
	v_mov_b32_e32 v115, v47
	v_mov_b32_e32 v114, v47
	v_mov_b32_e32 v113, v47
	v_mov_b32_e32 v112, v47
	v_mov_b32_e32 v107, v47
	v_mov_b32_e32 v106, v47
	v_mov_b32_e32 v105, v47
	v_mov_b32_e32 v104, v47
	v_mov_b32_e32 v99, v47
	v_mov_b32_e32 v98, v47
	v_mov_b32_e32 v97, v47
	v_mov_b32_e32 v96, v47
	v_mov_b32_e32 v159, v47
	v_mov_b32_e32 v158, v47
	v_mov_b32_e32 v157, v47
	v_mov_b32_e32 v156, v47
	v_mov_b32_e32 v151, v47
	v_mov_b32_e32 v150, v47
	v_mov_b32_e32 v149, v47
	v_mov_b32_e32 v148, v47
	v_mov_b32_e32 v143, v47
	v_mov_b32_e32 v142, v47
	v_mov_b32_e32 v141, v47
	v_mov_b32_e32 v140, v47
	v_mov_b32_e32 v135, v47
	v_mov_b32_e32 v134, v47
	v_mov_b32_e32 v133, v47
	v_mov_b32_e32 v132, v47
	v_mov_b32_e32 v127, v47
	v_mov_b32_e32 v126, v47
	v_mov_b32_e32 v125, v47
	v_mov_b32_e32 v124, v47
	v_mov_b32_e32 v119, v47
	v_mov_b32_e32 v118, v47
	v_mov_b32_e32 v117, v47
	v_mov_b32_e32 v116, v47
	v_mov_b32_e32 v111, v47
	v_mov_b32_e32 v110, v47
	v_mov_b32_e32 v109, v47
	v_mov_b32_e32 v108, v47
	v_mov_b32_e32 v103, v47
	v_mov_b32_e32 v102, v47
	v_mov_b32_e32 v101, v47
	v_mov_b32_e32 v100, v47
	v_mov_b32_e32 v91, v47
	v_mov_b32_e32 v90, v47
	v_mov_b32_e32 v89, v47
	v_mov_b32_e32 v88, v47
	v_mov_b32_e32 v83, v47
	v_mov_b32_e32 v82, v47
	v_mov_b32_e32 v81, v47
	v_mov_b32_e32 v80, v47
	v_mov_b32_e32 v75, v47
	v_mov_b32_e32 v74, v47
	v_mov_b32_e32 v73, v47
	v_mov_b32_e32 v72, v47
	v_mov_b32_e32 v67, v47
	v_mov_b32_e32 v66, v47
	v_mov_b32_e32 v65, v47
	v_mov_b32_e32 v64, v47
	v_mov_b32_e32 v59, v47
	v_mov_b32_e32 v58, v47
	v_mov_b32_e32 v57, v47
	v_mov_b32_e32 v56, v47
	v_mov_b32_e32 v51, v47
	v_mov_b32_e32 v50, v47
	v_mov_b32_e32 v49, v47
	v_mov_b32_e32 v48, v47
	v_mov_b32_e32 v39, v47
	v_mov_b32_e32 v38, v47
	v_mov_b32_e32 v37, v47
	v_mov_b32_e32 v36, v47
	v_mov_b32_e32 v35, v47
	v_mov_b32_e32 v34, v47
	v_mov_b32_e32 v33, v47
	v_mov_b32_e32 v32, v47
	v_mov_b32_e32 v95, v47
	v_mov_b32_e32 v94, v47
	v_mov_b32_e32 v93, v47
	v_mov_b32_e32 v92, v47
	v_mov_b32_e32 v87, v47
	v_mov_b32_e32 v86, v47
	v_mov_b32_e32 v85, v47
	v_mov_b32_e32 v84, v47
	v_mov_b32_e32 v79, v47
	v_mov_b32_e32 v78, v47
	v_mov_b32_e32 v77, v47
	v_mov_b32_e32 v76, v47
	v_mov_b32_e32 v71, v47
	v_mov_b32_e32 v70, v47
	v_mov_b32_e32 v69, v47
	v_mov_b32_e32 v68, v47
	s_cbranch_vccnz .LBB0_1706
	s_and_b64 s[18:19], s[38:39], exec
	s_cselect_b32 s49, s75, s23
	s_cselect_b32 s51, s74, s22
	s_add_u32 vcc_lo, s2, 0x100
	s_addc_u32 vcc_hi, s3, 0
	s_add_u32 s38, s22, 0x20080
	v_mov_b32_e32 v68, 0
	s_addc_u32 s39, s23, 0
	s_mov_b32 s2, 0
	v_mov_b32_e32 v69, v68
	v_mov_b32_e32 v70, v68
	v_mov_b32_e32 v71, v68
	v_mov_b32_e32 v76, v68
	v_mov_b32_e32 v77, v68
	v_mov_b32_e32 v78, v68
	v_mov_b32_e32 v79, v68
	v_mov_b32_e32 v84, v68
	v_mov_b32_e32 v85, v68
	v_mov_b32_e32 v86, v68
	v_mov_b32_e32 v87, v68
	v_mov_b32_e32 v92, v68
	v_mov_b32_e32 v93, v68
	v_mov_b32_e32 v94, v68
	v_mov_b32_e32 v95, v68
	v_mov_b32_e32 v32, v68
	v_mov_b32_e32 v33, v68
	v_mov_b32_e32 v34, v68
	v_mov_b32_e32 v35, v68
	v_mov_b32_e32 v36, v68
	v_mov_b32_e32 v37, v68
	v_mov_b32_e32 v38, v68
	v_mov_b32_e32 v39, v68
	v_mov_b32_e32 v48, v68
	v_mov_b32_e32 v49, v68
	v_mov_b32_e32 v50, v68
	v_mov_b32_e32 v51, v68
	v_mov_b32_e32 v56, v68
	v_mov_b32_e32 v57, v68
	v_mov_b32_e32 v58, v68
	v_mov_b32_e32 v59, v68
	v_mov_b32_e32 v64, v68
	v_mov_b32_e32 v65, v68
	v_mov_b32_e32 v66, v68
	v_mov_b32_e32 v67, v68
	v_mov_b32_e32 v72, v68
	v_mov_b32_e32 v73, v68
	v_mov_b32_e32 v74, v68
	v_mov_b32_e32 v75, v68
	v_mov_b32_e32 v80, v68
	v_mov_b32_e32 v81, v68
	v_mov_b32_e32 v82, v68
	v_mov_b32_e32 v83, v68
	v_mov_b32_e32 v88, v68
	v_mov_b32_e32 v89, v68
	v_mov_b32_e32 v90, v68
	v_mov_b32_e32 v91, v68
	v_mov_b32_e32 v100, v68
	v_mov_b32_e32 v101, v68
	v_mov_b32_e32 v102, v68
	v_mov_b32_e32 v103, v68
	v_mov_b32_e32 v108, v68
	v_mov_b32_e32 v109, v68
	v_mov_b32_e32 v110, v68
	v_mov_b32_e32 v111, v68
	v_mov_b32_e32 v116, v68
	v_mov_b32_e32 v117, v68
	v_mov_b32_e32 v118, v68
	v_mov_b32_e32 v119, v68
	v_mov_b32_e32 v124, v68
	v_mov_b32_e32 v125, v68
	v_mov_b32_e32 v126, v68
	v_mov_b32_e32 v127, v68
	v_mov_b32_e32 v132, v68
	v_mov_b32_e32 v133, v68
	v_mov_b32_e32 v134, v68
	v_mov_b32_e32 v135, v68
	v_mov_b32_e32 v140, v68
	v_mov_b32_e32 v141, v68
	v_mov_b32_e32 v142, v68
	v_mov_b32_e32 v143, v68
	v_mov_b32_e32 v148, v68
	v_mov_b32_e32 v149, v68
	v_mov_b32_e32 v150, v68
	v_mov_b32_e32 v151, v68
	v_mov_b32_e32 v156, v68
	v_mov_b32_e32 v157, v68
	v_mov_b32_e32 v158, v68
	v_mov_b32_e32 v159, v68
	v_mov_b32_e32 v96, v68
	v_mov_b32_e32 v97, v68
	v_mov_b32_e32 v98, v68
	v_mov_b32_e32 v99, v68
	v_mov_b32_e32 v104, v68
	v_mov_b32_e32 v105, v68
	v_mov_b32_e32 v106, v68
	v_mov_b32_e32 v107, v68
	v_mov_b32_e32 v112, v68
	v_mov_b32_e32 v113, v68
	v_mov_b32_e32 v114, v68
	v_mov_b32_e32 v115, v68
	v_mov_b32_e32 v120, v68
	v_mov_b32_e32 v121, v68
	v_mov_b32_e32 v122, v68
	v_mov_b32_e32 v123, v68
	v_mov_b32_e32 v128, v68
	v_mov_b32_e32 v129, v68
	v_mov_b32_e32 v130, v68
	v_mov_b32_e32 v131, v68
	v_mov_b32_e32 v136, v68
	v_mov_b32_e32 v137, v68
	v_mov_b32_e32 v138, v68
	v_mov_b32_e32 v139, v68
	v_mov_b32_e32 v144, v68
	v_mov_b32_e32 v145, v68
	v_mov_b32_e32 v146, v68
	v_mov_b32_e32 v147, v68
	v_mov_b32_e32 v152, v68
	v_mov_b32_e32 v153, v68
	v_mov_b32_e32 v154, v68
	v_mov_b32_e32 v155, v68
	v_mov_b32_e32 v60, v68
	v_mov_b32_e32 v61, v68
	v_mov_b32_e32 v62, v68
	v_mov_b32_e32 v63, v68
	v_mov_b32_e32 v52, v68
	v_mov_b32_e32 v53, v68
	v_mov_b32_e32 v54, v68
	v_mov_b32_e32 v55, v68
	v_mov_b32_e32 v40, v68
	v_mov_b32_e32 v41, v68
	v_mov_b32_e32 v42, v68
	v_mov_b32_e32 v43, v68
	v_mov_b32_e32 v44, v68
	v_mov_b32_e32 v45, v68
	v_mov_b32_e32 v46, v68
	v_mov_b32_e32 v47, v68
	s_mov_b64 s[4:5], 0x30080
	.p2align 6

.LBB0_1778:
	v_mov_b32_e32 v35, 0
	s_andn2_b64 vcc, exec, s[42:43]
	v_mov_b32_e32 v34, v35
	v_mov_b32_e32 v33, v35
	v_mov_b32_e32 v32, v35
	v_mov_b32_e32 v39, v35
	v_mov_b32_e32 v38, v35
	v_mov_b32_e32 v37, v35
	v_mov_b32_e32 v36, v35
	v_mov_b32_e32 v51, v35
	v_mov_b32_e32 v50, v35
	v_mov_b32_e32 v49, v35
	v_mov_b32_e32 v48, v35
	v_mov_b32_e32 v55, v35
	v_mov_b32_e32 v54, v35
	v_mov_b32_e32 v53, v35
	v_mov_b32_e32 v52, v35
	v_mov_b32_e32 v159, v35
	v_mov_b32_e32 v158, v35
	v_mov_b32_e32 v157, v35
	v_mov_b32_e32 v156, v35
	v_mov_b32_e32 v155, v35
	v_mov_b32_e32 v154, v35
	v_mov_b32_e32 v153, v35
	v_mov_b32_e32 v152, v35
	v_mov_b32_e32 v143, v35
	v_mov_b32_e32 v142, v35
	v_mov_b32_e32 v141, v35
	v_mov_b32_e32 v140, v35
	v_mov_b32_e32 v139, v35
	v_mov_b32_e32 v138, v35
	v_mov_b32_e32 v137, v35
	v_mov_b32_e32 v136, v35
	v_mov_b32_e32 v127, v35
	v_mov_b32_e32 v126, v35
	v_mov_b32_e32 v125, v35
	v_mov_b32_e32 v124, v35
	v_mov_b32_e32 v123, v35
	v_mov_b32_e32 v122, v35
	v_mov_b32_e32 v121, v35
	v_mov_b32_e32 v120, v35
	v_mov_b32_e32 v111, v35
	v_mov_b32_e32 v110, v35
	v_mov_b32_e32 v109, v35
	v_mov_b32_e32 v108, v35
	v_mov_b32_e32 v107, v35
	v_mov_b32_e32 v106, v35
	v_mov_b32_e32 v105, v35
	v_mov_b32_e32 v104, v35
	v_mov_b32_e32 v151, v35
	v_mov_b32_e32 v150, v35
	v_mov_b32_e32 v149, v35
	v_mov_b32_e32 v148, v35
	v_mov_b32_e32 v147, v35
	v_mov_b32_e32 v146, v35
	v_mov_b32_e32 v145, v35
	v_mov_b32_e32 v144, v35
	v_mov_b32_e32 v135, v35
	v_mov_b32_e32 v134, v35
	v_mov_b32_e32 v133, v35
	v_mov_b32_e32 v132, v35
	v_mov_b32_e32 v131, v35
	v_mov_b32_e32 v130, v35
	v_mov_b32_e32 v129, v35
	v_mov_b32_e32 v128, v35
	v_mov_b32_e32 v119, v35
	v_mov_b32_e32 v118, v35
	v_mov_b32_e32 v117, v35
	v_mov_b32_e32 v116, v35
	v_mov_b32_e32 v115, v35
	v_mov_b32_e32 v114, v35
	v_mov_b32_e32 v113, v35
	v_mov_b32_e32 v112, v35
	v_mov_b32_e32 v103, v35
	v_mov_b32_e32 v102, v35
	v_mov_b32_e32 v101, v35
	v_mov_b32_e32 v100, v35
	v_mov_b32_e32 v99, v35
	v_mov_b32_e32 v98, v35
	v_mov_b32_e32 v97, v35
	v_mov_b32_e32 v96, v35
	v_mov_b32_e32 v95, v35
	v_mov_b32_e32 v94, v35
	v_mov_b32_e32 v93, v35
	v_mov_b32_e32 v92, v35
	v_mov_b32_e32 v91, v35
	v_mov_b32_e32 v90, v35
	v_mov_b32_e32 v89, v35
	v_mov_b32_e32 v88, v35
	v_mov_b32_e32 v79, v35
	v_mov_b32_e32 v78, v35
	v_mov_b32_e32 v77, v35
	v_mov_b32_e32 v76, v35
	v_mov_b32_e32 v75, v35
	v_mov_b32_e32 v74, v35
	v_mov_b32_e32 v73, v35
	v_mov_b32_e32 v72, v35
	v_mov_b32_e32 v63, v35
	v_mov_b32_e32 v62, v35
	v_mov_b32_e32 v61, v35
	v_mov_b32_e32 v60, v35
	v_mov_b32_e32 v59, v35
	v_mov_b32_e32 v58, v35
	v_mov_b32_e32 v57, v35
	v_mov_b32_e32 v56, v35
	v_mov_b32_e32 v47, v35
	v_mov_b32_e32 v46, v35
	v_mov_b32_e32 v45, v35
	v_mov_b32_e32 v44, v35
	v_mov_b32_e32 v43, v35
	v_mov_b32_e32 v42, v35
	v_mov_b32_e32 v41, v35
	v_mov_b32_e32 v40, v35
	v_mov_b32_e32 v87, v35
	v_mov_b32_e32 v86, v35
	v_mov_b32_e32 v85, v35
	v_mov_b32_e32 v84, v35
	v_mov_b32_e32 v83, v35
	v_mov_b32_e32 v82, v35
	v_mov_b32_e32 v81, v35
	v_mov_b32_e32 v80, v35
	v_mov_b32_e32 v71, v35
	v_mov_b32_e32 v70, v35
	v_mov_b32_e32 v69, v35
	v_mov_b32_e32 v68, v35
	v_mov_b32_e32 v67, v35
	v_mov_b32_e32 v66, v35
	v_mov_b32_e32 v65, v35
	v_mov_b32_e32 v64, v35
	s_cbranch_vccnz .LBB0_1781
	s_add_u32 s47, s2, 0x100
	s_addc_u32 s96, s3, 0
	s_add_u32 s54, s22, 0x70080
	v_mov_b32_e32 v64, 0
	s_addc_u32 s55, s23, 0
	s_mov_b32 s2, 0
	v_mov_b32_e32 v65, v64
	v_mov_b32_e32 v66, v64
	v_mov_b32_e32 v67, v64
	v_mov_b32_e32 v68, v64
	v_mov_b32_e32 v69, v64
	v_mov_b32_e32 v70, v64
	v_mov_b32_e32 v71, v64
	v_mov_b32_e32 v80, v64
	v_mov_b32_e32 v81, v64
	v_mov_b32_e32 v82, v64
	v_mov_b32_e32 v83, v64
	v_mov_b32_e32 v84, v64
	v_mov_b32_e32 v85, v64
	v_mov_b32_e32 v86, v64
	v_mov_b32_e32 v87, v64
	v_mov_b32_e32 v40, v64
	v_mov_b32_e32 v41, v64
	v_mov_b32_e32 v42, v64
	v_mov_b32_e32 v43, v64
	v_mov_b32_e32 v44, v64
	v_mov_b32_e32 v45, v64
	v_mov_b32_e32 v46, v64
	v_mov_b32_e32 v47, v64
	v_mov_b32_e32 v56, v64
	v_mov_b32_e32 v57, v64
	v_mov_b32_e32 v58, v64
	v_mov_b32_e32 v59, v64
	v_mov_b32_e32 v60, v64
	v_mov_b32_e32 v61, v64
	v_mov_b32_e32 v62, v64
	v_mov_b32_e32 v63, v64
	v_mov_b32_e32 v72, v64
	v_mov_b32_e32 v73, v64
	v_mov_b32_e32 v74, v64
	v_mov_b32_e32 v75, v64
	v_mov_b32_e32 v76, v64
	v_mov_b32_e32 v77, v64
	v_mov_b32_e32 v78, v64
	v_mov_b32_e32 v79, v64
	v_mov_b32_e32 v88, v64
	v_mov_b32_e32 v89, v64
	v_mov_b32_e32 v90, v64
	v_mov_b32_e32 v91, v64
	v_mov_b32_e32 v92, v64
	v_mov_b32_e32 v93, v64
	v_mov_b32_e32 v94, v64
	v_mov_b32_e32 v95, v64
	v_mov_b32_e32 v96, v64
	v_mov_b32_e32 v97, v64
	v_mov_b32_e32 v98, v64
	v_mov_b32_e32 v99, v64
	v_mov_b32_e32 v100, v64
	v_mov_b32_e32 v101, v64
	v_mov_b32_e32 v102, v64
	v_mov_b32_e32 v103, v64
	v_mov_b32_e32 v112, v64
	v_mov_b32_e32 v113, v64
	v_mov_b32_e32 v114, v64
	v_mov_b32_e32 v115, v64
	v_mov_b32_e32 v116, v64
	v_mov_b32_e32 v117, v64
	v_mov_b32_e32 v118, v64
	v_mov_b32_e32 v119, v64
	v_mov_b32_e32 v128, v64
	v_mov_b32_e32 v129, v64
	v_mov_b32_e32 v130, v64
	v_mov_b32_e32 v131, v64
	v_mov_b32_e32 v132, v64
	v_mov_b32_e32 v133, v64
	v_mov_b32_e32 v134, v64
	v_mov_b32_e32 v135, v64
	v_mov_b32_e32 v144, v64
	v_mov_b32_e32 v145, v64
	v_mov_b32_e32 v146, v64
	v_mov_b32_e32 v147, v64
	v_mov_b32_e32 v148, v64
	v_mov_b32_e32 v149, v64
	v_mov_b32_e32 v150, v64
	v_mov_b32_e32 v151, v64
	v_mov_b32_e32 v104, v64
	v_mov_b32_e32 v105, v64
	v_mov_b32_e32 v106, v64
	v_mov_b32_e32 v107, v64
	v_mov_b32_e32 v108, v64
	v_mov_b32_e32 v109, v64
	v_mov_b32_e32 v110, v64
	v_mov_b32_e32 v111, v64
	v_mov_b32_e32 v120, v64
	v_mov_b32_e32 v121, v64
	v_mov_b32_e32 v122, v64
	v_mov_b32_e32 v123, v64
	v_mov_b32_e32 v124, v64
	v_mov_b32_e32 v125, v64
	v_mov_b32_e32 v126, v64
	v_mov_b32_e32 v127, v64
	v_mov_b32_e32 v136, v64
	v_mov_b32_e32 v137, v64
	v_mov_b32_e32 v138, v64
	v_mov_b32_e32 v139, v64
	v_mov_b32_e32 v140, v64
	v_mov_b32_e32 v141, v64
	v_mov_b32_e32 v142, v64
	v_mov_b32_e32 v143, v64
	v_mov_b32_e32 v152, v64
	v_mov_b32_e32 v153, v64
	v_mov_b32_e32 v154, v64
	v_mov_b32_e32 v155, v64
	v_mov_b32_e32 v156, v64
	v_mov_b32_e32 v157, v64
	v_mov_b32_e32 v158, v64
	v_mov_b32_e32 v159, v64
	v_mov_b32_e32 v52, v64
	v_mov_b32_e32 v53, v64
	v_mov_b32_e32 v54, v64
	v_mov_b32_e32 v55, v64
	v_mov_b32_e32 v48, v64
	v_mov_b32_e32 v49, v64
	v_mov_b32_e32 v50, v64
	v_mov_b32_e32 v51, v64
	v_mov_b32_e32 v36, v64
	v_mov_b32_e32 v37, v64
	v_mov_b32_e32 v38, v64
	v_mov_b32_e32 v39, v64
	v_mov_b32_e32 v32, v64
	v_mov_b32_e32 v33, v64
	v_mov_b32_e32 v34, v64
	v_mov_b32_e32 v35, v64
	s_mov_b64 s[4:5], 0x70080
	s_mov_b64 s[12:13], 0xa8000
	s_mov_b64 s[64:65], 0x38080
	s_mov_b64 s[72:73], 0xa8080
	s_mov_b64 s[84:85], 0x70000
	.p2align 6
